# 8-phase K-loops: dropped the blanket lgkmcnt(0) after the pre-MFMA barrier; the per-consumer counted LDS waits guard each fragment (first MFMAs start earlier)
# baseline (speedup 1.0000x reference)
; #define G_BAR() __builtin_amdgcn_s_barrier()
; #define G_SCHED() __builtin_amdgcn_sched_barrier(0)
; #define D_STAGE_A(slot, half, kt) D_STAGE(rsA, voffA, slot, half, kt)
; #define D_STAGE_B(slot, half, kt) D_STAGE(rsB, voffB, slot, half, kt)
; #define D_LDA(dst, slot) do { _Pragma("unroll") for (int m = 0; m < 4; ++m) _Pragma("unroll") for (int k = 0; k < 2; ++k) \
;     dst[m][k] = *(const LDS_AS bf16x8*)(lds + (slot) + aoff + m * 2048 + k * 1024); } while (0)
; #define D_LDB(dst, slot) do { _Pragma("unroll") for (int n = 0; n < 2; ++n) _Pragma("unroll") for (int k = 0; k < 2; ++k) \
;     dst[n][k] = *(const LDS_AS bf16x8*)(lds + (slot) + boff + n * 2048 + k * 1024); } while (0)
; #define D_MMA(ai, bj, At, Bf) do { __builtin_amdgcn_s_setprio(1); _Pragma("unroll") for (int m = 0; m < 4; ++m) _Pragma("unroll") for (int n = 0; n < 2; ++n) _Pragma("unroll") for (int k = 0; k < 2; ++k) \
;     acc[ai][bj][m][n] = __builtin_amdgcn_mfma_f32_16x16x32_bf16(Bf[n][k], At[m][k], acc[ai][bj][m][n], 0, 0, 0); __builtin_amdgcn_s_setprio(0); } while (0)
; #define D_WAIT_L(n) asm volatile("s_waitcnt lgkmcnt(" #n ")" ::: "memory")
; #define D_STAGE_A(slot, half, kt) D_STAGE(rsA, voffA, slot, half, kt)
; #define D_STAGE_B(slot, half, kt) do { _Pragma("unroll") for (int _i = 0; _i < 2; ++_i) { const unsigned _m0 = ldsw + (unsigned)((slot) + _i * 8192); const unsigned _so = (unsigned)(kt) * 128u + (half) * bt_half + _i * bt_piece; \
;     asm volatile("s_mov_b32 m0, %0\n\ts_nop 4\n\tbuffer_load_dwordx4 %1, %2, %3 offen lds" :: "s"(_m0), "v"(voffB0), "s"(rsB), "s"(_so) : "m0", "memory"); } } while (0)
; #define D_WAIT_L(n) asm volatile("s_waitcnt lgkmcnt(" #n ")" ::: "memory")
; template <class Cfg>
; DI void gemm256dma_unit(LDS_AS unsigned char* lds, const Cfg& cfg) {
;     ...
;     D_LDB(B0, G_SB(0, 0)); G_SCHED(); D_LDA(At, G_SA(0, 0)); D_STAGE_A(G_SA(1, 1), 1, t1);
;     D_WAIT_L(8); G_BAR(); D_WAIT_L(0); G_SCHED(); D_MMA(0, 0, At, B0); G_BAR(); G_SCHED();
;     D_LDB(B1, G_SB(0, 1)); D_STAGE_B(G_SB(0, 0), 0, t2);
;     G_BAR(); D_WAIT_L(0); G_SCHED(); D_MMA(0, 1, At, B1); G_BAR(); G_SCHED();
;     D_LDA(At, G_SA(0, 1)); D_STAGE_A(G_SA(0, 0), 0, t2);
;     G_BAR(); D_WAIT_L(0); G_SCHED(); D_MMA(1, 0, At, B0); G_BAR(); G_SCHED();
.LBB0_279:
	ds_read_b128 v[142:145], v139
	ds_read_b128 v[150:153], v139 offset:1024
	ds_read_b128 v[154:157], v139 offset:2048
	ds_read_b128 v[158:161], v139 offset:3072
	s_add_i32 s30, s29, 2
	s_add_i32 s38, s28, 0xffffff00
	s_add_i32 s31, s28, 0xffffff80
	s_cmp_lt_u32 s29, 30
	s_cselect_b32 s96, s31, 0
	s_cselect_b32 s31, s28, 0x80
	s_addk_i32 s28, 0x100
	s_cmp_gt_u32 s29, 29
	ds_read_b128 v[162:165], v138 offset:16
	ds_read_b128 v[166:169], v138 offset:1040
	ds_read_b128 v[170:173], v138 offset:2064
	ds_read_b128 v[174:177], v138 offset:3088
	ds_read_b128 v[178:181], v138 offset:4112
	ds_read_b128 v[182:185], v138 offset:5136
	ds_read_b128 v[186:189], v138 offset:6160
	ds_read_b128 v[192:195], v138 offset:7184
	s_mov_b32 m0, vcc_lo
	s_nop 0
	buffer_load_dwordx4 v135, s[20:23], s38 offen lds
	s_nop 0
	s_mov_b32 m0, vcc_hi
	s_nop 0
	buffer_load_dwordx4 v132, s[20:23], s38 offen lds
	s_waitcnt lgkmcnt(8)
	s_waitcnt vmcnt(10)
	s_barrier
	s_nop 0
	s_setprio 1
	s_waitcnt lgkmcnt(7)
	v_mfma_f32_16x16x32_bf16 v[124:127], v[142:145], v[162:165], v[124:127]
	v_mfma_f32_16x16x32_bf16 v[120:123], v[154:157], v[162:165], v[120:123]
	s_waitcnt lgkmcnt(5)
	v_mfma_f32_16x16x32_bf16 v[108:111], v[142:145], v[170:173], v[108:111]
	v_mfma_f32_16x16x32_bf16 v[104:107], v[154:157], v[170:173], v[104:107]
	s_waitcnt lgkmcnt(3)
	v_mfma_f32_16x16x32_bf16 v[92:95], v[142:145], v[178:181], v[92:95]
	v_mfma_f32_16x16x32_bf16 v[88:91], v[154:157], v[178:181], v[88:91]
	s_waitcnt lgkmcnt(1)
	v_mfma_f32_16x16x32_bf16 v[76:79], v[142:145], v[186:189], v[76:79]
	v_mfma_f32_16x16x32_bf16 v[72:75], v[154:157], v[186:189], v[72:75]
	v_mfma_f32_16x16x32_bf16 v[124:127], v[150:153], v[166:169], v[124:127]
	v_mfma_f32_16x16x32_bf16 v[120:123], v[158:161], v[166:169], v[120:123]
	v_mfma_f32_16x16x32_bf16 v[108:111], v[150:153], v[174:177], v[108:111]
	v_mfma_f32_16x16x32_bf16 v[104:107], v[158:161], v[174:177], v[104:107]
	v_mfma_f32_16x16x32_bf16 v[92:95], v[150:153], v[182:185], v[92:95]
	v_mfma_f32_16x16x32_bf16 v[88:91], v[158:161], v[182:185], v[88:91]
	s_waitcnt lgkmcnt(0)
	v_mfma_f32_16x16x32_bf16 v[76:79], v[150:153], v[192:195], v[76:79]
	v_mfma_f32_16x16x32_bf16 v[72:75], v[158:161], v[192:195], v[72:75]
	s_setprio 0
	s_barrier
	ds_read_b128 v[196:199], v140
	ds_read_b128 v[200:203], v140 offset:1024
	ds_read_b128 v[204:207], v140 offset:2048
	ds_read_b128 v[208:211], v140 offset:3072
	s_mov_b32 m0, s33
	s_nop 0
	buffer_load_dwordx4 v133, s[8:11], s96 offen lds
	s_nop 0
	s_mov_b32 m0, s39
	s_nop 0
	buffer_load_dwordx4 v128, s[8:11], s96 offen lds
	s_waitcnt vmcnt(10)
	s_barrier
	s_nop 0
	s_setprio 1
	s_waitcnt lgkmcnt(3)
	v_mfma_f32_16x16x32_bf16 v[116:119], v[196:199], v[162:165], v[116:119]
	s_waitcnt lgkmcnt(1)
	v_mfma_f32_16x16x32_bf16 v[112:115], v[204:207], v[162:165], v[112:115]
	v_mfma_f32_16x16x32_bf16 v[100:103], v[196:199], v[170:173], v[100:103]
	v_mfma_f32_16x16x32_bf16 v[96:99], v[204:207], v[170:173], v[96:99]
	v_mfma_f32_16x16x32_bf16 v[84:87], v[196:199], v[178:181], v[84:87]
	v_mfma_f32_16x16x32_bf16 v[80:83], v[204:207], v[178:181], v[80:83]
	v_mfma_f32_16x16x32_bf16 v[68:71], v[196:199], v[186:189], v[68:71]
	v_mfma_f32_16x16x32_bf16 v[64:67], v[204:207], v[186:189], v[64:67]
	v_mfma_f32_16x16x32_bf16 v[116:119], v[200:203], v[166:169], v[116:119]
	s_waitcnt lgkmcnt(0)
	v_mfma_f32_16x16x32_bf16 v[112:115], v[208:211], v[166:169], v[112:115]
	v_mfma_f32_16x16x32_bf16 v[100:103], v[200:203], v[174:177], v[100:103]
	v_mfma_f32_16x16x32_bf16 v[96:99], v[208:211], v[174:177], v[96:99]
	v_mfma_f32_16x16x32_bf16 v[84:87], v[200:203], v[182:185], v[84:87]
	v_mfma_f32_16x16x32_bf16 v[80:83], v[208:211], v[182:185], v[80:83]
	v_mfma_f32_16x16x32_bf16 v[68:71], v[200:203], v[192:195], v[68:71]
	v_mfma_f32_16x16x32_bf16 v[64:67], v[208:211], v[192:195], v[64:67]
	s_setprio 0
	s_barrier
	ds_read_b128 v[162:165], v138 offset:16400
	ds_read_b128 v[166:169], v138 offset:17424
	ds_read_b128 v[170:173], v138 offset:18448
	ds_read_b128 v[174:177], v138 offset:19472
	ds_read_b128 v[178:181], v138 offset:20496
	ds_read_b128 v[182:185], v138 offset:21520
	ds_read_b128 v[186:189], v138 offset:22544
	ds_read_b128 v[192:195], v138 offset:23568
	s_mov_b32 m0, s1
	s_nop 0
	buffer_load_dwordx4 v134, s[20:23], s96 offen lds
	s_nop 0
	s_mov_b32 m0, s42
	s_nop 0
	buffer_load_dwordx4 v131, s[20:23], s96 offen lds
	s_barrier
	s_nop 0
	s_setprio 1
	s_waitcnt lgkmcnt(7)
	v_mfma_f32_16x16x32_bf16 v[60:63], v[142:145], v[162:165], v[60:63]
	v_mfma_f32_16x16x32_bf16 v[56:59], v[154:157], v[162:165], v[56:59]
	s_waitcnt lgkmcnt(5)
	v_mfma_f32_16x16x32_bf16 v[44:47], v[142:145], v[170:173], v[44:47]
	v_mfma_f32_16x16x32_bf16 v[40:43], v[154:157], v[170:173], v[40:43]
	s_waitcnt lgkmcnt(3)
	v_mfma_f32_16x16x32_bf16 v[28:31], v[142:145], v[178:181], v[28:31]
	v_mfma_f32_16x16x32_bf16 v[24:27], v[154:157], v[178:181], v[24:27]
	s_waitcnt lgkmcnt(1)
	v_mfma_f32_16x16x32_bf16 v[12:15], v[142:145], v[186:189], v[12:15]
	v_mfma_f32_16x16x32_bf16 v[8:11], v[154:157], v[186:189], v[8:11]
	v_mfma_f32_16x16x32_bf16 v[60:63], v[150:153], v[166:169], v[60:63]
	v_mfma_f32_16x16x32_bf16 v[56:59], v[158:161], v[166:169], v[56:59]
	v_mfma_f32_16x16x32_bf16 v[44:47], v[150:153], v[174:177], v[44:47]
	v_mfma_f32_16x16x32_bf16 v[40:43], v[158:161], v[174:177], v[40:43]
	v_mfma_f32_16x16x32_bf16 v[28:31], v[150:153], v[182:185], v[28:31]
	v_mfma_f32_16x16x32_bf16 v[24:27], v[158:161], v[182:185], v[24:27]
	s_waitcnt lgkmcnt(0)
	v_mfma_f32_16x16x32_bf16 v[12:15], v[150:153], v[192:195], v[12:15]
	v_mfma_f32_16x16x32_bf16 v[8:11], v[158:161], v[192:195], v[8:11]
	s_setprio 0
	s_barrier
; #define G_WAIT_V(n) asm volatile("s_waitcnt vmcnt(" #n ")" ::: "memory")
; #define G_BAR() __builtin_amdgcn_s_barrier()
; #define G_SCHED() __builtin_amdgcn_sched_barrier(0)
; #define D_STAGE_A(slot, half, kt) D_STAGE(rsA, voffA, slot, half, kt)
; #define D_STAGE_B(slot, half, kt) D_STAGE(rsB, voffB, slot, half, kt)
; #define D_LDA(dst, slot) do { _Pragma("unroll") for (int m = 0; m < 4; ++m) _Pragma("unroll") for (int k = 0; k < 2; ++k) \
;     dst[m][k] = *(const LDS_AS bf16x8*)(lds + (slot) + aoff + m * 2048 + k * 1024); } while (0)
; #define D_LDB(dst, slot) do { _Pragma("unroll") for (int n = 0; n < 2; ++n) _Pragma("unroll") for (int k = 0; k < 2; ++k) \
;     dst[n][k] = *(const LDS_AS bf16x8*)(lds + (slot) + boff + n * 2048 + k * 1024); } while (0)
; #define D_MMA(ai, bj, At, Bf) do { __builtin_amdgcn_s_setprio(1); _Pragma("unroll") for (int m = 0; m < 4; ++m) _Pragma("unroll") for (int n = 0; n < 2; ++n) _Pragma("unroll") for (int k = 0; k < 2; ++k) \
;     acc[ai][bj][m][n] = __builtin_amdgcn_mfma_f32_16x16x32_bf16(Bf[n][k], At[m][k], acc[ai][bj][m][n], 0, 0, 0); __builtin_amdgcn_s_setprio(0); } while (0)
; #define D_WAIT_L(n) asm volatile("s_waitcnt lgkmcnt(" #n ")" ::: "memory")
; #define D_STAGE_A(slot, half, kt) D_STAGE(rsA, voffA, slot, half, kt)
; #define D_STAGE_B(slot, half, kt) do { _Pragma("unroll") for (int _i = 0; _i < 2; ++_i) { const unsigned _m0 = ldsw + (unsigned)((slot) + _i * 8192); const unsigned _so = (unsigned)(kt) * 128u + (half) * bt_half + _i * bt_piece; \
;     asm volatile("s_mov_b32 m0, %0\n\ts_nop 4\n\tbuffer_load_dwordx4 %1, %2, %3 offen lds" :: "s"(_m0), "v"(voffB0), "s"(rsB), "s"(_so) : "m0", "memory"); } } while (0)
; #define D_WAIT_L(n) asm volatile("s_waitcnt lgkmcnt(" #n ")" ::: "memory")
; template <class Cfg>
; DI void gemm256dma_unit(LDS_AS unsigned char* lds, const Cfg& cfg) {
;     ...
;     D_STAGE_B(G_SB(0, 1), 1, t2);
;     G_WAIT_V(6); G_BAR(); G_SCHED(); D_MMA(1, 1, At, B1); G_BAR(); G_SCHED();
;     D_LDB(B0, G_SB(1, 0)); G_SCHED(); D_LDA(At, G_SA(1, 0)); D_STAGE_A(G_SA(0, 1), 1, t2);
;     D_WAIT_L(8); G_BAR(); D_WAIT_L(0); G_SCHED(); D_MMA(0, 0, At, B0); G_BAR(); G_SCHED();
;     D_LDB(B1, G_SB(1, 1)); D_STAGE_B(G_SB(1, 0), 0, t3);
	s_mov_b32 m0, s43
	s_nop 0
	buffer_load_dwordx4 v130, s[8:11], s96 offen lds
	s_nop 0
	s_mov_b32 m0, s54
	s_nop 0
	buffer_load_dwordx4 v136, s[8:11], s96 offen lds
	s_waitcnt vmcnt(10)
	s_barrier
	s_setprio 1
	v_mfma_f32_16x16x32_bf16 v[52:55], v[196:199], v[162:165], v[52:55]
	v_mfma_f32_16x16x32_bf16 v[48:51], v[204:207], v[162:165], v[48:51]
	v_mfma_f32_16x16x32_bf16 v[36:39], v[196:199], v[170:173], v[36:39]
	v_mfma_f32_16x16x32_bf16 v[32:35], v[204:207], v[170:173], v[32:35]
	v_mfma_f32_16x16x32_bf16 v[20:23], v[196:199], v[178:181], v[20:23]
	v_mfma_f32_16x16x32_bf16 v[16:19], v[204:207], v[178:181], v[16:19]
	v_mfma_f32_16x16x32_bf16 v[4:7], v[196:199], v[186:189], v[4:7]
	v_mfma_f32_16x16x32_bf16 v[0:3], v[204:207], v[186:189], v[0:3]
	v_mfma_f32_16x16x32_bf16 v[52:55], v[200:203], v[166:169], v[52:55]
	v_mfma_f32_16x16x32_bf16 v[48:51], v[208:211], v[166:169], v[48:51]
	v_mfma_f32_16x16x32_bf16 v[36:39], v[200:203], v[174:177], v[36:39]
	v_mfma_f32_16x16x32_bf16 v[32:35], v[208:211], v[174:177], v[32:35]
	v_mfma_f32_16x16x32_bf16 v[20:23], v[200:203], v[182:185], v[20:23]
	v_mfma_f32_16x16x32_bf16 v[16:19], v[208:211], v[182:185], v[16:19]
	v_mfma_f32_16x16x32_bf16 v[4:7], v[200:203], v[192:195], v[4:7]
	v_mfma_f32_16x16x32_bf16 v[0:3], v[208:211], v[192:195], v[0:3]
	s_setprio 0
	s_barrier
	v_add_u32_e32 v141, 0x18010, v137
	ds_read_b128 v[142:145], v141
	ds_read_b128 v[150:153], v141 offset:1024
	ds_read_b128 v[154:157], v141 offset:2048
	ds_read_b128 v[158:161], v141 offset:3072
	ds_read_b128 v[162:165], v138 offset:32784
	ds_read_b128 v[166:169], v138 offset:33808
	ds_read_b128 v[170:173], v138 offset:34832
	ds_read_b128 v[174:177], v138 offset:35856
	ds_read_b128 v[178:181], v138 offset:36880
	ds_read_b128 v[182:185], v138 offset:37904
	ds_read_b128 v[186:189], v138 offset:38928
	ds_read_b128 v[192:195], v138 offset:39952
	s_mov_b32 m0, s60
	s_nop 0
	buffer_load_dwordx4 v135, s[20:23], s96 offen lds
	s_nop 0
	s_mov_b32 m0, s61
	s_nop 0
	buffer_load_dwordx4 v132, s[20:23], s96 offen lds
	s_waitcnt lgkmcnt(8)
	s_waitcnt vmcnt(10)
	s_barrier
	s_nop 0
	s_setprio 1
	s_waitcnt lgkmcnt(7)
	v_mfma_f32_16x16x32_bf16 v[124:127], v[142:145], v[162:165], v[124:127]
	v_mfma_f32_16x16x32_bf16 v[120:123], v[154:157], v[162:165], v[120:123]
	s_waitcnt lgkmcnt(5)
	v_mfma_f32_16x16x32_bf16 v[108:111], v[142:145], v[170:173], v[108:111]
	v_mfma_f32_16x16x32_bf16 v[104:107], v[154:157], v[170:173], v[104:107]
	s_waitcnt lgkmcnt(3)
	v_mfma_f32_16x16x32_bf16 v[92:95], v[142:145], v[178:181], v[92:95]
	v_mfma_f32_16x16x32_bf16 v[88:91], v[154:157], v[178:181], v[88:91]
	s_waitcnt lgkmcnt(1)
	v_mfma_f32_16x16x32_bf16 v[76:79], v[142:145], v[186:189], v[76:79]
	v_mfma_f32_16x16x32_bf16 v[72:75], v[154:157], v[186:189], v[72:75]
	v_mfma_f32_16x16x32_bf16 v[124:127], v[150:153], v[166:169], v[124:127]
	v_mfma_f32_16x16x32_bf16 v[120:123], v[158:161], v[166:169], v[120:123]
	v_mfma_f32_16x16x32_bf16 v[108:111], v[150:153], v[174:177], v[108:111]
	v_mfma_f32_16x16x32_bf16 v[104:107], v[158:161], v[174:177], v[104:107]
	v_mfma_f32_16x16x32_bf16 v[92:95], v[150:153], v[182:185], v[92:95]
	v_mfma_f32_16x16x32_bf16 v[88:91], v[158:161], v[182:185], v[88:91]
	s_waitcnt lgkmcnt(0)
	v_mfma_f32_16x16x32_bf16 v[76:79], v[150:153], v[192:195], v[76:79]
	v_mfma_f32_16x16x32_bf16 v[72:75], v[158:161], v[192:195], v[72:75]
	s_setprio 0
	s_barrier
	v_add_u32_e32 v141, 0x1c010, v137
	ds_read_b128 v[196:199], v141
	ds_read_b128 v[200:203], v141 offset:1024
	ds_read_b128 v[204:207], v141 offset:2048
	ds_read_b128 v[208:211], v141 offset:3072
	s_mov_b32 m0, s62
	s_nop 0
	buffer_load_dwordx4 v133, s[8:11], s31 offen lds
	s_nop 0
	s_mov_b32 m0, s63
	s_nop 0
	buffer_load_dwordx4 v128, s[8:11], s31 offen lds
	s_waitcnt vmcnt(10)
	s_barrier
; #define G_WAIT_V(n) asm volatile("s_waitcnt vmcnt(" #n ")" ::: "memory")
; #define G_BAR() __builtin_amdgcn_s_barrier()
; #define G_SCHED() __builtin_amdgcn_sched_barrier(0)
; #define D_STAGE_A(slot, half, kt) D_STAGE(rsA, voffA, slot, half, kt)
; #define D_STAGE_B(slot, half, kt) D_STAGE(rsB, voffB, slot, half, kt)
; #define D_LDA(dst, slot) do { _Pragma("unroll") for (int m = 0; m < 4; ++m) _Pragma("unroll") for (int k = 0; k < 2; ++k) \
;     dst[m][k] = *(const LDS_AS bf16x8*)(lds + (slot) + aoff + m * 2048 + k * 1024); } while (0)
; #define D_MMA(ai, bj, At, Bf) do { __builtin_amdgcn_s_setprio(1); _Pragma("unroll") for (int m = 0; m < 4; ++m) _Pragma("unroll") for (int n = 0; n < 2; ++n) _Pragma("unroll") for (int k = 0; k < 2; ++k) \
;     acc[ai][bj][m][n] = __builtin_amdgcn_mfma_f32_16x16x32_bf16(Bf[n][k], At[m][k], acc[ai][bj][m][n], 0, 0, 0); __builtin_amdgcn_s_setprio(0); } while (0)
; #define D_WAIT_L(n) asm volatile("s_waitcnt lgkmcnt(" #n ")" ::: "memory")
; #define D_STAGE_A(slot, half, kt) D_STAGE(rsA, voffA, slot, half, kt)
; #define D_STAGE_B(slot, half, kt) do { _Pragma("unroll") for (int _i = 0; _i < 2; ++_i) { const unsigned _m0 = ldsw + (unsigned)((slot) + _i * 8192); const unsigned _so = (unsigned)(kt) * 128u + (half) * bt_half + _i * bt_piece; \
;     asm volatile("s_mov_b32 m0, %0\n\ts_nop 4\n\tbuffer_load_dwordx4 %1, %2, %3 offen lds" :: "s"(_m0), "v"(voffB0), "s"(rsB), "s"(_so) : "m0", "memory"); } } while (0)
; #define D_LDA(dst, slot) do { _Pragma("unroll") for (int m = 0; m < 4; ++m) { \
;     const i32x4 _lo = *(const LDS_AS i32x4*)(lds + (slot) + aoff[0] + m * 2048); const i32x4 _hi = *(const LDS_AS i32x4*)(lds + (slot) + aoff[1] + m * 2048); \
;     dst[m] = __builtin_shufflevector(_lo, _hi, 0, 1, 2, 3, 4, 5, 6, 7); } } while (0)
; #define D_WAIT_L(n) asm volatile("s_waitcnt lgkmcnt(" #n ")" ::: "memory")
; template <class Cfg>
; DI void gemm256dma_unit(LDS_AS unsigned char* lds, const Cfg& cfg) {
;     ...
;     G_BAR(); D_WAIT_L(0); G_SCHED(); D_MMA(0, 1, At, B1); G_BAR(); G_SCHED();
;     D_LDA(At, G_SA(1, 1)); D_STAGE_A(G_SA(1, 0), 0, t3);
;     G_BAR(); D_WAIT_L(0); G_SCHED(); D_MMA(1, 0, At, B0); G_BAR(); G_SCHED();
;     D_STAGE_B(G_SB(1, 1), 1, t3);
;     G_WAIT_V(6); G_BAR(); G_SCHED(); D_MMA(1, 1, At, B1); G_BAR(); G_SCHED();
;   }
;   G_WAIT_V(0);
;   if (wr == 0) G_BAR();
	s_nop 0
	s_setprio 1
	s_waitcnt lgkmcnt(3)
	v_mfma_f32_16x16x32_bf16 v[116:119], v[196:199], v[162:165], v[116:119]
	s_waitcnt lgkmcnt(1)
	v_mfma_f32_16x16x32_bf16 v[112:115], v[204:207], v[162:165], v[112:115]
	v_mfma_f32_16x16x32_bf16 v[100:103], v[196:199], v[170:173], v[100:103]
	v_mfma_f32_16x16x32_bf16 v[96:99], v[204:207], v[170:173], v[96:99]
	v_mfma_f32_16x16x32_bf16 v[84:87], v[196:199], v[178:181], v[84:87]
	v_mfma_f32_16x16x32_bf16 v[80:83], v[204:207], v[178:181], v[80:83]
	v_mfma_f32_16x16x32_bf16 v[68:71], v[196:199], v[186:189], v[68:71]
	v_mfma_f32_16x16x32_bf16 v[64:67], v[204:207], v[186:189], v[64:67]
	v_mfma_f32_16x16x32_bf16 v[116:119], v[200:203], v[166:169], v[116:119]
	s_waitcnt lgkmcnt(0)
	v_mfma_f32_16x16x32_bf16 v[112:115], v[208:211], v[166:169], v[112:115]
	v_mfma_f32_16x16x32_bf16 v[100:103], v[200:203], v[174:177], v[100:103]
	v_mfma_f32_16x16x32_bf16 v[96:99], v[208:211], v[174:177], v[96:99]
	v_mfma_f32_16x16x32_bf16 v[84:87], v[200:203], v[182:185], v[84:87]
	v_mfma_f32_16x16x32_bf16 v[80:83], v[208:211], v[182:185], v[80:83]
	v_mfma_f32_16x16x32_bf16 v[68:71], v[200:203], v[192:195], v[68:71]
	v_mfma_f32_16x16x32_bf16 v[64:67], v[208:211], v[192:195], v[64:67]
	s_setprio 0
	s_barrier
	ds_read_b128 v[162:165], v138 offset:49168
	ds_read_b128 v[166:169], v138 offset:50192
	ds_read_b128 v[170:173], v138 offset:51216
	ds_read_b128 v[174:177], v138 offset:52240
	ds_read_b128 v[178:181], v138 offset:53264
	ds_read_b128 v[182:185], v138 offset:54288
	ds_read_b128 v[186:189], v138 offset:55312
	ds_read_b128 v[192:195], v138 offset:56336
	s_mov_b32 m0, s64
	s_nop 0
	buffer_load_dwordx4 v134, s[20:23], s31 offen lds
	s_nop 0
	s_mov_b32 m0, s65
	s_nop 0
	buffer_load_dwordx4 v131, s[20:23], s31 offen lds
	s_barrier
	s_nop 0
	s_setprio 1
	s_waitcnt lgkmcnt(7)
	v_mfma_f32_16x16x32_bf16 v[60:63], v[142:145], v[162:165], v[60:63]
	v_mfma_f32_16x16x32_bf16 v[56:59], v[154:157], v[162:165], v[56:59]
	s_waitcnt lgkmcnt(5)
	v_mfma_f32_16x16x32_bf16 v[44:47], v[142:145], v[170:173], v[44:47]
	v_mfma_f32_16x16x32_bf16 v[40:43], v[154:157], v[170:173], v[40:43]
	s_waitcnt lgkmcnt(3)
	v_mfma_f32_16x16x32_bf16 v[28:31], v[142:145], v[178:181], v[28:31]
	v_mfma_f32_16x16x32_bf16 v[24:27], v[154:157], v[178:181], v[24:27]
	s_waitcnt lgkmcnt(1)
	v_mfma_f32_16x16x32_bf16 v[12:15], v[142:145], v[186:189], v[12:15]
	v_mfma_f32_16x16x32_bf16 v[8:11], v[154:157], v[186:189], v[8:11]
	v_mfma_f32_16x16x32_bf16 v[60:63], v[150:153], v[166:169], v[60:63]
	v_mfma_f32_16x16x32_bf16 v[56:59], v[158:161], v[166:169], v[56:59]
	v_mfma_f32_16x16x32_bf16 v[44:47], v[150:153], v[174:177], v[44:47]
	v_mfma_f32_16x16x32_bf16 v[40:43], v[158:161], v[174:177], v[40:43]
	v_mfma_f32_16x16x32_bf16 v[28:31], v[150:153], v[182:185], v[28:31]
	v_mfma_f32_16x16x32_bf16 v[24:27], v[158:161], v[182:185], v[24:27]
	s_waitcnt lgkmcnt(0)
	v_mfma_f32_16x16x32_bf16 v[12:15], v[150:153], v[192:195], v[12:15]
	v_mfma_f32_16x16x32_bf16 v[8:11], v[158:161], v[192:195], v[8:11]
	s_setprio 0
	s_barrier
	s_mov_b32 m0, s66
	s_nop 0
	buffer_load_dwordx4 v130, s[8:11], s31 offen lds
	s_nop 0
	s_mov_b32 m0, s67
	s_nop 0
	buffer_load_dwordx4 v136, s[8:11], s31 offen lds
	s_waitcnt vmcnt(10)
	s_barrier
	s_setprio 1
	v_mfma_f32_16x16x32_bf16 v[52:55], v[196:199], v[162:165], v[52:55]
	v_mfma_f32_16x16x32_bf16 v[48:51], v[204:207], v[162:165], v[48:51]
	v_mfma_f32_16x16x32_bf16 v[36:39], v[196:199], v[170:173], v[36:39]
	v_mfma_f32_16x16x32_bf16 v[32:35], v[204:207], v[170:173], v[32:35]
	v_mfma_f32_16x16x32_bf16 v[20:23], v[196:199], v[178:181], v[20:23]
	v_mfma_f32_16x16x32_bf16 v[16:19], v[204:207], v[178:181], v[16:19]
	v_mfma_f32_16x16x32_bf16 v[4:7], v[196:199], v[186:189], v[4:7]
	v_mfma_f32_16x16x32_bf16 v[0:3], v[204:207], v[186:189], v[0:3]
	v_mfma_f32_16x16x32_bf16 v[52:55], v[200:203], v[166:169], v[52:55]
	v_mfma_f32_16x16x32_bf16 v[48:51], v[208:211], v[166:169], v[48:51]
	v_mfma_f32_16x16x32_bf16 v[36:39], v[200:203], v[174:177], v[36:39]
	v_mfma_f32_16x16x32_bf16 v[32:35], v[208:211], v[174:177], v[32:35]
	v_mfma_f32_16x16x32_bf16 v[20:23], v[200:203], v[182:185], v[20:23]
	v_mfma_f32_16x16x32_bf16 v[16:19], v[208:211], v[182:185], v[16:19]
	v_mfma_f32_16x16x32_bf16 v[4:7], v[200:203], v[192:195], v[4:7]
	v_mfma_f32_16x16x32_bf16 v[0:3], v[208:211], v[192:195], v[0:3]
	s_setprio 0
	s_barrier
	s_mov_b32 s29, s30
	s_cbranch_scc0 .LBB0_279
	s_waitcnt vmcnt(0)
	s_cmpk_lt_u32 s24, 0x100
	s_cbranch_scc0 .LBB0_282
	s_barrier

; #define G_WAIT_V(n) asm volatile("s_waitcnt vmcnt(" #n ")" ::: "memory")
; #define G_BAR() __builtin_amdgcn_s_barrier()
; #define G_SCHED() __builtin_amdgcn_sched_barrier(0)
; #define D_STAGE_A(slot, half, kt) D_STAGE(rsA, voffA, slot, half, kt)
; #define D_STAGE_B(slot, half, kt) D_STAGE(rsB, voffB, slot, half, kt)
; #define D_LDA(dst, slot) do { _Pragma("unroll") for (int m = 0; m < 4; ++m) _Pragma("unroll") for (int k = 0; k < 2; ++k) \
;     dst[m][k] = *(const LDS_AS bf16x8*)(lds + (slot) + aoff + m * 2048 + k * 1024); } while (0)
; #define D_LDB(dst, slot) do { _Pragma("unroll") for (int n = 0; n < 2; ++n) _Pragma("unroll") for (int k = 0; k < 2; ++k) \
;     dst[n][k] = *(const LDS_AS bf16x8*)(lds + (slot) + boff + n * 2048 + k * 1024); } while (0)
; #define D_WAIT_L(n) asm volatile("s_waitcnt lgkmcnt(" #n ")" ::: "memory")
; #define D_STAGE_A(slot, half, kt) D_STAGE(rsA, voffA, slot, half, kt)
; template <class Cfg>
; DI void gemm256dma_unit(LDS_AS unsigned char* lds, const Cfg& cfg) {
;     ...
;   for (int t = 0; t < nt; t += 2) {
;     const int t1 = t + 1;
;     const int t2 = (t + 2 < nt) ? t + 2 : 0;
;     const int t3 = (t + 2 < nt) ? t + 3 : 1;
;     D_LDB(B0, G_SB(0, 0)); G_SCHED(); D_LDA(At, G_SA(0, 0)); D_STAGE_A(G_SA(1, 1), 1, t1);
;     D_WAIT_L(8); G_BAR(); D_WAIT_L(0); G_SCHED(); D_MMA(0, 0, At, B0); G_BAR(); G_SCHED();
;     D_LDB(B1, G_SB(0, 1)); D_STAGE_B(G_SB(0, 0), 0, t2);
;     G_BAR(); D_WAIT_L(0); G_SCHED(); D_MMA(0, 1, At, B1); G_BAR(); G_SCHED();
;     D_LDA(At, G_SA(0, 1)); D_STAGE_A(G_SA(0, 0), 0, t2);
;     G_BAR(); D_WAIT_L(0); G_SCHED(); D_MMA(1, 0, At, B0); G_BAR(); G_SCHED();
;     D_STAGE_B(G_SB(0, 1), 1, t2);
;     G_WAIT_V(6); G_BAR(); G_SCHED(); D_MMA(1, 1, At, B1); G_BAR(); G_SCHED();
;     D_LDB(B0, G_SB(1, 0)); G_SCHED(); D_LDA(At, G_SA(1, 0)); D_STAGE_A(G_SA(0, 1), 1, t2);
;     D_WAIT_L(8); G_BAR(); D_WAIT_L(0); G_SCHED(); D_MMA(0, 0, At, B0); G_BAR(); G_SCHED();
;     D_LDB(B1, G_SB(1, 1)); D_STAGE_B(G_SB(1, 0), 0, t3);
;     G_BAR(); D_WAIT_L(0); G_SCHED(); D_MMA(0, 1, At, B1); G_BAR(); G_SCHED();
;     D_LDA(At, G_SA(1, 1)); D_STAGE_A(G_SA(1, 0), 0, t3);
;     G_BAR(); D_WAIT_L(0); G_SCHED(); D_MMA(1, 0, At, B0); G_BAR(); G_SCHED();
;     D_STAGE_B(G_SB(1, 1), 1, t3);
;     G_WAIT_V(6); G_BAR(); G_SCHED(); D_MMA(1, 1, At, B1); G_BAR(); G_SCHED();
;   }
.LBB0_830:
	v_add_u32_e32 v139, 0x10010, v136
	ds_read_b128 v[140:143], v139
	ds_read_b128 v[144:147], v139 offset:1024
	ds_read_b128 v[148:151], v139 offset:2048
	ds_read_b128 v[152:155], v139 offset:3072
	s_add_i32 s54, s47, 2
	s_add_i32 s38, s46, 0xffffff00
	s_add_i32 s55, s46, 0xffffff80
	s_cmp_lt_u32 s47, 6
	s_cselect_b32 s60, s55, 0
	s_cselect_b32 s55, s46, 0x80
	s_addk_i32 s46, 0x100
	s_cmp_gt_u32 s47, 5
	ds_read_b128 v[156:159], v137 offset:16
	ds_read_b128 v[160:163], v137 offset:1040
	ds_read_b128 v[164:167], v137 offset:2064
	ds_read_b128 v[168:171], v137 offset:3088
	ds_read_b128 v[172:175], v137 offset:4112
	ds_read_b128 v[176:179], v137 offset:5136
	ds_read_b128 v[180:183], v137 offset:6160
	ds_read_b128 v[184:187], v137 offset:7184
	s_mov_b32 m0, s42
	s_nop 0
	buffer_load_dwordx4 v134, s[12:15], s38 offen lds
	s_nop 0
	s_mov_b32 m0, s43
	s_nop 0
	buffer_load_dwordx4 v131, s[12:15], s38 offen lds
	s_waitcnt lgkmcnt(8)
	s_waitcnt vmcnt(10)
	s_barrier
	s_nop 0
	s_setprio 1
	s_waitcnt lgkmcnt(7)
	v_mfma_f32_16x16x32_bf16 v[124:127], v[140:143], v[156:159], v[124:127]
	v_mfma_f32_16x16x32_bf16 v[120:123], v[148:151], v[156:159], v[120:123]
	s_waitcnt lgkmcnt(5)
	v_mfma_f32_16x16x32_bf16 v[108:111], v[140:143], v[164:167], v[108:111]
	v_mfma_f32_16x16x32_bf16 v[104:107], v[148:151], v[164:167], v[104:107]
	s_waitcnt lgkmcnt(3)
	v_mfma_f32_16x16x32_bf16 v[92:95], v[140:143], v[172:175], v[92:95]
	v_mfma_f32_16x16x32_bf16 v[88:91], v[148:151], v[172:175], v[88:91]
	s_waitcnt lgkmcnt(1)
	v_mfma_f32_16x16x32_bf16 v[76:79], v[140:143], v[180:183], v[76:79]
	v_mfma_f32_16x16x32_bf16 v[72:75], v[148:151], v[180:183], v[72:75]
	v_mfma_f32_16x16x32_bf16 v[124:127], v[144:147], v[160:163], v[124:127]
	v_mfma_f32_16x16x32_bf16 v[120:123], v[152:155], v[160:163], v[120:123]
	v_mfma_f32_16x16x32_bf16 v[108:111], v[144:147], v[168:171], v[108:111]
	v_mfma_f32_16x16x32_bf16 v[104:107], v[152:155], v[168:171], v[104:107]
	v_mfma_f32_16x16x32_bf16 v[92:95], v[144:147], v[176:179], v[92:95]
	v_mfma_f32_16x16x32_bf16 v[88:91], v[152:155], v[176:179], v[88:91]
	s_waitcnt lgkmcnt(0)
	v_mfma_f32_16x16x32_bf16 v[76:79], v[144:147], v[184:187], v[76:79]
	v_mfma_f32_16x16x32_bf16 v[72:75], v[152:155], v[184:187], v[72:75]
	s_setprio 0
	s_barrier
	v_add_u32_e32 v139, 0x14010, v136
	ds_read_b128 v[192:195], v139
	ds_read_b128 v[196:199], v139 offset:1024
	ds_read_b128 v[200:203], v139 offset:2048
	ds_read_b128 v[204:207], v139 offset:3072
	s_mov_b32 m0, s3
	s_nop 0
	buffer_load_dwordx4 v132, s[8:11], s60 offen lds
	s_nop 0
	s_mov_b32 m0, s19
	s_nop 0
	buffer_load_dwordx4 v128, s[8:11], s60 offen lds
	s_waitcnt vmcnt(10)
	s_barrier
	s_nop 0
	s_setprio 1
	s_waitcnt lgkmcnt(3)
	v_mfma_f32_16x16x32_bf16 v[116:119], v[192:195], v[156:159], v[116:119]
	s_waitcnt lgkmcnt(1)
	v_mfma_f32_16x16x32_bf16 v[112:115], v[200:203], v[156:159], v[112:115]
	v_mfma_f32_16x16x32_bf16 v[100:103], v[192:195], v[164:167], v[100:103]
	v_mfma_f32_16x16x32_bf16 v[96:99], v[200:203], v[164:167], v[96:99]
	v_mfma_f32_16x16x32_bf16 v[84:87], v[192:195], v[172:175], v[84:87]
	v_mfma_f32_16x16x32_bf16 v[80:83], v[200:203], v[172:175], v[80:83]
	v_mfma_f32_16x16x32_bf16 v[68:71], v[192:195], v[180:183], v[68:71]
	v_mfma_f32_16x16x32_bf16 v[64:67], v[200:203], v[180:183], v[64:67]
	v_mfma_f32_16x16x32_bf16 v[116:119], v[196:199], v[160:163], v[116:119]
	s_waitcnt lgkmcnt(0)
	v_mfma_f32_16x16x32_bf16 v[112:115], v[204:207], v[160:163], v[112:115]
	v_mfma_f32_16x16x32_bf16 v[100:103], v[196:199], v[168:171], v[100:103]
	v_mfma_f32_16x16x32_bf16 v[96:99], v[204:207], v[168:171], v[96:99]
	v_mfma_f32_16x16x32_bf16 v[84:87], v[196:199], v[176:179], v[84:87]
	v_mfma_f32_16x16x32_bf16 v[80:83], v[204:207], v[176:179], v[80:83]
	v_mfma_f32_16x16x32_bf16 v[68:71], v[196:199], v[184:187], v[68:71]
	v_mfma_f32_16x16x32_bf16 v[64:67], v[204:207], v[184:187], v[64:67]
	s_setprio 0
	s_barrier
	ds_read_b128 v[156:159], v137 offset:16400
	ds_read_b128 v[160:163], v137 offset:17424
	ds_read_b128 v[164:167], v137 offset:18448
	ds_read_b128 v[168:171], v137 offset:19472
	ds_read_b128 v[172:175], v137 offset:20496
	ds_read_b128 v[176:179], v137 offset:21520
	ds_read_b128 v[180:183], v137 offset:22544
	ds_read_b128 v[184:187], v137 offset:23568
	s_mov_b32 m0, s2
	s_nop 0
	buffer_load_dwordx4 v133, s[12:15], s60 offen lds
	s_nop 0
	s_mov_b32 m0, s26
	s_nop 0
	buffer_load_dwordx4 v130, s[12:15], s60 offen lds
	s_barrier
	s_nop 0
	s_setprio 1
	s_waitcnt lgkmcnt(7)
	v_mfma_f32_16x16x32_bf16 v[60:63], v[140:143], v[156:159], v[60:63]
	v_mfma_f32_16x16x32_bf16 v[56:59], v[148:151], v[156:159], v[56:59]
	s_waitcnt lgkmcnt(5)
	v_mfma_f32_16x16x32_bf16 v[44:47], v[140:143], v[164:167], v[44:47]
	v_mfma_f32_16x16x32_bf16 v[40:43], v[148:151], v[164:167], v[40:43]
	s_waitcnt lgkmcnt(3)
	v_mfma_f32_16x16x32_bf16 v[28:31], v[140:143], v[172:175], v[28:31]
	v_mfma_f32_16x16x32_bf16 v[24:27], v[148:151], v[172:175], v[24:27]
	s_waitcnt lgkmcnt(1)
	v_mfma_f32_16x16x32_bf16 v[12:15], v[140:143], v[180:183], v[12:15]
	v_mfma_f32_16x16x32_bf16 v[8:11], v[148:151], v[180:183], v[8:11]
	v_mfma_f32_16x16x32_bf16 v[60:63], v[144:147], v[160:163], v[60:63]
	v_mfma_f32_16x16x32_bf16 v[56:59], v[152:155], v[160:163], v[56:59]
	v_mfma_f32_16x16x32_bf16 v[44:47], v[144:147], v[168:171], v[44:47]
	v_mfma_f32_16x16x32_bf16 v[40:43], v[152:155], v[168:171], v[40:43]
	v_mfma_f32_16x16x32_bf16 v[28:31], v[144:147], v[176:179], v[28:31]
	v_mfma_f32_16x16x32_bf16 v[24:27], v[152:155], v[176:179], v[24:27]
	s_waitcnt lgkmcnt(0)
	v_mfma_f32_16x16x32_bf16 v[12:15], v[144:147], v[184:187], v[12:15]
	v_mfma_f32_16x16x32_bf16 v[8:11], v[152:155], v[184:187], v[8:11]
	s_setprio 0
	s_barrier
; #define G_WAIT_V(n) asm volatile("s_waitcnt vmcnt(" #n ")" ::: "memory")
; #define G_BAR() __builtin_amdgcn_s_barrier()
; #define G_SCHED() __builtin_amdgcn_sched_barrier(0)
; #define D_STAGE_A(slot, half, kt) D_STAGE(rsA, voffA, slot, half, kt)
; #define D_STAGE_B(slot, half, kt) D_STAGE(rsB, voffB, slot, half, kt)
; #define D_LDA(dst, slot) do { _Pragma("unroll") for (int m = 0; m < 4; ++m) _Pragma("unroll") for (int k = 0; k < 2; ++k) \
;     dst[m][k] = *(const LDS_AS bf16x8*)(lds + (slot) + aoff + m * 2048 + k * 1024); } while (0)
; #define D_LDB(dst, slot) do { _Pragma("unroll") for (int n = 0; n < 2; ++n) _Pragma("unroll") for (int k = 0; k < 2; ++k) \
;     dst[n][k] = *(const LDS_AS bf16x8*)(lds + (slot) + boff + n * 2048 + k * 1024); } while (0)
; #define D_WAIT_L(n) asm volatile("s_waitcnt lgkmcnt(" #n ")" ::: "memory")
; #define D_STAGE_A(slot, half, kt) D_STAGE(rsA, voffA, slot, half, kt)
; template <class Cfg>
; DI void gemm256dma_unit(LDS_AS unsigned char* lds, const Cfg& cfg) {
;     ...
;   for (int t = 0; t < nt; t += 2) {
;     const int t1 = t + 1;
;     const int t2 = (t + 2 < nt) ? t + 2 : 0;
;     const int t3 = (t + 2 < nt) ? t + 3 : 1;
;     D_LDB(B0, G_SB(0, 0)); G_SCHED(); D_LDA(At, G_SA(0, 0)); D_STAGE_A(G_SA(1, 1), 1, t1);
;     D_WAIT_L(8); G_BAR(); D_WAIT_L(0); G_SCHED(); D_MMA(0, 0, At, B0); G_BAR(); G_SCHED();
;     D_LDB(B1, G_SB(0, 1)); D_STAGE_B(G_SB(0, 0), 0, t2);
;     G_BAR(); D_WAIT_L(0); G_SCHED(); D_MMA(0, 1, At, B1); G_BAR(); G_SCHED();
;     D_LDA(At, G_SA(0, 1)); D_STAGE_A(G_SA(0, 0), 0, t2);
;     G_BAR(); D_WAIT_L(0); G_SCHED(); D_MMA(1, 0, At, B0); G_BAR(); G_SCHED();
;     D_STAGE_B(G_SB(0, 1), 1, t2);
;     G_WAIT_V(6); G_BAR(); G_SCHED(); D_MMA(1, 1, At, B1); G_BAR(); G_SCHED();
;     D_LDB(B0, G_SB(1, 0)); G_SCHED(); D_LDA(At, G_SA(1, 0)); D_STAGE_A(G_SA(0, 1), 1, t2);
;     D_WAIT_L(8); G_BAR(); D_WAIT_L(0); G_SCHED(); D_MMA(0, 0, At, B0); G_BAR(); G_SCHED();
;     D_LDB(B1, G_SB(1, 1)); D_STAGE_B(G_SB(1, 0), 0, t3);
;     G_BAR(); D_WAIT_L(0); G_SCHED(); D_MMA(0, 1, At, B1); G_BAR(); G_SCHED();
;     D_LDA(At, G_SA(1, 1)); D_STAGE_A(G_SA(1, 0), 0, t3);
;     G_BAR(); D_WAIT_L(0); G_SCHED(); D_MMA(1, 0, At, B0); G_BAR(); G_SCHED();
;     D_STAGE_B(G_SB(1, 1), 1, t3);
;     G_WAIT_V(6); G_BAR(); G_SCHED(); D_MMA(1, 1, At, B1); G_BAR(); G_SCHED();
;   }
	s_mov_b32 m0, s27
	s_nop 0
	buffer_load_dwordx4 v129, s[8:11], s60 offen lds
	s_nop 0
	s_mov_b32 m0, s28
	s_nop 0
	buffer_load_dwordx4 v135, s[8:11], s60 offen lds
	s_waitcnt vmcnt(10)
	s_barrier
	s_setprio 1
	v_mfma_f32_16x16x32_bf16 v[52:55], v[192:195], v[156:159], v[52:55]
	v_mfma_f32_16x16x32_bf16 v[48:51], v[200:203], v[156:159], v[48:51]
	v_mfma_f32_16x16x32_bf16 v[36:39], v[192:195], v[164:167], v[36:39]
	v_mfma_f32_16x16x32_bf16 v[32:35], v[200:203], v[164:167], v[32:35]
	v_mfma_f32_16x16x32_bf16 v[20:23], v[192:195], v[172:175], v[20:23]
	v_mfma_f32_16x16x32_bf16 v[16:19], v[200:203], v[172:175], v[16:19]
	v_mfma_f32_16x16x32_bf16 v[4:7], v[192:195], v[180:183], v[4:7]
	v_mfma_f32_16x16x32_bf16 v[0:3], v[200:203], v[180:183], v[0:3]
	v_mfma_f32_16x16x32_bf16 v[52:55], v[196:199], v[160:163], v[52:55]
	v_mfma_f32_16x16x32_bf16 v[48:51], v[204:207], v[160:163], v[48:51]
	v_mfma_f32_16x16x32_bf16 v[36:39], v[196:199], v[168:171], v[36:39]
	v_mfma_f32_16x16x32_bf16 v[32:35], v[204:207], v[168:171], v[32:35]
	v_mfma_f32_16x16x32_bf16 v[20:23], v[196:199], v[176:179], v[20:23]
	v_mfma_f32_16x16x32_bf16 v[16:19], v[204:207], v[176:179], v[16:19]
	v_mfma_f32_16x16x32_bf16 v[4:7], v[196:199], v[184:187], v[4:7]
	v_mfma_f32_16x16x32_bf16 v[0:3], v[204:207], v[184:187], v[0:3]
	s_setprio 0
	s_barrier
	v_add_u32_e32 v139, 0x18010, v136
	ds_read_b128 v[140:143], v139
	ds_read_b128 v[144:147], v139 offset:1024
	ds_read_b128 v[148:151], v139 offset:2048
	ds_read_b128 v[152:155], v139 offset:3072
	ds_read_b128 v[156:159], v137 offset:32784
	ds_read_b128 v[160:163], v137 offset:33808
	ds_read_b128 v[164:167], v137 offset:34832
	ds_read_b128 v[168:171], v137 offset:35856
	ds_read_b128 v[172:175], v137 offset:36880
	ds_read_b128 v[176:179], v137 offset:37904
	ds_read_b128 v[180:183], v137 offset:38928
	ds_read_b128 v[184:187], v137 offset:39952
	s_mov_b32 m0, s30
	s_nop 0
	buffer_load_dwordx4 v134, s[12:15], s60 offen lds
	s_nop 0
	s_mov_b32 m0, s31
	s_nop 0
	buffer_load_dwordx4 v131, s[12:15], s60 offen lds
	s_waitcnt lgkmcnt(8)
	s_waitcnt vmcnt(10)
	s_barrier
	s_nop 0
	s_setprio 1
	s_waitcnt lgkmcnt(7)
	v_mfma_f32_16x16x32_bf16 v[124:127], v[140:143], v[156:159], v[124:127]
	v_mfma_f32_16x16x32_bf16 v[120:123], v[148:151], v[156:159], v[120:123]
	s_waitcnt lgkmcnt(5)
	v_mfma_f32_16x16x32_bf16 v[108:111], v[140:143], v[164:167], v[108:111]
	v_mfma_f32_16x16x32_bf16 v[104:107], v[148:151], v[164:167], v[104:107]
	s_waitcnt lgkmcnt(3)
	v_mfma_f32_16x16x32_bf16 v[92:95], v[140:143], v[172:175], v[92:95]
	v_mfma_f32_16x16x32_bf16 v[88:91], v[148:151], v[172:175], v[88:91]
	s_waitcnt lgkmcnt(1)
	v_mfma_f32_16x16x32_bf16 v[76:79], v[140:143], v[180:183], v[76:79]
	v_mfma_f32_16x16x32_bf16 v[72:75], v[148:151], v[180:183], v[72:75]
	v_mfma_f32_16x16x32_bf16 v[124:127], v[144:147], v[160:163], v[124:127]
	v_mfma_f32_16x16x32_bf16 v[120:123], v[152:155], v[160:163], v[120:123]
	v_mfma_f32_16x16x32_bf16 v[108:111], v[144:147], v[168:171], v[108:111]
	v_mfma_f32_16x16x32_bf16 v[104:107], v[152:155], v[168:171], v[104:107]
	v_mfma_f32_16x16x32_bf16 v[92:95], v[144:147], v[176:179], v[92:95]
	v_mfma_f32_16x16x32_bf16 v[88:91], v[152:155], v[176:179], v[88:91]
	s_waitcnt lgkmcnt(0)
	v_mfma_f32_16x16x32_bf16 v[76:79], v[144:147], v[184:187], v[76:79]
	v_mfma_f32_16x16x32_bf16 v[72:75], v[152:155], v[184:187], v[72:75]
	s_setprio 0
	s_barrier
	v_add_u32_e32 v139, 0x1c010, v136
	ds_read_b128 v[192:195], v139
	ds_read_b128 v[196:199], v139 offset:1024
	ds_read_b128 v[200:203], v139 offset:2048
	ds_read_b128 v[204:207], v139 offset:3072
	s_mov_b32 m0, s33
	s_nop 0
	buffer_load_dwordx4 v132, s[8:11], s55 offen lds
	s_nop 0
	s_mov_b32 m0, s34
	s_nop 0
	buffer_load_dwordx4 v128, s[8:11], s55 offen lds
	s_waitcnt vmcnt(10)
	s_barrier
; #define G_WAIT_V(n) asm volatile("s_waitcnt vmcnt(" #n ")" ::: "memory")
; #define G_BAR() __builtin_amdgcn_s_barrier()
; #define G_SCHED() __builtin_amdgcn_sched_barrier(0)
; #define D_STAGE_A(slot, half, kt) D_STAGE(rsA, voffA, slot, half, kt)
; #define D_STAGE_B(slot, half, kt) D_STAGE(rsB, voffB, slot, half, kt)
; #define D_LDA(dst, slot) do { _Pragma("unroll") for (int m = 0; m < 4; ++m) _Pragma("unroll") for (int k = 0; k < 2; ++k) \
;     dst[m][k] = *(const LDS_AS bf16x8*)(lds + (slot) + aoff + m * 2048 + k * 1024); } while (0)
; #define D_LDB(dst, slot) do { _Pragma("unroll") for (int n = 0; n < 2; ++n) _Pragma("unroll") for (int k = 0; k < 2; ++k) \
;     dst[n][k] = *(const LDS_AS bf16x8*)(lds + (slot) + boff + n * 2048 + k * 1024); } while (0)
; #define D_WAIT_L(n) asm volatile("s_waitcnt lgkmcnt(" #n ")" ::: "memory")
; #define D_STAGE_A(slot, half, kt) D_STAGE(rsA, voffA, slot, half, kt)
; template <class Cfg>
; DI void gemm256dma_unit(LDS_AS unsigned char* lds, const Cfg& cfg) {
;     ...
;   for (int t = 0; t < nt; t += 2) {
;     const int t1 = t + 1;
;     const int t2 = (t + 2 < nt) ? t + 2 : 0;
;     const int t3 = (t + 2 < nt) ? t + 3 : 1;
;     D_LDB(B0, G_SB(0, 0)); G_SCHED(); D_LDA(At, G_SA(0, 0)); D_STAGE_A(G_SA(1, 1), 1, t1);
;     D_WAIT_L(8); G_BAR(); D_WAIT_L(0); G_SCHED(); D_MMA(0, 0, At, B0); G_BAR(); G_SCHED();
;     D_LDB(B1, G_SB(0, 1)); D_STAGE_B(G_SB(0, 0), 0, t2);
;     G_BAR(); D_WAIT_L(0); G_SCHED(); D_MMA(0, 1, At, B1); G_BAR(); G_SCHED();
;     D_LDA(At, G_SA(0, 1)); D_STAGE_A(G_SA(0, 0), 0, t2);
;     G_BAR(); D_WAIT_L(0); G_SCHED(); D_MMA(1, 0, At, B0); G_BAR(); G_SCHED();
;     D_STAGE_B(G_SB(0, 1), 1, t2);
;     G_WAIT_V(6); G_BAR(); G_SCHED(); D_MMA(1, 1, At, B1); G_BAR(); G_SCHED();
;     D_LDB(B0, G_SB(1, 0)); G_SCHED(); D_LDA(At, G_SA(1, 0)); D_STAGE_A(G_SA(0, 1), 1, t2);
;     D_WAIT_L(8); G_BAR(); D_WAIT_L(0); G_SCHED(); D_MMA(0, 0, At, B0); G_BAR(); G_SCHED();
;     D_LDB(B1, G_SB(1, 1)); D_STAGE_B(G_SB(1, 0), 0, t3);
;     G_BAR(); D_WAIT_L(0); G_SCHED(); D_MMA(0, 1, At, B1); G_BAR(); G_SCHED();
;     D_LDA(At, G_SA(1, 1)); D_STAGE_A(G_SA(1, 0), 0, t3);
;     G_BAR(); D_WAIT_L(0); G_SCHED(); D_MMA(1, 0, At, B0); G_BAR(); G_SCHED();
;     D_STAGE_B(G_SB(1, 1), 1, t3);
;     G_WAIT_V(6); G_BAR(); G_SCHED(); D_MMA(1, 1, At, B1); G_BAR(); G_SCHED();
;   }
	s_nop 0
	s_setprio 1
	s_waitcnt lgkmcnt(3)
	v_mfma_f32_16x16x32_bf16 v[116:119], v[192:195], v[156:159], v[116:119]
	s_waitcnt lgkmcnt(1)
	v_mfma_f32_16x16x32_bf16 v[112:115], v[200:203], v[156:159], v[112:115]
	v_mfma_f32_16x16x32_bf16 v[100:103], v[192:195], v[164:167], v[100:103]
	v_mfma_f32_16x16x32_bf16 v[96:99], v[200:203], v[164:167], v[96:99]
	v_mfma_f32_16x16x32_bf16 v[84:87], v[192:195], v[172:175], v[84:87]
	v_mfma_f32_16x16x32_bf16 v[80:83], v[200:203], v[172:175], v[80:83]
	v_mfma_f32_16x16x32_bf16 v[68:71], v[192:195], v[180:183], v[68:71]
	v_mfma_f32_16x16x32_bf16 v[64:67], v[200:203], v[180:183], v[64:67]
	v_mfma_f32_16x16x32_bf16 v[116:119], v[196:199], v[160:163], v[116:119]
	s_waitcnt lgkmcnt(0)
	v_mfma_f32_16x16x32_bf16 v[112:115], v[204:207], v[160:163], v[112:115]
	v_mfma_f32_16x16x32_bf16 v[100:103], v[196:199], v[168:171], v[100:103]
	v_mfma_f32_16x16x32_bf16 v[96:99], v[204:207], v[168:171], v[96:99]
	v_mfma_f32_16x16x32_bf16 v[84:87], v[196:199], v[176:179], v[84:87]
	v_mfma_f32_16x16x32_bf16 v[80:83], v[204:207], v[176:179], v[80:83]
	v_mfma_f32_16x16x32_bf16 v[68:71], v[196:199], v[184:187], v[68:71]
	v_mfma_f32_16x16x32_bf16 v[64:67], v[204:207], v[184:187], v[64:67]
	s_setprio 0
	s_barrier
	ds_read_b128 v[156:159], v137 offset:49168
	ds_read_b128 v[160:163], v137 offset:50192
	ds_read_b128 v[164:167], v137 offset:51216
	ds_read_b128 v[168:171], v137 offset:52240
	ds_read_b128 v[172:175], v137 offset:53264
	ds_read_b128 v[176:179], v137 offset:54288
	ds_read_b128 v[180:183], v137 offset:55312
	ds_read_b128 v[184:187], v137 offset:56336
	s_mov_b32 m0, s35
	s_nop 0
	buffer_load_dwordx4 v133, s[12:15], s55 offen lds
	s_nop 0
	s_mov_b32 m0, s36
	s_nop 0
	buffer_load_dwordx4 v130, s[12:15], s55 offen lds
	s_barrier
	s_nop 0
	s_setprio 1
	s_waitcnt lgkmcnt(7)
	v_mfma_f32_16x16x32_bf16 v[60:63], v[140:143], v[156:159], v[60:63]
	v_mfma_f32_16x16x32_bf16 v[56:59], v[148:151], v[156:159], v[56:59]
	s_waitcnt lgkmcnt(5)
	v_mfma_f32_16x16x32_bf16 v[44:47], v[140:143], v[164:167], v[44:47]
	v_mfma_f32_16x16x32_bf16 v[40:43], v[148:151], v[164:167], v[40:43]
	s_waitcnt lgkmcnt(3)
	v_mfma_f32_16x16x32_bf16 v[28:31], v[140:143], v[172:175], v[28:31]
	v_mfma_f32_16x16x32_bf16 v[24:27], v[148:151], v[172:175], v[24:27]
	s_waitcnt lgkmcnt(1)
	v_mfma_f32_16x16x32_bf16 v[12:15], v[140:143], v[180:183], v[12:15]
	v_mfma_f32_16x16x32_bf16 v[8:11], v[148:151], v[180:183], v[8:11]
	v_mfma_f32_16x16x32_bf16 v[60:63], v[144:147], v[160:163], v[60:63]
	v_mfma_f32_16x16x32_bf16 v[56:59], v[152:155], v[160:163], v[56:59]
	v_mfma_f32_16x16x32_bf16 v[44:47], v[144:147], v[168:171], v[44:47]
	v_mfma_f32_16x16x32_bf16 v[40:43], v[152:155], v[168:171], v[40:43]
	v_mfma_f32_16x16x32_bf16 v[28:31], v[144:147], v[176:179], v[28:31]
	v_mfma_f32_16x16x32_bf16 v[24:27], v[152:155], v[176:179], v[24:27]
	s_waitcnt lgkmcnt(0)
	v_mfma_f32_16x16x32_bf16 v[12:15], v[144:147], v[184:187], v[12:15]
	v_mfma_f32_16x16x32_bf16 v[8:11], v[152:155], v[184:187], v[8:11]
	s_setprio 0
	s_barrier
	s_mov_b32 m0, s37
	s_nop 0
	buffer_load_dwordx4 v129, s[8:11], s55 offen lds
	s_nop 0
	s_mov_b32 m0, s39
	s_nop 0
	buffer_load_dwordx4 v135, s[8:11], s55 offen lds
	s_waitcnt vmcnt(10)
	s_barrier
	s_setprio 1
	v_mfma_f32_16x16x32_bf16 v[52:55], v[192:195], v[156:159], v[52:55]
	v_mfma_f32_16x16x32_bf16 v[48:51], v[200:203], v[156:159], v[48:51]
	v_mfma_f32_16x16x32_bf16 v[36:39], v[192:195], v[164:167], v[36:39]
	v_mfma_f32_16x16x32_bf16 v[32:35], v[200:203], v[164:167], v[32:35]
	v_mfma_f32_16x16x32_bf16 v[20:23], v[192:195], v[172:175], v[20:23]
	v_mfma_f32_16x16x32_bf16 v[16:19], v[200:203], v[172:175], v[16:19]
	v_mfma_f32_16x16x32_bf16 v[4:7], v[192:195], v[180:183], v[4:7]
	v_mfma_f32_16x16x32_bf16 v[0:3], v[200:203], v[180:183], v[0:3]
	v_mfma_f32_16x16x32_bf16 v[52:55], v[196:199], v[160:163], v[52:55]
	v_mfma_f32_16x16x32_bf16 v[48:51], v[204:207], v[160:163], v[48:51]
	v_mfma_f32_16x16x32_bf16 v[36:39], v[196:199], v[168:171], v[36:39]
	v_mfma_f32_16x16x32_bf16 v[32:35], v[204:207], v[168:171], v[32:35]
	v_mfma_f32_16x16x32_bf16 v[20:23], v[196:199], v[176:179], v[20:23]
	v_mfma_f32_16x16x32_bf16 v[16:19], v[204:207], v[176:179], v[16:19]
	v_mfma_f32_16x16x32_bf16 v[4:7], v[196:199], v[184:187], v[4:7]
	v_mfma_f32_16x16x32_bf16 v[0:3], v[204:207], v[184:187], v[0:3]
	s_setprio 0
	s_barrier
	s_mov_b32 s47, s54
	s_cbranch_scc0 .LBB0_830
	s_waitcnt vmcnt(0)
	s_cmpk_lt_u32 s16, 0x100
	s_cbranch_scc0 .LBB0_833
	s_barrier

; #define G_WAIT_V(n) asm volatile("s_waitcnt vmcnt(" #n ")" ::: "memory")
; #define G_BAR() __builtin_amdgcn_s_barrier()
; #define G_SCHED() __builtin_amdgcn_sched_barrier(0)
; #define D_STAGE_A(slot, half, kt) D_STAGE(rsA, voffA, slot, half, kt)
; #define D_STAGE_B(slot, half, kt) D_STAGE(rsB, voffB, slot, half, kt)
; #define D_LDA(dst, slot) do { _Pragma("unroll") for (int m = 0; m < 4; ++m) _Pragma("unroll") for (int k = 0; k < 2; ++k) \
;     dst[m][k] = *(const LDS_AS bf16x8*)(lds + (slot) + aoff + m * 2048 + k * 1024); } while (0)
; #define D_LDB(dst, slot) do { _Pragma("unroll") for (int n = 0; n < 2; ++n) _Pragma("unroll") for (int k = 0; k < 2; ++k) \
;     dst[n][k] = *(const LDS_AS bf16x8*)(lds + (slot) + boff + n * 2048 + k * 1024); } while (0)
; #define D_WAIT_L(n) asm volatile("s_waitcnt lgkmcnt(" #n ")" ::: "memory")
; #define D_STAGE_A(slot, half, kt) D_STAGE(rsA, voffA, slot, half, kt)
; template <class Cfg>
; DI void gemm256dma_unit(LDS_AS unsigned char* lds, const Cfg& cfg) {
;     ...
;   for (int t = 0; t < nt; t += 2) {
;     const int t1 = t + 1;
;     const int t2 = (t + 2 < nt) ? t + 2 : 0;
;     const int t3 = (t + 2 < nt) ? t + 3 : 1;
;     D_LDB(B0, G_SB(0, 0)); G_SCHED(); D_LDA(At, G_SA(0, 0)); D_STAGE_A(G_SA(1, 1), 1, t1);
;     D_WAIT_L(8); G_BAR(); D_WAIT_L(0); G_SCHED(); D_MMA(0, 0, At, B0); G_BAR(); G_SCHED();
;     D_LDB(B1, G_SB(0, 1)); D_STAGE_B(G_SB(0, 0), 0, t2);
;     G_BAR(); D_WAIT_L(0); G_SCHED(); D_MMA(0, 1, At, B1); G_BAR(); G_SCHED();
;     D_LDA(At, G_SA(0, 1)); D_STAGE_A(G_SA(0, 0), 0, t2);
;     G_BAR(); D_WAIT_L(0); G_SCHED(); D_MMA(1, 0, At, B0); G_BAR(); G_SCHED();
;     D_STAGE_B(G_SB(0, 1), 1, t2);
;     G_WAIT_V(6); G_BAR(); G_SCHED(); D_MMA(1, 1, At, B1); G_BAR(); G_SCHED();
;     D_LDB(B0, G_SB(1, 0)); G_SCHED(); D_LDA(At, G_SA(1, 0)); D_STAGE_A(G_SA(0, 1), 1, t2);
;     D_WAIT_L(8); G_BAR(); D_WAIT_L(0); G_SCHED(); D_MMA(0, 0, At, B0); G_BAR(); G_SCHED();
;     D_LDB(B1, G_SB(1, 1)); D_STAGE_B(G_SB(1, 0), 0, t3);
;     G_BAR(); D_WAIT_L(0); G_SCHED(); D_MMA(0, 1, At, B1); G_BAR(); G_SCHED();
;     D_LDA(At, G_SA(1, 1)); D_STAGE_A(G_SA(1, 0), 0, t3);
;     G_BAR(); D_WAIT_L(0); G_SCHED(); D_MMA(1, 0, At, B0); G_BAR(); G_SCHED();
;     D_STAGE_B(G_SB(1, 1), 1, t3);
;     G_WAIT_V(6); G_BAR(); G_SCHED(); D_MMA(1, 1, At, B1); G_BAR(); G_SCHED();
;   }
.LBB0_1266:
	ds_read_b128 v[142:145], v137
	ds_read_b128 v[146:149], v137 offset:1024
	ds_read_b128 v[150:153], v137 offset:2048
	ds_read_b128 v[154:157], v137 offset:3072
	s_add_i32 s34, s33, 2
	s_add_i32 s36, s31, 0xffffff00
	s_add_i32 s35, s31, 0xffffff80
	s_cmp_lt_u32 s33, 30
	s_cselect_b32 s37, s35, 0
	s_cselect_b32 s35, s31, 0x80
	s_addk_i32 s31, 0x100
	s_cmp_gt_u32 s33, 29
	ds_read_b128 v[158:161], v138 offset:16
	ds_read_b128 v[162:165], v138 offset:1040
	ds_read_b128 v[166:169], v138 offset:2064
	ds_read_b128 v[170:173], v138 offset:3088
	ds_read_b128 v[174:177], v138 offset:4112
	ds_read_b128 v[178:181], v138 offset:5136
	ds_read_b128 v[182:185], v138 offset:6160
	ds_read_b128 v[186:189], v138 offset:7184
	s_mov_b32 m0, s29
	s_nop 0
	buffer_load_dwordx4 v129, s[0:3], s36 offen lds
	s_nop 0
	s_mov_b32 m0, s30
	s_nop 0
	buffer_load_dwordx4 v134, s[0:3], s36 offen lds
	s_waitcnt lgkmcnt(8)
	s_waitcnt vmcnt(10)
	s_barrier
	s_nop 0
	s_setprio 1
	s_waitcnt lgkmcnt(7)
	v_mfma_f32_16x16x32_bf16 v[124:127], v[142:145], v[158:161], v[124:127]
	v_mfma_f32_16x16x32_bf16 v[120:123], v[150:153], v[158:161], v[120:123]
	s_waitcnt lgkmcnt(5)
	v_mfma_f32_16x16x32_bf16 v[108:111], v[142:145], v[166:169], v[108:111]
	v_mfma_f32_16x16x32_bf16 v[104:107], v[150:153], v[166:169], v[104:107]
	s_waitcnt lgkmcnt(3)
	v_mfma_f32_16x16x32_bf16 v[92:95], v[142:145], v[174:177], v[92:95]
	v_mfma_f32_16x16x32_bf16 v[88:91], v[150:153], v[174:177], v[88:91]
	s_waitcnt lgkmcnt(1)
	v_mfma_f32_16x16x32_bf16 v[76:79], v[142:145], v[182:185], v[76:79]
	v_mfma_f32_16x16x32_bf16 v[72:75], v[150:153], v[182:185], v[72:75]
	v_mfma_f32_16x16x32_bf16 v[124:127], v[146:149], v[162:165], v[124:127]
	v_mfma_f32_16x16x32_bf16 v[120:123], v[154:157], v[162:165], v[120:123]
	v_mfma_f32_16x16x32_bf16 v[108:111], v[146:149], v[170:173], v[108:111]
	v_mfma_f32_16x16x32_bf16 v[104:107], v[154:157], v[170:173], v[104:107]
	v_mfma_f32_16x16x32_bf16 v[92:95], v[146:149], v[178:181], v[92:95]
	v_mfma_f32_16x16x32_bf16 v[88:91], v[154:157], v[178:181], v[88:91]
	s_waitcnt lgkmcnt(0)
	v_mfma_f32_16x16x32_bf16 v[76:79], v[146:149], v[186:189], v[76:79]
	v_mfma_f32_16x16x32_bf16 v[72:75], v[154:157], v[186:189], v[72:75]
	s_setprio 0
	s_barrier
	ds_read_b128 v[192:195], v139
	ds_read_b128 v[196:199], v139 offset:1024
	ds_read_b128 v[200:203], v139 offset:2048
	ds_read_b128 v[204:207], v139 offset:3072
	s_mov_b32 m0, s13
	s_nop 0
	buffer_load_dwordx4 v130, s[44:47], s37 offen lds
	s_nop 0
	s_mov_b32 m0, s14
	s_nop 0
	buffer_load_dwordx4 v135, s[44:47], s37 offen lds
	s_waitcnt vmcnt(10)
	s_barrier
	s_nop 0
	s_setprio 1
	s_waitcnt lgkmcnt(3)
	v_mfma_f32_16x16x32_bf16 v[116:119], v[192:195], v[158:161], v[116:119]
	s_waitcnt lgkmcnt(1)
	v_mfma_f32_16x16x32_bf16 v[112:115], v[200:203], v[158:161], v[112:115]
	v_mfma_f32_16x16x32_bf16 v[100:103], v[192:195], v[166:169], v[100:103]
	v_mfma_f32_16x16x32_bf16 v[96:99], v[200:203], v[166:169], v[96:99]
	v_mfma_f32_16x16x32_bf16 v[84:87], v[192:195], v[174:177], v[84:87]
	v_mfma_f32_16x16x32_bf16 v[80:83], v[200:203], v[174:177], v[80:83]
	v_mfma_f32_16x16x32_bf16 v[68:71], v[192:195], v[182:185], v[68:71]
	v_mfma_f32_16x16x32_bf16 v[64:67], v[200:203], v[182:185], v[64:67]
	v_mfma_f32_16x16x32_bf16 v[116:119], v[196:199], v[162:165], v[116:119]
	s_waitcnt lgkmcnt(0)
	v_mfma_f32_16x16x32_bf16 v[112:115], v[204:207], v[162:165], v[112:115]
	v_mfma_f32_16x16x32_bf16 v[100:103], v[196:199], v[170:173], v[100:103]
	v_mfma_f32_16x16x32_bf16 v[96:99], v[204:207], v[170:173], v[96:99]
	v_mfma_f32_16x16x32_bf16 v[84:87], v[196:199], v[178:181], v[84:87]
	v_mfma_f32_16x16x32_bf16 v[80:83], v[204:207], v[178:181], v[80:83]
	v_mfma_f32_16x16x32_bf16 v[68:71], v[196:199], v[186:189], v[68:71]
	v_mfma_f32_16x16x32_bf16 v[64:67], v[204:207], v[186:189], v[64:67]
	s_setprio 0
	s_barrier
	ds_read_b128 v[158:161], v138 offset:16400
	ds_read_b128 v[162:165], v138 offset:17424
	ds_read_b128 v[166:169], v138 offset:18448
	ds_read_b128 v[170:173], v138 offset:19472
	ds_read_b128 v[174:177], v138 offset:20496
	ds_read_b128 v[178:181], v138 offset:21520
	ds_read_b128 v[182:185], v138 offset:22544
	ds_read_b128 v[186:189], v138 offset:23568
	s_mov_b32 m0, s15
	s_nop 0
	buffer_load_dwordx4 v128, s[0:3], s37 offen lds
	s_nop 0
	s_mov_b32 m0, s16
	s_nop 0
	buffer_load_dwordx4 v133, s[0:3], s37 offen lds
	s_barrier
	s_nop 0
	s_setprio 1
	s_waitcnt lgkmcnt(7)
	v_mfma_f32_16x16x32_bf16 v[60:63], v[142:145], v[158:161], v[60:63]
	v_mfma_f32_16x16x32_bf16 v[56:59], v[150:153], v[158:161], v[56:59]
	s_waitcnt lgkmcnt(5)
	v_mfma_f32_16x16x32_bf16 v[44:47], v[142:145], v[166:169], v[44:47]
	v_mfma_f32_16x16x32_bf16 v[40:43], v[150:153], v[166:169], v[40:43]
	s_waitcnt lgkmcnt(3)
	v_mfma_f32_16x16x32_bf16 v[28:31], v[142:145], v[174:177], v[28:31]
	v_mfma_f32_16x16x32_bf16 v[24:27], v[150:153], v[174:177], v[24:27]
	s_waitcnt lgkmcnt(1)
	v_mfma_f32_16x16x32_bf16 v[12:15], v[142:145], v[182:185], v[12:15]
	v_mfma_f32_16x16x32_bf16 v[8:11], v[150:153], v[182:185], v[8:11]
	v_mfma_f32_16x16x32_bf16 v[60:63], v[146:149], v[162:165], v[60:63]
	v_mfma_f32_16x16x32_bf16 v[56:59], v[154:157], v[162:165], v[56:59]
	v_mfma_f32_16x16x32_bf16 v[44:47], v[146:149], v[170:173], v[44:47]
	v_mfma_f32_16x16x32_bf16 v[40:43], v[154:157], v[170:173], v[40:43]
	v_mfma_f32_16x16x32_bf16 v[28:31], v[146:149], v[178:181], v[28:31]
	v_mfma_f32_16x16x32_bf16 v[24:27], v[154:157], v[178:181], v[24:27]
	s_waitcnt lgkmcnt(0)
	v_mfma_f32_16x16x32_bf16 v[12:15], v[146:149], v[186:189], v[12:15]
	v_mfma_f32_16x16x32_bf16 v[8:11], v[154:157], v[186:189], v[8:11]
	s_setprio 0
	s_barrier
; #define G_WAIT_V(n) asm volatile("s_waitcnt vmcnt(" #n ")" ::: "memory")
; #define G_BAR() __builtin_amdgcn_s_barrier()
; #define G_SCHED() __builtin_amdgcn_sched_barrier(0)
; #define D_STAGE_A(slot, half, kt) D_STAGE(rsA, voffA, slot, half, kt)
; #define D_STAGE_B(slot, half, kt) D_STAGE(rsB, voffB, slot, half, kt)
; #define D_LDA(dst, slot) do { _Pragma("unroll") for (int m = 0; m < 4; ++m) _Pragma("unroll") for (int k = 0; k < 2; ++k) \
;     dst[m][k] = *(const LDS_AS bf16x8*)(lds + (slot) + aoff + m * 2048 + k * 1024); } while (0)
; #define D_LDB(dst, slot) do { _Pragma("unroll") for (int n = 0; n < 2; ++n) _Pragma("unroll") for (int k = 0; k < 2; ++k) \
;     dst[n][k] = *(const LDS_AS bf16x8*)(lds + (slot) + boff + n * 2048 + k * 1024); } while (0)
; #define D_WAIT_L(n) asm volatile("s_waitcnt lgkmcnt(" #n ")" ::: "memory")
; #define D_STAGE_A(slot, half, kt) D_STAGE(rsA, voffA, slot, half, kt)
; template <class Cfg>
; DI void gemm256dma_unit(LDS_AS unsigned char* lds, const Cfg& cfg) {
;     ...
;   for (int t = 0; t < nt; t += 2) {
;     const int t1 = t + 1;
;     const int t2 = (t + 2 < nt) ? t + 2 : 0;
;     const int t3 = (t + 2 < nt) ? t + 3 : 1;
;     D_LDB(B0, G_SB(0, 0)); G_SCHED(); D_LDA(At, G_SA(0, 0)); D_STAGE_A(G_SA(1, 1), 1, t1);
;     D_WAIT_L(8); G_BAR(); D_WAIT_L(0); G_SCHED(); D_MMA(0, 0, At, B0); G_BAR(); G_SCHED();
;     D_LDB(B1, G_SB(0, 1)); D_STAGE_B(G_SB(0, 0), 0, t2);
;     G_BAR(); D_WAIT_L(0); G_SCHED(); D_MMA(0, 1, At, B1); G_BAR(); G_SCHED();
;     D_LDA(At, G_SA(0, 1)); D_STAGE_A(G_SA(0, 0), 0, t2);
;     G_BAR(); D_WAIT_L(0); G_SCHED(); D_MMA(1, 0, At, B0); G_BAR(); G_SCHED();
;     D_STAGE_B(G_SB(0, 1), 1, t2);
;     G_WAIT_V(6); G_BAR(); G_SCHED(); D_MMA(1, 1, At, B1); G_BAR(); G_SCHED();
;     D_LDB(B0, G_SB(1, 0)); G_SCHED(); D_LDA(At, G_SA(1, 0)); D_STAGE_A(G_SA(0, 1), 1, t2);
;     D_WAIT_L(8); G_BAR(); D_WAIT_L(0); G_SCHED(); D_MMA(0, 0, At, B0); G_BAR(); G_SCHED();
;     D_LDB(B1, G_SB(1, 1)); D_STAGE_B(G_SB(1, 0), 0, t3);
;     G_BAR(); D_WAIT_L(0); G_SCHED(); D_MMA(0, 1, At, B1); G_BAR(); G_SCHED();
;     D_LDA(At, G_SA(1, 1)); D_STAGE_A(G_SA(1, 0), 0, t3);
;     G_BAR(); D_WAIT_L(0); G_SCHED(); D_MMA(1, 0, At, B0); G_BAR(); G_SCHED();
;     D_STAGE_B(G_SB(1, 1), 1, t3);
;     G_WAIT_V(6); G_BAR(); G_SCHED(); D_MMA(1, 1, At, B1); G_BAR(); G_SCHED();
;   }
	s_mov_b32 m0, s17
	s_nop 0
	buffer_load_dwordx4 v131, s[44:47], s37 offen lds
	s_nop 0
	s_mov_b32 m0, s19
	s_nop 0
	buffer_load_dwordx4 v136, s[44:47], s37 offen lds
	s_waitcnt vmcnt(10)
	s_barrier
	s_setprio 1
	v_mfma_f32_16x16x32_bf16 v[52:55], v[192:195], v[158:161], v[52:55]
	v_mfma_f32_16x16x32_bf16 v[48:51], v[200:203], v[158:161], v[48:51]
	v_mfma_f32_16x16x32_bf16 v[36:39], v[192:195], v[166:169], v[36:39]
	v_mfma_f32_16x16x32_bf16 v[32:35], v[200:203], v[166:169], v[32:35]
	v_mfma_f32_16x16x32_bf16 v[20:23], v[192:195], v[174:177], v[20:23]
	v_mfma_f32_16x16x32_bf16 v[16:19], v[200:203], v[174:177], v[16:19]
	v_mfma_f32_16x16x32_bf16 v[4:7], v[192:195], v[182:185], v[4:7]
	v_mfma_f32_16x16x32_bf16 v[0:3], v[200:203], v[182:185], v[0:3]
	v_mfma_f32_16x16x32_bf16 v[52:55], v[196:199], v[162:165], v[52:55]
	v_mfma_f32_16x16x32_bf16 v[48:51], v[204:207], v[162:165], v[48:51]
	v_mfma_f32_16x16x32_bf16 v[36:39], v[196:199], v[170:173], v[36:39]
	v_mfma_f32_16x16x32_bf16 v[32:35], v[204:207], v[170:173], v[32:35]
	v_mfma_f32_16x16x32_bf16 v[20:23], v[196:199], v[178:181], v[20:23]
	v_mfma_f32_16x16x32_bf16 v[16:19], v[204:207], v[178:181], v[16:19]
	v_mfma_f32_16x16x32_bf16 v[4:7], v[196:199], v[186:189], v[4:7]
	v_mfma_f32_16x16x32_bf16 v[0:3], v[204:207], v[186:189], v[0:3]
	s_setprio 0
	s_barrier
	ds_read_b128 v[142:145], v140
	ds_read_b128 v[146:149], v140 offset:1024
	ds_read_b128 v[150:153], v140 offset:2048
	ds_read_b128 v[154:157], v140 offset:3072
	ds_read_b128 v[158:161], v138 offset:32784
	ds_read_b128 v[162:165], v138 offset:33808
	ds_read_b128 v[166:169], v138 offset:34832
	ds_read_b128 v[170:173], v138 offset:35856
	ds_read_b128 v[174:177], v138 offset:36880
	ds_read_b128 v[178:181], v138 offset:37904
	ds_read_b128 v[182:185], v138 offset:38928
	ds_read_b128 v[186:189], v138 offset:39952
	s_mov_b32 m0, s20
	s_nop 0
	buffer_load_dwordx4 v129, s[0:3], s37 offen lds
	s_nop 0
	s_mov_b32 m0, s22
	s_nop 0
	buffer_load_dwordx4 v134, s[0:3], s37 offen lds
	s_waitcnt lgkmcnt(8)
	s_waitcnt vmcnt(10)
	s_barrier
	s_nop 0
	s_setprio 1
	s_waitcnt lgkmcnt(7)
	v_mfma_f32_16x16x32_bf16 v[124:127], v[142:145], v[158:161], v[124:127]
	v_mfma_f32_16x16x32_bf16 v[120:123], v[150:153], v[158:161], v[120:123]
	s_waitcnt lgkmcnt(5)
	v_mfma_f32_16x16x32_bf16 v[108:111], v[142:145], v[166:169], v[108:111]
	v_mfma_f32_16x16x32_bf16 v[104:107], v[150:153], v[166:169], v[104:107]
	s_waitcnt lgkmcnt(3)
	v_mfma_f32_16x16x32_bf16 v[92:95], v[142:145], v[174:177], v[92:95]
	v_mfma_f32_16x16x32_bf16 v[88:91], v[150:153], v[174:177], v[88:91]
	s_waitcnt lgkmcnt(1)
	v_mfma_f32_16x16x32_bf16 v[76:79], v[142:145], v[182:185], v[76:79]
	v_mfma_f32_16x16x32_bf16 v[72:75], v[150:153], v[182:185], v[72:75]
	v_mfma_f32_16x16x32_bf16 v[124:127], v[146:149], v[162:165], v[124:127]
	v_mfma_f32_16x16x32_bf16 v[120:123], v[154:157], v[162:165], v[120:123]
	v_mfma_f32_16x16x32_bf16 v[108:111], v[146:149], v[170:173], v[108:111]
	v_mfma_f32_16x16x32_bf16 v[104:107], v[154:157], v[170:173], v[104:107]
	v_mfma_f32_16x16x32_bf16 v[92:95], v[146:149], v[178:181], v[92:95]
	v_mfma_f32_16x16x32_bf16 v[88:91], v[154:157], v[178:181], v[88:91]
	s_waitcnt lgkmcnt(0)
	v_mfma_f32_16x16x32_bf16 v[76:79], v[146:149], v[186:189], v[76:79]
	v_mfma_f32_16x16x32_bf16 v[72:75], v[154:157], v[186:189], v[72:75]
	s_setprio 0
	s_barrier
	ds_read_b128 v[192:195], v141
	ds_read_b128 v[196:199], v141 offset:1024
	ds_read_b128 v[200:203], v141 offset:2048
	ds_read_b128 v[204:207], v141 offset:3072
	s_mov_b32 m0, s23
	s_nop 0
	buffer_load_dwordx4 v130, s[44:47], s35 offen lds
	s_nop 0
	s_mov_b32 m0, s24
	s_nop 0
	buffer_load_dwordx4 v135, s[44:47], s35 offen lds
	s_waitcnt vmcnt(10)
	s_barrier
; #define G_WAIT_V(n) asm volatile("s_waitcnt vmcnt(" #n ")" ::: "memory")
; #define G_BAR() __builtin_amdgcn_s_barrier()
; #define G_SCHED() __builtin_amdgcn_sched_barrier(0)
; #define D_STAGE_A(slot, half, kt) D_STAGE(rsA, voffA, slot, half, kt)
; #define D_STAGE_B(slot, half, kt) D_STAGE(rsB, voffB, slot, half, kt)
; #define D_LDA(dst, slot) do { _Pragma("unroll") for (int m = 0; m < 4; ++m) _Pragma("unroll") for (int k = 0; k < 2; ++k) \
;     dst[m][k] = *(const LDS_AS bf16x8*)(lds + (slot) + aoff + m * 2048 + k * 1024); } while (0)
; #define D_LDB(dst, slot) do { _Pragma("unroll") for (int n = 0; n < 2; ++n) _Pragma("unroll") for (int k = 0; k < 2; ++k) \
;     dst[n][k] = *(const LDS_AS bf16x8*)(lds + (slot) + boff + n * 2048 + k * 1024); } while (0)
; #define D_WAIT_L(n) asm volatile("s_waitcnt lgkmcnt(" #n ")" ::: "memory")
; #define D_STAGE_A(slot, half, kt) D_STAGE(rsA, voffA, slot, half, kt)
; template <class Cfg>
; DI void gemm256dma_unit(LDS_AS unsigned char* lds, const Cfg& cfg) {
;     ...
;   for (int t = 0; t < nt; t += 2) {
;     const int t1 = t + 1;
;     const int t2 = (t + 2 < nt) ? t + 2 : 0;
;     const int t3 = (t + 2 < nt) ? t + 3 : 1;
;     D_LDB(B0, G_SB(0, 0)); G_SCHED(); D_LDA(At, G_SA(0, 0)); D_STAGE_A(G_SA(1, 1), 1, t1);
;     D_WAIT_L(8); G_BAR(); D_WAIT_L(0); G_SCHED(); D_MMA(0, 0, At, B0); G_BAR(); G_SCHED();
;     D_LDB(B1, G_SB(0, 1)); D_STAGE_B(G_SB(0, 0), 0, t2);
;     G_BAR(); D_WAIT_L(0); G_SCHED(); D_MMA(0, 1, At, B1); G_BAR(); G_SCHED();
;     D_LDA(At, G_SA(0, 1)); D_STAGE_A(G_SA(0, 0), 0, t2);
;     G_BAR(); D_WAIT_L(0); G_SCHED(); D_MMA(1, 0, At, B0); G_BAR(); G_SCHED();
;     D_STAGE_B(G_SB(0, 1), 1, t2);
;     G_WAIT_V(6); G_BAR(); G_SCHED(); D_MMA(1, 1, At, B1); G_BAR(); G_SCHED();
;     D_LDB(B0, G_SB(1, 0)); G_SCHED(); D_LDA(At, G_SA(1, 0)); D_STAGE_A(G_SA(0, 1), 1, t2);
;     D_WAIT_L(8); G_BAR(); D_WAIT_L(0); G_SCHED(); D_MMA(0, 0, At, B0); G_BAR(); G_SCHED();
;     D_LDB(B1, G_SB(1, 1)); D_STAGE_B(G_SB(1, 0), 0, t3);
;     G_BAR(); D_WAIT_L(0); G_SCHED(); D_MMA(0, 1, At, B1); G_BAR(); G_SCHED();
;     D_LDA(At, G_SA(1, 1)); D_STAGE_A(G_SA(1, 0), 0, t3);
;     G_BAR(); D_WAIT_L(0); G_SCHED(); D_MMA(1, 0, At, B0); G_BAR(); G_SCHED();
;     D_STAGE_B(G_SB(1, 1), 1, t3);
;     G_WAIT_V(6); G_BAR(); G_SCHED(); D_MMA(1, 1, At, B1); G_BAR(); G_SCHED();
;   }
	s_nop 0
	s_setprio 1
	s_waitcnt lgkmcnt(3)
	v_mfma_f32_16x16x32_bf16 v[116:119], v[192:195], v[158:161], v[116:119]
	s_waitcnt lgkmcnt(1)
	v_mfma_f32_16x16x32_bf16 v[112:115], v[200:203], v[158:161], v[112:115]
	v_mfma_f32_16x16x32_bf16 v[100:103], v[192:195], v[166:169], v[100:103]
	v_mfma_f32_16x16x32_bf16 v[96:99], v[200:203], v[166:169], v[96:99]
	v_mfma_f32_16x16x32_bf16 v[84:87], v[192:195], v[174:177], v[84:87]
	v_mfma_f32_16x16x32_bf16 v[80:83], v[200:203], v[174:177], v[80:83]
	v_mfma_f32_16x16x32_bf16 v[68:71], v[192:195], v[182:185], v[68:71]
	v_mfma_f32_16x16x32_bf16 v[64:67], v[200:203], v[182:185], v[64:67]
	v_mfma_f32_16x16x32_bf16 v[116:119], v[196:199], v[162:165], v[116:119]
	s_waitcnt lgkmcnt(0)
	v_mfma_f32_16x16x32_bf16 v[112:115], v[204:207], v[162:165], v[112:115]
	v_mfma_f32_16x16x32_bf16 v[100:103], v[196:199], v[170:173], v[100:103]
	v_mfma_f32_16x16x32_bf16 v[96:99], v[204:207], v[170:173], v[96:99]
	v_mfma_f32_16x16x32_bf16 v[84:87], v[196:199], v[178:181], v[84:87]
	v_mfma_f32_16x16x32_bf16 v[80:83], v[204:207], v[178:181], v[80:83]
	v_mfma_f32_16x16x32_bf16 v[68:71], v[196:199], v[186:189], v[68:71]
	v_mfma_f32_16x16x32_bf16 v[64:67], v[204:207], v[186:189], v[64:67]
	s_setprio 0
	s_barrier
	ds_read_b128 v[158:161], v138 offset:49168
	ds_read_b128 v[162:165], v138 offset:50192
	ds_read_b128 v[166:169], v138 offset:51216
	ds_read_b128 v[170:173], v138 offset:52240
	ds_read_b128 v[174:177], v138 offset:53264
	ds_read_b128 v[178:181], v138 offset:54288
	ds_read_b128 v[182:185], v138 offset:55312
	ds_read_b128 v[186:189], v138 offset:56336
	s_mov_b32 m0, s25
	s_nop 0
	buffer_load_dwordx4 v128, s[0:3], s35 offen lds
	s_nop 0
	s_mov_b32 m0, s26
	s_nop 0
	buffer_load_dwordx4 v133, s[0:3], s35 offen lds
	s_barrier
	s_nop 0
	s_setprio 1
	s_waitcnt lgkmcnt(7)
	v_mfma_f32_16x16x32_bf16 v[60:63], v[142:145], v[158:161], v[60:63]
	v_mfma_f32_16x16x32_bf16 v[56:59], v[150:153], v[158:161], v[56:59]
	s_waitcnt lgkmcnt(5)
	v_mfma_f32_16x16x32_bf16 v[44:47], v[142:145], v[166:169], v[44:47]
	v_mfma_f32_16x16x32_bf16 v[40:43], v[150:153], v[166:169], v[40:43]
	s_waitcnt lgkmcnt(3)
	v_mfma_f32_16x16x32_bf16 v[28:31], v[142:145], v[174:177], v[28:31]
	v_mfma_f32_16x16x32_bf16 v[24:27], v[150:153], v[174:177], v[24:27]
	s_waitcnt lgkmcnt(1)
	v_mfma_f32_16x16x32_bf16 v[12:15], v[142:145], v[182:185], v[12:15]
	v_mfma_f32_16x16x32_bf16 v[8:11], v[150:153], v[182:185], v[8:11]
	v_mfma_f32_16x16x32_bf16 v[60:63], v[146:149], v[162:165], v[60:63]
	v_mfma_f32_16x16x32_bf16 v[56:59], v[154:157], v[162:165], v[56:59]
	v_mfma_f32_16x16x32_bf16 v[44:47], v[146:149], v[170:173], v[44:47]
	v_mfma_f32_16x16x32_bf16 v[40:43], v[154:157], v[170:173], v[40:43]
	v_mfma_f32_16x16x32_bf16 v[28:31], v[146:149], v[178:181], v[28:31]
	v_mfma_f32_16x16x32_bf16 v[24:27], v[154:157], v[178:181], v[24:27]
	s_waitcnt lgkmcnt(0)
	v_mfma_f32_16x16x32_bf16 v[12:15], v[146:149], v[186:189], v[12:15]
	v_mfma_f32_16x16x32_bf16 v[8:11], v[154:157], v[186:189], v[8:11]
	s_setprio 0
	s_barrier
	s_mov_b32 m0, s27
	s_nop 0
	buffer_load_dwordx4 v131, s[44:47], s35 offen lds
	s_nop 0
	s_mov_b32 m0, s28
	s_nop 0
	buffer_load_dwordx4 v136, s[44:47], s35 offen lds
	s_waitcnt vmcnt(10)
	s_barrier
	s_setprio 1
	v_mfma_f32_16x16x32_bf16 v[52:55], v[192:195], v[158:161], v[52:55]
	v_mfma_f32_16x16x32_bf16 v[48:51], v[200:203], v[158:161], v[48:51]
	v_mfma_f32_16x16x32_bf16 v[36:39], v[192:195], v[166:169], v[36:39]
	v_mfma_f32_16x16x32_bf16 v[32:35], v[200:203], v[166:169], v[32:35]
	v_mfma_f32_16x16x32_bf16 v[20:23], v[192:195], v[174:177], v[20:23]
	v_mfma_f32_16x16x32_bf16 v[16:19], v[200:203], v[174:177], v[16:19]
	v_mfma_f32_16x16x32_bf16 v[4:7], v[192:195], v[182:185], v[4:7]
	v_mfma_f32_16x16x32_bf16 v[0:3], v[200:203], v[182:185], v[0:3]
	v_mfma_f32_16x16x32_bf16 v[52:55], v[196:199], v[162:165], v[52:55]
	v_mfma_f32_16x16x32_bf16 v[48:51], v[204:207], v[162:165], v[48:51]
	v_mfma_f32_16x16x32_bf16 v[36:39], v[196:199], v[170:173], v[36:39]
	v_mfma_f32_16x16x32_bf16 v[32:35], v[204:207], v[170:173], v[32:35]
	v_mfma_f32_16x16x32_bf16 v[20:23], v[196:199], v[178:181], v[20:23]
	v_mfma_f32_16x16x32_bf16 v[16:19], v[204:207], v[178:181], v[16:19]
	v_mfma_f32_16x16x32_bf16 v[4:7], v[196:199], v[186:189], v[4:7]
	v_mfma_f32_16x16x32_bf16 v[0:3], v[204:207], v[186:189], v[0:3]
	s_setprio 0
	s_barrier
	s_mov_b32 s33, s34
	s_cbranch_scc0 .LBB0_1266
	s_waitcnt vmcnt(0)
	s_cmpk_lt_u32 s12, 0x100
	s_cbranch_scc0 .LBB0_1262
	s_barrier
	s_branch .LBB0_1262

; #define G_WAIT_V(n) asm volatile("s_waitcnt vmcnt(" #n ")" ::: "memory")
; #define G_BAR() __builtin_amdgcn_s_barrier()
; #define G_SCHED() __builtin_amdgcn_sched_barrier(0)
; #define D_STAGE_A(slot, half, kt) D_STAGE(rsA, voffA, slot, half, kt)
; #define D_STAGE_B(slot, half, kt) D_STAGE(rsB, voffB, slot, half, kt)
; #define D_LDA(dst, slot) do { _Pragma("unroll") for (int m = 0; m < 4; ++m) _Pragma("unroll") for (int k = 0; k < 2; ++k) \
;     dst[m][k] = *(const LDS_AS bf16x8*)(lds + (slot) + aoff + m * 2048 + k * 1024); } while (0)
; #define D_LDB(dst, slot) do { _Pragma("unroll") for (int n = 0; n < 2; ++n) _Pragma("unroll") for (int k = 0; k < 2; ++k) \
;     dst[n][k] = *(const LDS_AS bf16x8*)(lds + (slot) + boff + n * 2048 + k * 1024); } while (0)
; #define D_WAIT_L(n) asm volatile("s_waitcnt lgkmcnt(" #n ")" ::: "memory")
; #define D_STAGE_A(slot, half, kt) D_STAGE(rsA, voffA, slot, half, kt)
; #define D_WAIT_L(n) asm volatile("s_waitcnt lgkmcnt(" #n ")" ::: "memory")
;     ...
;   for (int t = 0; t < (F8_PEEL ? nt - 2 : nt); t += 2) {
;     const int t1 = t + 1;
;     const int t2 = (F8_PEEL || t + 2 < nt) ? t + 2 : t;
;     const int t3 = (F8_PEEL || t + 2 < nt) ? t + 3 : t + 1;
;     D_LDB(B0, G_SB(0, 0)); G_SCHED(); D_LDA(At, G_SA(0, 0)); D_STAGE_A(G_SA(1, 1), 1, t1);
;     D_WAIT_L(8); G_BAR(); D_WAIT_L(0); G_SCHED(); D_MMA(0, 0, At, B0); G_BAR(); G_SCHED();
;     D_LDB(B1, G_SB(0, 1)); D_STAGE_B(G_SB(0, 0), 0, t2);
;     G_BAR(); D_WAIT_L(0); G_SCHED(); D_MMA(0, 1, At, B1); G_BAR(); G_SCHED();
;     D_LDA(At, G_SA(0, 1)); D_STAGE_A(G_SA(0, 0), 0, t2);
;     G_BAR(); D_WAIT_L(0); G_SCHED(); D_MMA(1, 0, At, B0); G_BAR(); G_SCHED();
;     D_STAGE_B(G_SB(0, 1), 1, t2);
;     G_WAIT_V(6); G_BAR(); G_SCHED(); D_MMA(1, 1, At, B1); G_BAR(); G_SCHED();
;     D_LDB(B0, G_SB(1, 0)); G_SCHED(); D_LDA(At, G_SA(1, 0)); D_STAGE_A(G_SA(0, 1), 1, t2);
;     D_WAIT_L(8); G_BAR(); D_WAIT_L(0); G_SCHED(); D_MMA(0, 0, At, B0); G_BAR(); G_SCHED();
;     D_LDB(B1, G_SB(1, 1)); D_STAGE_B(G_SB(1, 0), 0, t3);
;     G_BAR(); D_WAIT_L(0); G_SCHED(); D_MMA(0, 1, At, B1); G_BAR(); G_SCHED();
;     D_LDA(At, G_SA(1, 1)); D_STAGE_A(G_SA(1, 0), 0, t3);
;     G_BAR(); D_WAIT_L(0); G_SCHED(); D_MMA(1, 0, At, B0); G_BAR(); G_SCHED();
;     D_STAGE_B(G_SB(1, 1), 1, t3);
;     G_WAIT_V(6); G_BAR(); G_SCHED(); D_MMA(1, 1, At, B1); G_BAR(); G_SCHED();
;   }
.LBB0_1415:
	s_add_i32 s82, 0, 0x10010
	v_add_u32_e32 v72, s82, v125
	v_add_u32_e32 v73, s82, v126
	ds_read_b128 v[152:155], v72
	ds_read_b128 v[160:163], v72 offset:2048
	ds_read_b128 v[156:159], v73
	ds_read_b128 v[164:167], v73 offset:2048
	s_add_i32 s38, s79, 1
	s_add_i32 s80, s79, 3
	s_add_i32 s78, s79, 2
	s_add_i32 s96, 0, 0x14010
	s_cmp_lt_u32 s79, 14
	s_cselect_b32 s81, s78, s79
	s_cselect_b32 s38, s80, s38
	s_lshl_b32 s86, s81, 7
	s_lshl_b32 s81, s38, 7
	s_add_i32 s97, s86, 0x20000
	s_add_i32 s91, s86, 0x2000
	s_add_i32 s90, s86, 0x22000
	s_add_i32 s87, 0, 0x18010
	s_add_i32 s85, 0, 0x1c010
	s_add_i32 s84, s81, 0x20000
	s_add_i32 s83, s81, 0x2000
	s_add_i32 s82, s81, 0x22000
	s_add_i32 s80, s77, 0x100
	s_cmp_gt_u32 s79, 13
	ds_read_b128 v[168:171], v127 offset:16
	ds_read_b128 v[176:179], v127 offset:2064
	ds_read_b128 v[172:175], v128 offset:16
	ds_read_b128 v[180:183], v128 offset:2064
	ds_read_b128 v[192:195], v127 offset:4112
	ds_read_b128 v[200:203], v127 offset:6160
	ds_read_b128 v[196:199], v128 offset:4112
	ds_read_b128 v[204:207], v128 offset:6160
	s_mov_b32 m0, s75
	s_nop 0
	buffer_load_dwordx4 v121, s[8:11], s77 offen lds
	s_nop 0
	s_mov_b32 m0, s76
	s_nop 0
	buffer_load_dwordx4 v124, s[8:11], s77 offen lds
	s_waitcnt lgkmcnt(8)
	s_waitcnt vmcnt(10)
	s_barrier
	s_nop 0
	s_setprio 1
	s_waitcnt lgkmcnt(5)
	v_mfma_scale_f32_16x16x128_f8f6f4 v[134:137], v[160:167], v[168:175], v[136:139], v149, v148 op_sel_hi:[0,0,0]
	s_waitcnt lgkmcnt(0)
	v_mfma_scale_f32_16x16x128_f8f6f4 v[212:215], v[152:159], v[200:207], v[212:215], v149, v148 op_sel_hi:[0,0,0]
	v_mfma_scale_f32_16x16x128_f8f6f4 v[216:219], v[160:167], v[200:207], v[216:219], v149, v148 op_sel_hi:[0,0,0]
	v_mfma_scale_f32_16x16x128_f8f6f4 v[130:133], v[152:159], v[168:175], v[140:143], v149, v148 op_sel_hi:[0,0,0]
	v_mfma_scale_f32_16x16x128_f8f6f4 v[144:147], v[152:159], v[176:183], v[108:111], v149, v148 op_sel_hi:[0,0,0]
	v_mfma_scale_f32_16x16x128_f8f6f4 v[184:187], v[160:167], v[176:183], v[104:107], v149, v148 op_sel_hi:[0,0,0]
	v_mfma_scale_f32_16x16x128_f8f6f4 v[188:191], v[152:159], v[192:199], v[92:95], v149, v148 op_sel_hi:[0,0,0]
	v_mfma_scale_f32_16x16x128_f8f6f4 v[208:211], v[160:167], v[192:199], v[88:91], v149, v148 op_sel_hi:[0,0,0]
	s_setprio 0
	s_barrier
	v_add_u32_e32 v76, s96, v125
	v_add_u32_e32 v80, s96, v126
	ds_read_b128 v[72:75], v76
	s_nop 1
	ds_read_b128 v[88:91], v76 offset:2048
	ds_read_b128 v[76:79], v80
	ds_read_b128 v[92:95], v80 offset:2048
	s_mov_b32 m0, s23
	s_nop 0
	buffer_load_dwordx4 v122, s[4:7], s86 offen lds
	s_nop 0
	s_mov_b32 m0, s39
	s_nop 0
	buffer_load_dwordx4 v122, s[4:7], s97 offen lds
	s_waitcnt vmcnt(10)
	s_barrier
	s_nop 0
	s_setprio 1
	s_waitcnt lgkmcnt(1)
	v_mfma_scale_f32_16x16x128_f8f6f4 v[68:71], v[72:79], v[200:207], v[68:71], v149, v148 op_sel_hi:[0,0,0]
	s_waitcnt lgkmcnt(0)
	v_mfma_scale_f32_16x16x128_f8f6f4 v[56:59], v[88:95], v[200:207], v[56:59], v149, v148 op_sel_hi:[0,0,0]
	v_mfma_scale_f32_16x16x128_f8f6f4 v[220:223], v[72:79], v[168:175], v[116:119], v149, v148 op_sel_hi:[0,0,0]
	v_mfma_scale_f32_16x16x128_f8f6f4 v[168:171], v[88:95], v[168:175], v[112:115], v149, v148 op_sel_hi:[0,0,0]
	v_mfma_scale_f32_16x16x128_f8f6f4 v[172:175], v[72:79], v[176:183], v[100:103], v149, v148 op_sel_hi:[0,0,0]
	v_mfma_scale_f32_16x16x128_f8f6f4 v[176:179], v[88:95], v[176:183], v[96:99], v149, v148 op_sel_hi:[0,0,0]
	v_mfma_scale_f32_16x16x128_f8f6f4 v[180:183], v[72:79], v[192:199], v[84:87], v149, v148 op_sel_hi:[0,0,0]
	v_mfma_scale_f32_16x16x128_f8f6f4 v[192:195], v[88:95], v[192:199], v[8:11], v149, v148 op_sel_hi:[0,0,0]
	s_setprio 0
	s_barrier
	ds_read_b128 v[80:83], v127 offset:16400
	s_nop 1
	ds_read_b128 v[96:99], v127 offset:18448
	ds_read_b128 v[84:87], v128 offset:16400
	ds_read_b128 v[100:103], v128 offset:18448
	ds_read_b128 v[104:107], v127 offset:20496
	ds_read_b128 v[112:115], v127 offset:22544
	ds_read_b128 v[108:111], v128 offset:20496
	ds_read_b128 v[116:119], v128 offset:22544
	s_mov_b32 m0, s61
	s_nop 0
	buffer_load_dwordx4 v120, s[8:11], s86 offen lds
	s_nop 0
	s_mov_b32 m0, s62
	s_nop 0
	buffer_load_dwordx4 v123, s[8:11], s86 offen lds
	s_barrier
	s_nop 0
	s_setprio 1
	s_waitcnt lgkmcnt(5)
	v_mfma_scale_f32_16x16x128_f8f6f4 v[64:67], v[152:159], v[80:87], v[64:67], v149, v148 op_sel_hi:[0,0,0]
	v_mfma_scale_f32_16x16x128_f8f6f4 v[60:63], v[160:167], v[80:87], v[60:63], v149, v148 op_sel_hi:[0,0,0]
	s_waitcnt lgkmcnt(0)
	v_mfma_scale_f32_16x16x128_f8f6f4 v[236:239], v[160:167], v[112:119], v[236:239], v149, v148 op_sel_hi:[0,0,0]
	v_mfma_scale_f32_16x16x128_f8f6f4 v[200:203], v[152:159], v[96:103], v[44:47], v149, v148 op_sel_hi:[0,0,0]
	v_mfma_scale_f32_16x16x128_f8f6f4 v[204:207], v[160:167], v[96:103], v[40:43], v149, v148 op_sel_hi:[0,0,0]
	v_mfma_scale_f32_16x16x128_f8f6f4 v[224:227], v[152:159], v[104:111], v[28:31], v149, v148 op_sel_hi:[0,0,0]
	v_mfma_scale_f32_16x16x128_f8f6f4 v[228:231], v[160:167], v[104:111], v[24:27], v149, v148 op_sel_hi:[0,0,0]
	v_mfma_scale_f32_16x16x128_f8f6f4 v[232:235], v[152:159], v[112:119], v[12:15], v149, v148 op_sel_hi:[0,0,0]
	s_setprio 0
	s_barrier
	s_mov_b32 m0, s63
	s_nop 0
	buffer_load_dwordx4 v122, s[4:7], s91 offen lds
	s_nop 0
	s_mov_b32 m0, s66
	s_nop 0
	buffer_load_dwordx4 v122, s[4:7], s90 offen lds
	s_waitcnt vmcnt(10)
	s_barrier
; #define G_WAIT_V(n) asm volatile("s_waitcnt vmcnt(" #n ")" ::: "memory")
; #define G_BAR() __builtin_amdgcn_s_barrier()
; #define G_SCHED() __builtin_amdgcn_sched_barrier(0)
; #define D_STAGE_A(slot, half, kt) D_STAGE(rsA, voffA, slot, half, kt)
; #define D_STAGE_B(slot, half, kt) D_STAGE(rsB, voffB, slot, half, kt)
; #define D_LDA(dst, slot) do { _Pragma("unroll") for (int m = 0; m < 4; ++m) _Pragma("unroll") for (int k = 0; k < 2; ++k) \
;     dst[m][k] = *(const LDS_AS bf16x8*)(lds + (slot) + aoff + m * 2048 + k * 1024); } while (0)
; #define D_LDB(dst, slot) do { _Pragma("unroll") for (int n = 0; n < 2; ++n) _Pragma("unroll") for (int k = 0; k < 2; ++k) \
;     dst[n][k] = *(const LDS_AS bf16x8*)(lds + (slot) + boff + n * 2048 + k * 1024); } while (0)
; #define D_WAIT_L(n) asm volatile("s_waitcnt lgkmcnt(" #n ")" ::: "memory")
; #define D_STAGE_A(slot, half, kt) D_STAGE(rsA, voffA, slot, half, kt)
; #define D_WAIT_L(n) asm volatile("s_waitcnt lgkmcnt(" #n ")" ::: "memory")
;     ...
;   for (int t = 0; t < (F8_PEEL ? nt - 2 : nt); t += 2) {
;     const int t1 = t + 1;
;     const int t2 = (F8_PEEL || t + 2 < nt) ? t + 2 : t;
;     const int t3 = (F8_PEEL || t + 2 < nt) ? t + 3 : t + 1;
;     D_LDB(B0, G_SB(0, 0)); G_SCHED(); D_LDA(At, G_SA(0, 0)); D_STAGE_A(G_SA(1, 1), 1, t1);
;     D_WAIT_L(8); G_BAR(); D_WAIT_L(0); G_SCHED(); D_MMA(0, 0, At, B0); G_BAR(); G_SCHED();
;     D_LDB(B1, G_SB(0, 1)); D_STAGE_B(G_SB(0, 0), 0, t2);
;     G_BAR(); D_WAIT_L(0); G_SCHED(); D_MMA(0, 1, At, B1); G_BAR(); G_SCHED();
;     D_LDA(At, G_SA(0, 1)); D_STAGE_A(G_SA(0, 0), 0, t2);
;     G_BAR(); D_WAIT_L(0); G_SCHED(); D_MMA(1, 0, At, B0); G_BAR(); G_SCHED();
;     D_STAGE_B(G_SB(0, 1), 1, t2);
;     G_WAIT_V(6); G_BAR(); G_SCHED(); D_MMA(1, 1, At, B1); G_BAR(); G_SCHED();
;     D_LDB(B0, G_SB(1, 0)); G_SCHED(); D_LDA(At, G_SA(1, 0)); D_STAGE_A(G_SA(0, 1), 1, t2);
;     D_WAIT_L(8); G_BAR(); D_WAIT_L(0); G_SCHED(); D_MMA(0, 0, At, B0); G_BAR(); G_SCHED();
;     D_LDB(B1, G_SB(1, 1)); D_STAGE_B(G_SB(1, 0), 0, t3);
;     G_BAR(); D_WAIT_L(0); G_SCHED(); D_MMA(0, 1, At, B1); G_BAR(); G_SCHED();
;     D_LDA(At, G_SA(1, 1)); D_STAGE_A(G_SA(1, 0), 0, t3);
;     G_BAR(); D_WAIT_L(0); G_SCHED(); D_MMA(1, 0, At, B0); G_BAR(); G_SCHED();
;     D_STAGE_B(G_SB(1, 1), 1, t3);
;     G_WAIT_V(6); G_BAR(); G_SCHED(); D_MMA(1, 1, At, B1); G_BAR(); G_SCHED();
;   }
	s_setprio 1
	v_mfma_scale_f32_16x16x128_f8f6f4 v[52:55], v[72:79], v[80:87], v[52:55], v149, v148 op_sel_hi:[0,0,0]
	v_mfma_scale_f32_16x16x128_f8f6f4 v[48:51], v[88:95], v[80:87], v[48:51], v149, v148 op_sel_hi:[0,0,0]
	v_mfma_scale_f32_16x16x128_f8f6f4 v[240:243], v[72:79], v[96:103], v[36:39], v149, v148 op_sel_hi:[0,0,0]
	v_mfma_scale_f32_16x16x128_f8f6f4 v[244:247], v[88:95], v[96:103], v[32:35], v149, v148 op_sel_hi:[0,0,0]
	v_mfma_scale_f32_16x16x128_f8f6f4 v[248:251], v[72:79], v[104:111], v[20:23], v149, v148 op_sel_hi:[0,0,0]
	v_mfma_scale_f32_16x16x128_f8f6f4 v[80:83], v[88:95], v[104:111], v[16:19], v149, v148 op_sel_hi:[0,0,0]
	v_mfma_scale_f32_16x16x128_f8f6f4 v[72:75], v[72:79], v[112:119], v[4:7], v149, v148 op_sel_hi:[0,0,0]
	v_mfma_scale_f32_16x16x128_f8f6f4 v[76:79], v[88:95], v[112:119], v[0:3], v149, v148 op_sel_hi:[0,0,0]
	s_setprio 0
	s_barrier
	s_nop 3
	v_add_u32_e32 v4, s87, v125
	v_add_u32_e32 v8, s87, v126
	ds_read_b128 v[0:3], v4
	ds_read_b128 v[16:19], v4 offset:2048
	ds_read_b128 v[4:7], v8
	ds_read_b128 v[20:23], v8 offset:2048
	ds_read_b128 v[8:11], v127 offset:32784
	ds_read_b128 v[24:27], v127 offset:34832
	ds_read_b128 v[12:15], v128 offset:32784
	ds_read_b128 v[28:31], v128 offset:34832
	ds_read_b128 v[32:35], v127 offset:36880
	ds_read_b128 v[40:43], v127 offset:38928
	ds_read_b128 v[36:39], v128 offset:36880
	ds_read_b128 v[44:47], v128 offset:38928
	s_mov_b32 m0, s67
	s_nop 0
	buffer_load_dwordx4 v121, s[8:11], s86 offen lds
	s_nop 0
	s_mov_b32 m0, s68
	s_nop 0
	buffer_load_dwordx4 v124, s[8:11], s86 offen lds
	s_waitcnt lgkmcnt(8)
	s_waitcnt vmcnt(10)
	s_barrier
	s_nop 0
	s_setprio 1
	s_waitcnt lgkmcnt(5)
	v_mfma_scale_f32_16x16x128_f8f6f4 v[140:143], v[0:7], v[8:15], v[130:133], v149, v148 op_sel_hi:[0,0,0]
	v_mfma_scale_f32_16x16x128_f8f6f4 v[136:139], v[16:23], v[8:15], v[134:137], v149, v148 op_sel_hi:[0,0,0]
	s_waitcnt lgkmcnt(4)
	v_mfma_scale_f32_16x16x128_f8f6f4 v[108:111], v[0:7], v[24:31], v[144:147], v149, v148 op_sel_hi:[0,0,0]
	v_mfma_scale_f32_16x16x128_f8f6f4 v[104:107], v[16:23], v[24:31], v[184:187], v149, v148 op_sel_hi:[0,0,0]
	s_waitcnt lgkmcnt(1)
	v_mfma_scale_f32_16x16x128_f8f6f4 v[92:95], v[0:7], v[32:39], v[188:191], v149, v148 op_sel_hi:[0,0,0]
	v_mfma_scale_f32_16x16x128_f8f6f4 v[88:91], v[16:23], v[32:39], v[208:211], v149, v148 op_sel_hi:[0,0,0]
	s_waitcnt lgkmcnt(0)
	v_mfma_scale_f32_16x16x128_f8f6f4 v[212:215], v[0:7], v[40:47], v[212:215], v149, v148 op_sel_hi:[0,0,0]
	v_mfma_scale_f32_16x16x128_f8f6f4 v[216:219], v[16:23], v[40:47], v[216:219], v149, v148 op_sel_hi:[0,0,0]
	s_setprio 0
	s_barrier
	v_add_u32_e32 v84, s85, v125
	v_add_u32_e32 v85, s85, v126
	ds_read_b128 v[152:155], v84
	ds_read_b128 v[160:163], v84 offset:2048
	ds_read_b128 v[156:159], v85
	ds_read_b128 v[164:167], v85 offset:2048
	s_mov_b32 m0, s69
	s_nop 0
	buffer_load_dwordx4 v122, s[4:7], s81 offen lds
	s_nop 0
	s_mov_b32 m0, s70
	s_nop 0
	buffer_load_dwordx4 v122, s[4:7], s84 offen lds
	s_waitcnt vmcnt(10)
	s_barrier
	s_nop 0
	s_setprio 1
	s_waitcnt lgkmcnt(1)
	v_mfma_scale_f32_16x16x128_f8f6f4 v[116:119], v[152:159], v[8:15], v[220:223], v149, v148 op_sel_hi:[0,0,0]
	s_waitcnt lgkmcnt(0)
	v_mfma_scale_f32_16x16x128_f8f6f4 v[112:115], v[160:167], v[8:15], v[168:171], v149, v148 op_sel_hi:[0,0,0]
	v_mfma_scale_f32_16x16x128_f8f6f4 v[100:103], v[152:159], v[24:31], v[172:175], v149, v148 op_sel_hi:[0,0,0]
	v_mfma_scale_f32_16x16x128_f8f6f4 v[96:99], v[160:167], v[24:31], v[176:179], v149, v148 op_sel_hi:[0,0,0]
	v_mfma_scale_f32_16x16x128_f8f6f4 v[84:87], v[152:159], v[32:39], v[180:183], v149, v148 op_sel_hi:[0,0,0]
	v_mfma_scale_f32_16x16x128_f8f6f4 v[8:11], v[160:167], v[32:39], v[192:195], v149, v148 op_sel_hi:[0,0,0]
	v_mfma_scale_f32_16x16x128_f8f6f4 v[68:71], v[152:159], v[40:47], v[68:71], v149, v148 op_sel_hi:[0,0,0]
	v_mfma_scale_f32_16x16x128_f8f6f4 v[56:59], v[160:167], v[40:47], v[56:59], v149, v148 op_sel_hi:[0,0,0]
	s_setprio 0
	s_barrier
	ds_read_b128 v[32:35], v127 offset:49168
	ds_read_b128 v[168:171], v127 offset:51216
	ds_read_b128 v[36:39], v128 offset:49168
	ds_read_b128 v[172:175], v128 offset:51216
	ds_read_b128 v[176:179], v127 offset:53264
	ds_read_b128 v[192:195], v127 offset:55312
	ds_read_b128 v[180:183], v128 offset:53264
	ds_read_b128 v[196:199], v128 offset:55312
	s_mov_b32 m0, s71
	s_nop 0
	buffer_load_dwordx4 v120, s[8:11], s81 offen lds
	s_nop 0
	s_mov_b32 m0, s72
	s_nop 0
	buffer_load_dwordx4 v123, s[8:11], s81 offen lds
	s_barrier
	s_nop 0
	s_setprio 1
	s_waitcnt lgkmcnt(5)
	v_mfma_scale_f32_16x16x128_f8f6f4 v[64:67], v[0:7], v[32:39], v[64:67], v149, v148 op_sel_hi:[0,0,0]
	v_mfma_scale_f32_16x16x128_f8f6f4 v[60:63], v[16:23], v[32:39], v[60:63], v149, v148 op_sel_hi:[0,0,0]
	s_waitcnt lgkmcnt(4)
	v_mfma_scale_f32_16x16x128_f8f6f4 v[44:47], v[0:7], v[168:175], v[200:203], v149, v148 op_sel_hi:[0,0,0]
	v_mfma_scale_f32_16x16x128_f8f6f4 v[40:43], v[16:23], v[168:175], v[204:207], v149, v148 op_sel_hi:[0,0,0]
	s_waitcnt lgkmcnt(1)
	v_mfma_scale_f32_16x16x128_f8f6f4 v[28:31], v[0:7], v[176:183], v[224:227], v149, v148 op_sel_hi:[0,0,0]
	v_mfma_scale_f32_16x16x128_f8f6f4 v[24:27], v[16:23], v[176:183], v[228:231], v149, v148 op_sel_hi:[0,0,0]
	s_waitcnt lgkmcnt(0)
	v_mfma_scale_f32_16x16x128_f8f6f4 v[12:15], v[0:7], v[192:199], v[232:235], v149, v148 op_sel_hi:[0,0,0]
	v_mfma_scale_f32_16x16x128_f8f6f4 v[236:239], v[16:23], v[192:199], v[236:239], v149, v148 op_sel_hi:[0,0,0]
	s_setprio 0
	s_barrier
	s_mov_b32 m0, s73
	s_nop 0
	buffer_load_dwordx4 v122, s[4:7], s83 offen lds
	s_nop 0
	s_mov_b32 m0, s74
	s_nop 0
	buffer_load_dwordx4 v122, s[4:7], s82 offen lds
	s_waitcnt vmcnt(10)
	s_barrier
	s_setprio 1
	v_mfma_scale_f32_16x16x128_f8f6f4 v[52:55], v[152:159], v[32:39], v[52:55], v149, v148 op_sel_hi:[0,0,0]
	v_mfma_scale_f32_16x16x128_f8f6f4 v[48:51], v[160:167], v[32:39], v[48:51], v149, v148 op_sel_hi:[0,0,0]
	v_mfma_scale_f32_16x16x128_f8f6f4 v[36:39], v[152:159], v[168:175], v[240:243], v149, v148 op_sel_hi:[0,0,0]
	v_mfma_scale_f32_16x16x128_f8f6f4 v[32:35], v[160:167], v[168:175], v[244:247], v149, v148 op_sel_hi:[0,0,0]
	v_mfma_scale_f32_16x16x128_f8f6f4 v[20:23], v[152:159], v[176:183], v[248:251], v149, v148 op_sel_hi:[0,0,0]
	v_mfma_scale_f32_16x16x128_f8f6f4 v[16:19], v[160:167], v[176:183], v[80:83], v149, v148 op_sel_hi:[0,0,0]
	v_mfma_scale_f32_16x16x128_f8f6f4 v[4:7], v[152:159], v[192:199], v[72:75], v149, v148 op_sel_hi:[0,0,0]
	v_mfma_scale_f32_16x16x128_f8f6f4 v[0:3], v[160:167], v[192:199], v[76:79], v149, v148 op_sel_hi:[0,0,0]
	s_setprio 0
	s_barrier
	s_mov_b32 s77, s80
	s_mov_b32 s79, s78
	s_cbranch_scc0 .LBB0_1415
	s_waitcnt vmcnt(0)
	s_cmpk_lt_u32 s15, 0x100
	s_cbranch_scc0 .LBB0_1418
	s_barrier

; #define G_WAIT_V(n) asm volatile("s_waitcnt vmcnt(" #n ")" ::: "memory")
; #define G_BAR() __builtin_amdgcn_s_barrier()
; #define G_SCHED() __builtin_amdgcn_sched_barrier(0)
; #define D_STAGE_A(slot, half, kt) D_STAGE(rsA, voffA, slot, half, kt)
; #define D_STAGE_B(slot, half, kt) D_STAGE(rsB, voffB, slot, half, kt)
; #define D_LDA(dst, slot) do { _Pragma("unroll") for (int m = 0; m < 4; ++m) _Pragma("unroll") for (int k = 0; k < 2; ++k) \
;     dst[m][k] = *(const LDS_AS bf16x8*)(lds + (slot) + aoff + m * 2048 + k * 1024); } while (0)
; #define D_LDB(dst, slot) do { _Pragma("unroll") for (int n = 0; n < 2; ++n) _Pragma("unroll") for (int k = 0; k < 2; ++k) \
;     dst[n][k] = *(const LDS_AS bf16x8*)(lds + (slot) + boff + n * 2048 + k * 1024); } while (0)
; #define D_WAIT_L(n) asm volatile("s_waitcnt lgkmcnt(" #n ")" ::: "memory")
; #define D_STAGE_A(slot, half, kt) D_STAGE(rsA, voffA, slot, half, kt)
; #define D_WAIT_L(n) asm volatile("s_waitcnt lgkmcnt(" #n ")" ::: "memory")
;     ...
;   for (int t = 0; t < (F8_PEEL ? nt - 2 : nt); t += 2) {
;     const int t1 = t + 1;
;     const int t2 = (F8_PEEL || t + 2 < nt) ? t + 2 : t;
;     const int t3 = (F8_PEEL || t + 2 < nt) ? t + 3 : t + 1;
;     D_LDB(B0, G_SB(0, 0)); G_SCHED(); D_LDA(At, G_SA(0, 0)); D_STAGE_A(G_SA(1, 1), 1, t1);
;     D_WAIT_L(8); G_BAR(); D_WAIT_L(0); G_SCHED(); D_MMA(0, 0, At, B0); G_BAR(); G_SCHED();
;     D_LDB(B1, G_SB(0, 1)); D_STAGE_B(G_SB(0, 0), 0, t2);
;     G_BAR(); D_WAIT_L(0); G_SCHED(); D_MMA(0, 1, At, B1); G_BAR(); G_SCHED();
;     D_LDA(At, G_SA(0, 1)); D_STAGE_A(G_SA(0, 0), 0, t2);
;     G_BAR(); D_WAIT_L(0); G_SCHED(); D_MMA(1, 0, At, B0); G_BAR(); G_SCHED();
;     D_STAGE_B(G_SB(0, 1), 1, t2);
;     G_WAIT_V(6); G_BAR(); G_SCHED(); D_MMA(1, 1, At, B1); G_BAR(); G_SCHED();
;     D_LDB(B0, G_SB(1, 0)); G_SCHED(); D_LDA(At, G_SA(1, 0)); D_STAGE_A(G_SA(0, 1), 1, t2);
;     D_WAIT_L(8); G_BAR(); D_WAIT_L(0); G_SCHED(); D_MMA(0, 0, At, B0); G_BAR(); G_SCHED();
;     D_LDB(B1, G_SB(1, 1)); D_STAGE_B(G_SB(1, 0), 0, t3);
;     G_BAR(); D_WAIT_L(0); G_SCHED(); D_MMA(0, 1, At, B1); G_BAR(); G_SCHED();
;     D_LDA(At, G_SA(1, 1)); D_STAGE_A(G_SA(1, 0), 0, t3);
;     G_BAR(); D_WAIT_L(0); G_SCHED(); D_MMA(1, 0, At, B0); G_BAR(); G_SCHED();
;     D_STAGE_B(G_SB(1, 1), 1, t3);
;     G_WAIT_V(6); G_BAR(); G_SCHED(); D_MMA(1, 1, At, B1); G_BAR(); G_SCHED();
;   }
.LBB0_1443:
	s_add_i32 s81, 0, 0x10010
	v_add_u32_e32 v73, s81, v69
	v_add_u32_e32 v86, s81, v70
	ds_read_b128 v[74:77], v73
	ds_read_b128 v[82:85], v73 offset:2048
	ds_read_b128 v[78:81], v86
	ds_read_b128 v[86:89], v86 offset:2048
	s_add_i32 s38, s79, 1
	s_add_i32 s78, s79, 3
	s_add_i32 s76, s79, 2
	s_add_i32 s86, 0, 0x14010
	s_cmp_lt_u32 s79, 14
	s_cselect_b32 s80, s76, s79
	s_cselect_b32 s38, s78, s38
	s_lshl_b32 s85, s80, 7
	s_lshl_b32 s80, s38, 7
	s_add_i32 s87, s85, 0x20000
	s_add_i32 s90, s85, 0x2000
	s_add_i32 s91, s85, 0x22000
	s_add_i32 s96, 0, 0x18010
	s_add_i32 s84, 0, 0x1c010
	s_add_i32 s83, s80, 0x20000
	s_add_i32 s82, s80, 0x2000
	s_add_i32 s81, s80, 0x22000
	s_add_i32 s78, s77, 0x100
	s_cmp_gt_u32 s79, 13
	ds_read_b128 v[90:93], v71 offset:16
	ds_read_b128 v[98:101], v71 offset:2064
	ds_read_b128 v[94:97], v72 offset:16
	ds_read_b128 v[102:105], v72 offset:2064
	ds_read_b128 v[106:109], v71 offset:4112
	ds_read_b128 v[114:117], v71 offset:6160
	ds_read_b128 v[110:113], v72 offset:4112
	ds_read_b128 v[118:121], v72 offset:6160
	s_mov_b32 m0, s74
	s_nop 0
	buffer_load_dwordx4 v65, s[8:11], s77 offen lds
	s_nop 0
	s_mov_b32 m0, s75
	s_nop 0
	buffer_load_dwordx4 v68, s[8:11], s77 offen lds
	s_waitcnt lgkmcnt(8)
	s_waitcnt vmcnt(10)
	s_barrier
	s_nop 0
	s_setprio 1
	s_waitcnt lgkmcnt(5)
	v_mfma_scale_f32_16x16x128_f8f6f4 v[56:59], v[74:81], v[90:97], v[56:59], v149, v148 op_sel_hi:[0,0,0]
	v_mfma_scale_f32_16x16x128_f8f6f4 v[60:63], v[82:89], v[90:97], v[60:63], v149, v148 op_sel_hi:[0,0,0]
	s_waitcnt lgkmcnt(4)
	v_mfma_scale_f32_16x16x128_f8f6f4 v[44:47], v[74:81], v[98:105], v[44:47], v149, v148 op_sel_hi:[0,0,0]
	v_mfma_scale_f32_16x16x128_f8f6f4 v[40:43], v[82:89], v[98:105], v[40:43], v149, v148 op_sel_hi:[0,0,0]
	s_waitcnt lgkmcnt(1)
	v_mfma_scale_f32_16x16x128_f8f6f4 v[122:125], v[74:81], v[106:113], v[28:31], v149, v148 op_sel_hi:[0,0,0]
	v_mfma_scale_f32_16x16x128_f8f6f4 v[126:129], v[82:89], v[106:113], v[24:27], v149, v148 op_sel_hi:[0,0,0]
	s_waitcnt lgkmcnt(0)
	v_mfma_scale_f32_16x16x128_f8f6f4 v[130:133], v[74:81], v[114:121], v[12:15], v149, v148 op_sel_hi:[0,0,0]
	v_mfma_scale_f32_16x16x128_f8f6f4 v[134:137], v[82:89], v[114:121], v[8:11], v149, v148 op_sel_hi:[0,0,0]
	s_setprio 0
	s_barrier
	s_nop 3
	v_add_u32_e32 v12, s86, v69
	v_add_u32_e32 v28, s86, v70
	ds_read_b128 v[8:11], v12
	ds_read_b128 v[24:27], v12 offset:2048
	ds_read_b128 v[12:15], v28
	ds_read_b128 v[28:31], v28 offset:2048
	s_mov_b32 m0, s21
	s_nop 0
	buffer_load_dwordx4 v66, s[4:7], s85 offen lds
	s_nop 0
	s_mov_b32 m0, s39
	s_nop 0
	buffer_load_dwordx4 v66, s[4:7], s87 offen lds
	s_waitcnt vmcnt(10)
	s_barrier
	s_nop 0
	s_setprio 1
	s_waitcnt lgkmcnt(1)
	v_mfma_scale_f32_16x16x128_f8f6f4 v[52:55], v[8:15], v[90:97], v[52:55], v149, v148 op_sel_hi:[0,0,0]
	s_waitcnt lgkmcnt(0)
	v_mfma_scale_f32_16x16x128_f8f6f4 v[48:51], v[24:31], v[90:97], v[48:51], v149, v148 op_sel_hi:[0,0,0]
	v_mfma_scale_f32_16x16x128_f8f6f4 v[138:141], v[8:15], v[98:105], v[36:39], v149, v148 op_sel_hi:[0,0,0]
	v_mfma_scale_f32_16x16x128_f8f6f4 v[142:145], v[24:31], v[98:105], v[32:35], v149, v148 op_sel_hi:[0,0,0]
	v_mfma_scale_f32_16x16x128_f8f6f4 v[152:155], v[8:15], v[106:113], v[20:23], v149, v148 op_sel_hi:[0,0,0]
	v_mfma_scale_f32_16x16x128_f8f6f4 v[106:109], v[24:31], v[106:113], v[16:19], v149, v148 op_sel_hi:[0,0,0]
	v_mfma_scale_f32_16x16x128_f8f6f4 v[110:113], v[8:15], v[114:121], v[4:7], v149, v148 op_sel_hi:[0,0,0]
	v_mfma_scale_f32_16x16x128_f8f6f4 v[114:117], v[24:31], v[114:121], v[0:3], v149, v148 op_sel_hi:[0,0,0]
	s_setprio 0
	s_barrier
	s_mov_b32 m0, s60
	s_nop 0
	buffer_load_dwordx4 v64, s[8:11], s85 offen lds
	s_nop 0
	s_mov_b32 m0, s61
	s_nop 0
	buffer_load_dwordx4 v67, s[8:11], s85 offen lds
	s_barrier
	s_waitcnt lgkmcnt(0)
	s_barrier
; #define G_WAIT_V(n) asm volatile("s_waitcnt vmcnt(" #n ")" ::: "memory")
; #define G_BAR() __builtin_amdgcn_s_barrier()
; #define G_SCHED() __builtin_amdgcn_sched_barrier(0)
; #define D_STAGE_A(slot, half, kt) D_STAGE(rsA, voffA, slot, half, kt)
; #define D_STAGE_B(slot, half, kt) D_STAGE(rsB, voffB, slot, half, kt)
; #define D_LDA(dst, slot) do { _Pragma("unroll") for (int m = 0; m < 4; ++m) _Pragma("unroll") for (int k = 0; k < 2; ++k) \
;     dst[m][k] = *(const LDS_AS bf16x8*)(lds + (slot) + aoff + m * 2048 + k * 1024); } while (0)
; #define D_LDB(dst, slot) do { _Pragma("unroll") for (int n = 0; n < 2; ++n) _Pragma("unroll") for (int k = 0; k < 2; ++k) \
;     dst[n][k] = *(const LDS_AS bf16x8*)(lds + (slot) + boff + n * 2048 + k * 1024); } while (0)
; #define D_WAIT_L(n) asm volatile("s_waitcnt lgkmcnt(" #n ")" ::: "memory")
; #define D_STAGE_A(slot, half, kt) D_STAGE(rsA, voffA, slot, half, kt)
; #define D_WAIT_L(n) asm volatile("s_waitcnt lgkmcnt(" #n ")" ::: "memory")
;     ...
;   for (int t = 0; t < (F8_PEEL ? nt - 2 : nt); t += 2) {
;     const int t1 = t + 1;
;     const int t2 = (F8_PEEL || t + 2 < nt) ? t + 2 : t;
;     const int t3 = (F8_PEEL || t + 2 < nt) ? t + 3 : t + 1;
;     D_LDB(B0, G_SB(0, 0)); G_SCHED(); D_LDA(At, G_SA(0, 0)); D_STAGE_A(G_SA(1, 1), 1, t1);
;     D_WAIT_L(8); G_BAR(); D_WAIT_L(0); G_SCHED(); D_MMA(0, 0, At, B0); G_BAR(); G_SCHED();
;     D_LDB(B1, G_SB(0, 1)); D_STAGE_B(G_SB(0, 0), 0, t2);
;     G_BAR(); D_WAIT_L(0); G_SCHED(); D_MMA(0, 1, At, B1); G_BAR(); G_SCHED();
;     D_LDA(At, G_SA(0, 1)); D_STAGE_A(G_SA(0, 0), 0, t2);
;     G_BAR(); D_WAIT_L(0); G_SCHED(); D_MMA(1, 0, At, B0); G_BAR(); G_SCHED();
;     D_STAGE_B(G_SB(0, 1), 1, t2);
;     G_WAIT_V(6); G_BAR(); G_SCHED(); D_MMA(1, 1, At, B1); G_BAR(); G_SCHED();
;     D_LDB(B0, G_SB(1, 0)); G_SCHED(); D_LDA(At, G_SA(1, 0)); D_STAGE_A(G_SA(0, 1), 1, t2);
;     D_WAIT_L(8); G_BAR(); D_WAIT_L(0); G_SCHED(); D_MMA(0, 0, At, B0); G_BAR(); G_SCHED();
;     D_LDB(B1, G_SB(1, 1)); D_STAGE_B(G_SB(1, 0), 0, t3);
;     G_BAR(); D_WAIT_L(0); G_SCHED(); D_MMA(0, 1, At, B1); G_BAR(); G_SCHED();
;     D_LDA(At, G_SA(1, 1)); D_STAGE_A(G_SA(1, 0), 0, t3);
;     G_BAR(); D_WAIT_L(0); G_SCHED(); D_MMA(1, 0, At, B0); G_BAR(); G_SCHED();
;     D_STAGE_B(G_SB(1, 1), 1, t3);
;     G_WAIT_V(6); G_BAR(); G_SCHED(); D_MMA(1, 1, At, B1); G_BAR(); G_SCHED();
;   }
	s_mov_b32 m0, s62
	s_nop 0
	buffer_load_dwordx4 v66, s[4:7], s90 offen lds
	s_nop 0
	s_mov_b32 m0, s63
	s_nop 0
	buffer_load_dwordx4 v66, s[4:7], s91 offen lds
	s_waitcnt vmcnt(10)
	s_barrier
	s_barrier
	v_add_u32_e32 v4, s96, v69
	v_add_u32_e32 v8, s96, v70
	ds_read_b128 v[0:3], v4
	ds_read_b128 v[16:19], v4 offset:2048
	ds_read_b128 v[4:7], v8
	ds_read_b128 v[20:23], v8 offset:2048
	ds_read_b128 v[32:35], v71 offset:32784
	ds_read_b128 v[74:77], v71 offset:34832
	ds_read_b128 v[36:39], v72 offset:32784
	ds_read_b128 v[78:81], v72 offset:34832
	ds_read_b128 v[82:85], v71 offset:36880
	ds_read_b128 v[90:93], v71 offset:38928
	ds_read_b128 v[86:89], v72 offset:36880
	ds_read_b128 v[94:97], v72 offset:38928
	s_mov_b32 m0, s66
	s_nop 0
	buffer_load_dwordx4 v65, s[8:11], s85 offen lds
	s_nop 0
	s_mov_b32 m0, s67
	s_nop 0
	buffer_load_dwordx4 v68, s[8:11], s85 offen lds
	s_waitcnt lgkmcnt(8)
	s_waitcnt vmcnt(10)
	s_barrier
	s_nop 0
	s_setprio 1
	s_waitcnt lgkmcnt(5)
	v_mfma_scale_f32_16x16x128_f8f6f4 v[56:59], v[0:7], v[32:39], v[56:59], v149, v148 op_sel_hi:[0,0,0]
	v_mfma_scale_f32_16x16x128_f8f6f4 v[60:63], v[16:23], v[32:39], v[60:63], v149, v148 op_sel_hi:[0,0,0]
	s_waitcnt lgkmcnt(4)
	v_mfma_scale_f32_16x16x128_f8f6f4 v[44:47], v[0:7], v[74:81], v[44:47], v149, v148 op_sel_hi:[0,0,0]
	v_mfma_scale_f32_16x16x128_f8f6f4 v[40:43], v[16:23], v[74:81], v[40:43], v149, v148 op_sel_hi:[0,0,0]
	s_waitcnt lgkmcnt(1)
	v_mfma_scale_f32_16x16x128_f8f6f4 v[28:31], v[0:7], v[82:89], v[122:125], v149, v148 op_sel_hi:[0,0,0]
	v_mfma_scale_f32_16x16x128_f8f6f4 v[24:27], v[16:23], v[82:89], v[126:129], v149, v148 op_sel_hi:[0,0,0]
	s_waitcnt lgkmcnt(0)
	v_mfma_scale_f32_16x16x128_f8f6f4 v[12:15], v[0:7], v[90:97], v[130:133], v149, v148 op_sel_hi:[0,0,0]
	v_mfma_scale_f32_16x16x128_f8f6f4 v[8:11], v[16:23], v[90:97], v[134:137], v149, v148 op_sel_hi:[0,0,0]
	s_setprio 0
	s_barrier
	v_add_u32_e32 v4, s84, v69
	v_add_u32_e32 v16, s84, v70
	ds_read_b128 v[0:3], v4
	ds_read_b128 v[98:101], v4 offset:2048
	ds_read_b128 v[4:7], v16
	ds_read_b128 v[102:105], v16 offset:2048
	s_mov_b32 m0, s68
	s_nop 0
	buffer_load_dwordx4 v66, s[4:7], s80 offen lds
	s_nop 0
	s_mov_b32 m0, s69
	s_nop 0
	buffer_load_dwordx4 v66, s[4:7], s83 offen lds
	s_waitcnt vmcnt(10)
	s_barrier
	s_nop 0
	s_setprio 1
	s_waitcnt lgkmcnt(1)
	v_mfma_scale_f32_16x16x128_f8f6f4 v[52:55], v[0:7], v[32:39], v[52:55], v149, v148 op_sel_hi:[0,0,0]
	s_waitcnt lgkmcnt(0)
	v_mfma_scale_f32_16x16x128_f8f6f4 v[48:51], v[98:105], v[32:39], v[48:51], v149, v148 op_sel_hi:[0,0,0]
	v_mfma_scale_f32_16x16x128_f8f6f4 v[36:39], v[0:7], v[74:81], v[138:141], v149, v148 op_sel_hi:[0,0,0]
	v_mfma_scale_f32_16x16x128_f8f6f4 v[32:35], v[98:105], v[74:81], v[142:145], v149, v148 op_sel_hi:[0,0,0]
	v_mfma_scale_f32_16x16x128_f8f6f4 v[20:23], v[0:7], v[82:89], v[152:155], v149, v148 op_sel_hi:[0,0,0]
	v_mfma_scale_f32_16x16x128_f8f6f4 v[16:19], v[98:105], v[82:89], v[106:109], v149, v148 op_sel_hi:[0,0,0]
	v_mfma_scale_f32_16x16x128_f8f6f4 v[4:7], v[0:7], v[90:97], v[110:113], v149, v148 op_sel_hi:[0,0,0]
	v_mfma_scale_f32_16x16x128_f8f6f4 v[0:3], v[98:105], v[90:97], v[114:117], v149, v148 op_sel_hi:[0,0,0]
	s_setprio 0
	s_barrier
	s_mov_b32 m0, s70
	s_nop 0
	buffer_load_dwordx4 v64, s[8:11], s80 offen lds
	s_nop 0
	s_mov_b32 m0, s71
	s_nop 0
	buffer_load_dwordx4 v67, s[8:11], s80 offen lds
	s_barrier
	s_waitcnt lgkmcnt(0)
	s_barrier
	s_mov_b32 m0, s72
	s_nop 0
	buffer_load_dwordx4 v66, s[4:7], s82 offen lds
	s_nop 0
	s_mov_b32 m0, s73
	s_nop 0
	buffer_load_dwordx4 v66, s[4:7], s81 offen lds
	s_waitcnt vmcnt(10)
	s_barrier
	s_barrier
	s_mov_b32 s77, s78
	s_mov_b32 s79, s76
	s_cbranch_scc0 .LBB0_1443
	s_waitcnt vmcnt(0)
	s_cmpk_lt_u32 s15, 0x100
	s_cbranch_scc0 .LBB0_1446
	s_barrier

; #define G_WAIT_V(n) asm volatile("s_waitcnt vmcnt(" #n ")" ::: "memory")
; #define G_BAR() __builtin_amdgcn_s_barrier()
; #define G_SCHED() __builtin_amdgcn_sched_barrier(0)
; #define D_STAGE_A(slot, half, kt) D_STAGE(rsA, voffA, slot, half, kt)
; #define D_STAGE_B(slot, half, kt) D_STAGE(rsB, voffB, slot, half, kt)
; #define D_LDA(dst, slot) do { _Pragma("unroll") for (int m = 0; m < 4; ++m) _Pragma("unroll") for (int k = 0; k < 2; ++k) \
;     dst[m][k] = *(const LDS_AS bf16x8*)(lds + (slot) + aoff + m * 2048 + k * 1024); } while (0)
; #define D_LDB(dst, slot) do { _Pragma("unroll") for (int n = 0; n < 2; ++n) _Pragma("unroll") for (int k = 0; k < 2; ++k) \
;     dst[n][k] = *(const LDS_AS bf16x8*)(lds + (slot) + boff + n * 2048 + k * 1024); } while (0)
; #define D_WAIT_L(n) asm volatile("s_waitcnt lgkmcnt(" #n ")" ::: "memory")
; #define D_STAGE_A(slot, half, kt) D_STAGE(rsA, voffA, slot, half, kt)
; #define D_WAIT_L(n) asm volatile("s_waitcnt lgkmcnt(" #n ")" ::: "memory")
;     ...
;   for (int t = 0; t < (F8_PEEL ? nt - 2 : nt); t += 2) {
;     const int t1 = t + 1;
;     const int t2 = (F8_PEEL || t + 2 < nt) ? t + 2 : t;
;     const int t3 = (F8_PEEL || t + 2 < nt) ? t + 3 : t + 1;
;     D_LDB(B0, G_SB(0, 0)); G_SCHED(); D_LDA(At, G_SA(0, 0)); D_STAGE_A(G_SA(1, 1), 1, t1);
;     D_WAIT_L(8); G_BAR(); D_WAIT_L(0); G_SCHED(); D_MMA(0, 0, At, B0); G_BAR(); G_SCHED();
;     D_LDB(B1, G_SB(0, 1)); D_STAGE_B(G_SB(0, 0), 0, t2);
;     G_BAR(); D_WAIT_L(0); G_SCHED(); D_MMA(0, 1, At, B1); G_BAR(); G_SCHED();
;     D_LDA(At, G_SA(0, 1)); D_STAGE_A(G_SA(0, 0), 0, t2);
;     G_BAR(); D_WAIT_L(0); G_SCHED(); D_MMA(1, 0, At, B0); G_BAR(); G_SCHED();
;     D_STAGE_B(G_SB(0, 1), 1, t2);
;     G_WAIT_V(6); G_BAR(); G_SCHED(); D_MMA(1, 1, At, B1); G_BAR(); G_SCHED();
;     D_LDB(B0, G_SB(1, 0)); G_SCHED(); D_LDA(At, G_SA(1, 0)); D_STAGE_A(G_SA(0, 1), 1, t2);
;     D_WAIT_L(8); G_BAR(); D_WAIT_L(0); G_SCHED(); D_MMA(0, 0, At, B0); G_BAR(); G_SCHED();
;     D_LDB(B1, G_SB(1, 1)); D_STAGE_B(G_SB(1, 0), 0, t3);
;     G_BAR(); D_WAIT_L(0); G_SCHED(); D_MMA(0, 1, At, B1); G_BAR(); G_SCHED();
;     D_LDA(At, G_SA(1, 1)); D_STAGE_A(G_SA(1, 0), 0, t3);
;     G_BAR(); D_WAIT_L(0); G_SCHED(); D_MMA(1, 0, At, B0); G_BAR(); G_SCHED();
;     D_STAGE_B(G_SB(1, 1), 1, t3);
;     G_WAIT_V(6); G_BAR(); G_SCHED(); D_MMA(1, 1, At, B1); G_BAR(); G_SCHED();
;   }
.LBB0_1483:
	s_add_i32 s77, 0, 0x10010
	v_add_u32_e32 v72, s77, v124
	v_add_u32_e32 v73, s77, v125
	ds_read_b128 v[152:155], v72
	ds_read_b128 v[160:163], v72 offset:2048
	ds_read_b128 v[156:159], v73
	ds_read_b128 v[164:167], v73 offset:2048
	s_add_i32 s38, s73, 1
	s_add_i32 s75, s73, 3
	s_add_i32 s74, s73, 2
	s_add_i32 s85, 0, 0x14010
	s_cmp_lt_u32 s73, 14
	s_cselect_b32 s76, s74, s73
	s_cselect_b32 s38, s75, s38
	s_lshl_b32 s81, s76, 7
	s_lshl_b32 s76, s38, 7
	s_add_i32 s86, s81, 0x20000
	s_add_i32 s83, s81, 0x2000
	s_add_i32 s84, s81, 0x22000
	s_add_i32 s82, 0, 0x18010
	s_add_i32 s80, 0, 0x1c010
	s_add_i32 s79, s76, 0x20000
	s_add_i32 s77, s76, 0x2000
	s_add_i32 s78, s76, 0x22000
	s_add_i32 s75, s72, 0x100
	s_cmp_gt_u32 s73, 13
	ds_read_b128 v[168:171], v127 offset:16
	ds_read_b128 v[176:179], v127 offset:2064
	ds_read_b128 v[172:175], v128 offset:16
	ds_read_b128 v[180:183], v128 offset:2064
	ds_read_b128 v[192:195], v127 offset:4112
	ds_read_b128 v[200:203], v127 offset:6160
	ds_read_b128 v[196:199], v128 offset:4112
	ds_read_b128 v[204:207], v128 offset:6160
	s_waitcnt lgkmcnt(12)
	s_mov_b32 m0, s26
	s_nop 0
	buffer_load_dwordx4 v122, s[8:11], s72 offen lds
	s_nop 0
	s_mov_b32 m0, s62
	s_nop 0
	buffer_load_dwordx4 v123, s[8:11], s72 offen lds
	s_waitcnt lgkmcnt(8)
	s_waitcnt vmcnt(10)
	s_barrier
	s_nop 0
	s_setprio 1
	s_waitcnt lgkmcnt(5)
	v_mfma_scale_f32_16x16x128_f8f6f4 v[134:137], v[160:167], v[168:175], v[136:139], v149, v148 op_sel_hi:[0,0,0]
	s_waitcnt lgkmcnt(0)
	v_mfma_scale_f32_16x16x128_f8f6f4 v[220:223], v[152:159], v[200:207], v[220:223], v149, v148 op_sel_hi:[0,0,0]
	v_mfma_scale_f32_16x16x128_f8f6f4 v[224:227], v[160:167], v[200:207], v[224:227], v149, v148 op_sel_hi:[0,0,0]
	v_mfma_scale_f32_16x16x128_f8f6f4 v[130:133], v[152:159], v[168:175], v[140:143], v149, v148 op_sel_hi:[0,0,0]
	v_mfma_scale_f32_16x16x128_f8f6f4 v[184:187], v[152:159], v[176:183], v[108:111], v149, v148 op_sel_hi:[0,0,0]
	v_mfma_scale_f32_16x16x128_f8f6f4 v[208:211], v[160:167], v[176:183], v[104:107], v149, v148 op_sel_hi:[0,0,0]
	v_mfma_scale_f32_16x16x128_f8f6f4 v[212:215], v[152:159], v[192:199], v[92:95], v149, v148 op_sel_hi:[0,0,0]
	v_mfma_scale_f32_16x16x128_f8f6f4 v[216:219], v[160:167], v[192:199], v[88:91], v149, v148 op_sel_hi:[0,0,0]
	s_setprio 0
	s_barrier
	v_add_u32_e32 v76, s85, v124
	v_add_u32_e32 v80, s85, v125
	ds_read_b128 v[72:75], v76
	s_nop 1
	ds_read_b128 v[88:91], v76 offset:2048
	ds_read_b128 v[76:79], v80
	ds_read_b128 v[92:95], v80 offset:2048
	s_mov_b32 m0, s27
	s_nop 0
	buffer_load_dwordx4 v126, s[4:7], s81 offen lds
	s_nop 0
	s_mov_b32 m0, s63
	s_nop 0
	buffer_load_dwordx4 v126, s[4:7], s86 offen lds
	s_waitcnt vmcnt(10)
	s_barrier
	s_nop 0
	s_setprio 1
	s_waitcnt lgkmcnt(1)
	v_mfma_scale_f32_16x16x128_f8f6f4 v[68:71], v[72:79], v[200:207], v[68:71], v149, v148 op_sel_hi:[0,0,0]
	s_waitcnt lgkmcnt(0)
	v_mfma_scale_f32_16x16x128_f8f6f4 v[56:59], v[88:95], v[200:207], v[56:59], v149, v148 op_sel_hi:[0,0,0]
	v_mfma_scale_f32_16x16x128_f8f6f4 v[228:231], v[72:79], v[168:175], v[116:119], v149, v148 op_sel_hi:[0,0,0]
	v_mfma_scale_f32_16x16x128_f8f6f4 v[168:171], v[88:95], v[168:175], v[112:115], v149, v148 op_sel_hi:[0,0,0]
	v_mfma_scale_f32_16x16x128_f8f6f4 v[172:175], v[72:79], v[176:183], v[100:103], v149, v148 op_sel_hi:[0,0,0]
	v_mfma_scale_f32_16x16x128_f8f6f4 v[176:179], v[88:95], v[176:183], v[96:99], v149, v148 op_sel_hi:[0,0,0]
	v_mfma_scale_f32_16x16x128_f8f6f4 v[180:183], v[72:79], v[192:199], v[84:87], v149, v148 op_sel_hi:[0,0,0]
	v_mfma_scale_f32_16x16x128_f8f6f4 v[192:195], v[88:95], v[192:199], v[8:11], v149, v148 op_sel_hi:[0,0,0]
	s_setprio 0
	s_barrier
	ds_read_b128 v[80:83], v127 offset:16400
	s_nop 1
	ds_read_b128 v[96:99], v127 offset:18448
	ds_read_b128 v[84:87], v128 offset:16400
	ds_read_b128 v[100:103], v128 offset:18448
	ds_read_b128 v[104:107], v127 offset:20496
	ds_read_b128 v[112:115], v127 offset:22544
	ds_read_b128 v[108:111], v128 offset:20496
	ds_read_b128 v[116:119], v128 offset:22544
	s_mov_b32 m0, s17
	s_nop 0
	buffer_load_dwordx4 v120, s[8:11], s81 offen lds
	s_nop 0
	s_mov_b32 m0, s66
	s_nop 0
	buffer_load_dwordx4 v121, s[8:11], s81 offen lds
	s_barrier
	s_nop 0
	s_setprio 1
	s_waitcnt lgkmcnt(5)
	v_mfma_scale_f32_16x16x128_f8f6f4 v[64:67], v[152:159], v[80:87], v[64:67], v149, v148 op_sel_hi:[0,0,0]
	v_mfma_scale_f32_16x16x128_f8f6f4 v[60:63], v[160:167], v[80:87], v[60:63], v149, v148 op_sel_hi:[0,0,0]
	s_waitcnt lgkmcnt(0)
	v_mfma_scale_f32_16x16x128_f8f6f4 v[244:247], v[160:167], v[112:119], v[244:247], v149, v148 op_sel_hi:[0,0,0]
	v_mfma_scale_f32_16x16x128_f8f6f4 v[200:203], v[152:159], v[96:103], v[44:47], v149, v148 op_sel_hi:[0,0,0]
	v_mfma_scale_f32_16x16x128_f8f6f4 v[204:207], v[160:167], v[96:103], v[40:43], v149, v148 op_sel_hi:[0,0,0]
	v_mfma_scale_f32_16x16x128_f8f6f4 v[232:235], v[152:159], v[104:111], v[28:31], v149, v148 op_sel_hi:[0,0,0]
	v_mfma_scale_f32_16x16x128_f8f6f4 v[236:239], v[160:167], v[104:111], v[24:27], v149, v148 op_sel_hi:[0,0,0]
	v_mfma_scale_f32_16x16x128_f8f6f4 v[240:243], v[152:159], v[112:119], v[12:15], v149, v148 op_sel_hi:[0,0,0]
	s_setprio 0
	s_barrier
	s_mov_b32 m0, s28
	s_nop 0
	buffer_load_dwordx4 v126, s[4:7], s83 offen lds
	s_nop 0
	s_mov_b32 m0, s67
	s_nop 0
	buffer_load_dwordx4 v126, s[4:7], s84 offen lds
	s_waitcnt vmcnt(10)
	s_barrier
; #define G_WAIT_V(n) asm volatile("s_waitcnt vmcnt(" #n ")" ::: "memory")
; #define G_BAR() __builtin_amdgcn_s_barrier()
; #define G_SCHED() __builtin_amdgcn_sched_barrier(0)
; #define D_STAGE_A(slot, half, kt) D_STAGE(rsA, voffA, slot, half, kt)
; #define D_STAGE_B(slot, half, kt) D_STAGE(rsB, voffB, slot, half, kt)
; #define D_LDA(dst, slot) do { _Pragma("unroll") for (int m = 0; m < 4; ++m) _Pragma("unroll") for (int k = 0; k < 2; ++k) \
;     dst[m][k] = *(const LDS_AS bf16x8*)(lds + (slot) + aoff + m * 2048 + k * 1024); } while (0)
; #define D_LDB(dst, slot) do { _Pragma("unroll") for (int n = 0; n < 2; ++n) _Pragma("unroll") for (int k = 0; k < 2; ++k) \
;     dst[n][k] = *(const LDS_AS bf16x8*)(lds + (slot) + boff + n * 2048 + k * 1024); } while (0)
; #define D_WAIT_L(n) asm volatile("s_waitcnt lgkmcnt(" #n ")" ::: "memory")
; #define D_STAGE_A(slot, half, kt) D_STAGE(rsA, voffA, slot, half, kt)
; #define D_WAIT_L(n) asm volatile("s_waitcnt lgkmcnt(" #n ")" ::: "memory")
;     ...
;   for (int t = 0; t < (F8_PEEL ? nt - 2 : nt); t += 2) {
;     const int t1 = t + 1;
;     const int t2 = (F8_PEEL || t + 2 < nt) ? t + 2 : t;
;     const int t3 = (F8_PEEL || t + 2 < nt) ? t + 3 : t + 1;
;     D_LDB(B0, G_SB(0, 0)); G_SCHED(); D_LDA(At, G_SA(0, 0)); D_STAGE_A(G_SA(1, 1), 1, t1);
;     D_WAIT_L(8); G_BAR(); D_WAIT_L(0); G_SCHED(); D_MMA(0, 0, At, B0); G_BAR(); G_SCHED();
;     D_LDB(B1, G_SB(0, 1)); D_STAGE_B(G_SB(0, 0), 0, t2);
;     G_BAR(); D_WAIT_L(0); G_SCHED(); D_MMA(0, 1, At, B1); G_BAR(); G_SCHED();
;     D_LDA(At, G_SA(0, 1)); D_STAGE_A(G_SA(0, 0), 0, t2);
;     G_BAR(); D_WAIT_L(0); G_SCHED(); D_MMA(1, 0, At, B0); G_BAR(); G_SCHED();
;     D_STAGE_B(G_SB(0, 1), 1, t2);
;     G_WAIT_V(6); G_BAR(); G_SCHED(); D_MMA(1, 1, At, B1); G_BAR(); G_SCHED();
;     D_LDB(B0, G_SB(1, 0)); G_SCHED(); D_LDA(At, G_SA(1, 0)); D_STAGE_A(G_SA(0, 1), 1, t2);
;     D_WAIT_L(8); G_BAR(); D_WAIT_L(0); G_SCHED(); D_MMA(0, 0, At, B0); G_BAR(); G_SCHED();
;     D_LDB(B1, G_SB(1, 1)); D_STAGE_B(G_SB(1, 0), 0, t3);
;     G_BAR(); D_WAIT_L(0); G_SCHED(); D_MMA(0, 1, At, B1); G_BAR(); G_SCHED();
;     D_LDA(At, G_SA(1, 1)); D_STAGE_A(G_SA(1, 0), 0, t3);
;     G_BAR(); D_WAIT_L(0); G_SCHED(); D_MMA(1, 0, At, B0); G_BAR(); G_SCHED();
;     D_STAGE_B(G_SB(1, 1), 1, t3);
;     G_WAIT_V(6); G_BAR(); G_SCHED(); D_MMA(1, 1, At, B1); G_BAR(); G_SCHED();
;   }
	s_setprio 1
	v_mfma_scale_f32_16x16x128_f8f6f4 v[52:55], v[72:79], v[80:87], v[52:55], v149, v148 op_sel_hi:[0,0,0]
	v_mfma_scale_f32_16x16x128_f8f6f4 v[48:51], v[88:95], v[80:87], v[48:51], v149, v148 op_sel_hi:[0,0,0]
	v_mfma_scale_f32_16x16x128_f8f6f4 v[248:251], v[72:79], v[96:103], v[36:39], v149, v148 op_sel_hi:[0,0,0]
	v_mfma_scale_f32_16x16x128_f8f6f4 v[188:191], v[88:95], v[96:103], v[32:35], v149, v148 op_sel_hi:[0,0,0]
	v_mfma_scale_f32_16x16x128_f8f6f4 v[144:147], v[72:79], v[104:111], v[20:23], v149, v148 op_sel_hi:[0,0,0]
	v_mfma_scale_f32_16x16x128_f8f6f4 v[80:83], v[88:95], v[104:111], v[16:19], v149, v148 op_sel_hi:[0,0,0]
	v_mfma_scale_f32_16x16x128_f8f6f4 v[72:75], v[72:79], v[112:119], v[4:7], v149, v148 op_sel_hi:[0,0,0]
	v_mfma_scale_f32_16x16x128_f8f6f4 v[76:79], v[88:95], v[112:119], v[0:3], v149, v148 op_sel_hi:[0,0,0]
	s_setprio 0
	s_barrier
	s_nop 3
	v_add_u32_e32 v4, s82, v124
	v_add_u32_e32 v8, s82, v125
	ds_read_b128 v[0:3], v4
	ds_read_b128 v[16:19], v4 offset:2048
	ds_read_b128 v[4:7], v8
	ds_read_b128 v[20:23], v8 offset:2048
	ds_read_b128 v[8:11], v127 offset:32784
	ds_read_b128 v[24:27], v127 offset:34832
	ds_read_b128 v[12:15], v128 offset:32784
	ds_read_b128 v[28:31], v128 offset:34832
	ds_read_b128 v[32:35], v127 offset:36880
	ds_read_b128 v[40:43], v127 offset:38928
	ds_read_b128 v[36:39], v128 offset:36880
	ds_read_b128 v[44:47], v128 offset:38928
	s_mov_b32 m0, s29
	s_nop 0
	buffer_load_dwordx4 v122, s[8:11], s81 offen lds
	s_nop 0
	s_mov_b32 m0, s68
	s_nop 0
	buffer_load_dwordx4 v123, s[8:11], s81 offen lds
	s_waitcnt lgkmcnt(8)
	s_waitcnt vmcnt(10)
	s_barrier
	s_nop 0
	s_setprio 1
	s_waitcnt lgkmcnt(5)
	v_mfma_scale_f32_16x16x128_f8f6f4 v[140:143], v[0:7], v[8:15], v[130:133], v149, v148 op_sel_hi:[0,0,0]
	v_mfma_scale_f32_16x16x128_f8f6f4 v[136:139], v[16:23], v[8:15], v[134:137], v149, v148 op_sel_hi:[0,0,0]
	s_waitcnt lgkmcnt(4)
	v_mfma_scale_f32_16x16x128_f8f6f4 v[108:111], v[0:7], v[24:31], v[184:187], v149, v148 op_sel_hi:[0,0,0]
	v_mfma_scale_f32_16x16x128_f8f6f4 v[104:107], v[16:23], v[24:31], v[208:211], v149, v148 op_sel_hi:[0,0,0]
	s_waitcnt lgkmcnt(1)
	v_mfma_scale_f32_16x16x128_f8f6f4 v[92:95], v[0:7], v[32:39], v[212:215], v149, v148 op_sel_hi:[0,0,0]
	v_mfma_scale_f32_16x16x128_f8f6f4 v[88:91], v[16:23], v[32:39], v[216:219], v149, v148 op_sel_hi:[0,0,0]
	s_waitcnt lgkmcnt(0)
	v_mfma_scale_f32_16x16x128_f8f6f4 v[220:223], v[0:7], v[40:47], v[220:223], v149, v148 op_sel_hi:[0,0,0]
	v_mfma_scale_f32_16x16x128_f8f6f4 v[224:227], v[16:23], v[40:47], v[224:227], v149, v148 op_sel_hi:[0,0,0]
	s_setprio 0
	s_barrier
	v_add_u32_e32 v84, s80, v124
	v_add_u32_e32 v85, s80, v125
	ds_read_b128 v[152:155], v84
	ds_read_b128 v[160:163], v84 offset:2048
	ds_read_b128 v[156:159], v85
	ds_read_b128 v[164:167], v85 offset:2048
	s_mov_b32 m0, s39
	s_nop 0
	buffer_load_dwordx4 v126, s[4:7], s76 offen lds
	s_nop 0
	s_mov_b32 m0, s69
	s_nop 0
	buffer_load_dwordx4 v126, s[4:7], s79 offen lds
	s_waitcnt vmcnt(10)
	s_barrier
	s_nop 0
	s_setprio 1
	s_waitcnt lgkmcnt(1)
	v_mfma_scale_f32_16x16x128_f8f6f4 v[116:119], v[152:159], v[8:15], v[228:231], v149, v148 op_sel_hi:[0,0,0]
	s_waitcnt lgkmcnt(0)
	v_mfma_scale_f32_16x16x128_f8f6f4 v[112:115], v[160:167], v[8:15], v[168:171], v149, v148 op_sel_hi:[0,0,0]
	v_mfma_scale_f32_16x16x128_f8f6f4 v[100:103], v[152:159], v[24:31], v[172:175], v149, v148 op_sel_hi:[0,0,0]
	v_mfma_scale_f32_16x16x128_f8f6f4 v[96:99], v[160:167], v[24:31], v[176:179], v149, v148 op_sel_hi:[0,0,0]
	v_mfma_scale_f32_16x16x128_f8f6f4 v[84:87], v[152:159], v[32:39], v[180:183], v149, v148 op_sel_hi:[0,0,0]
	v_mfma_scale_f32_16x16x128_f8f6f4 v[8:11], v[160:167], v[32:39], v[192:195], v149, v148 op_sel_hi:[0,0,0]
	v_mfma_scale_f32_16x16x128_f8f6f4 v[68:71], v[152:159], v[40:47], v[68:71], v149, v148 op_sel_hi:[0,0,0]
	v_mfma_scale_f32_16x16x128_f8f6f4 v[56:59], v[160:167], v[40:47], v[56:59], v149, v148 op_sel_hi:[0,0,0]
	s_setprio 0
	s_barrier
	ds_read_b128 v[32:35], v127 offset:49168
	ds_read_b128 v[168:171], v127 offset:51216
	ds_read_b128 v[36:39], v128 offset:49168
	ds_read_b128 v[172:175], v128 offset:51216
	ds_read_b128 v[176:179], v127 offset:53264
	ds_read_b128 v[192:195], v127 offset:55312
	ds_read_b128 v[180:183], v128 offset:53264
	ds_read_b128 v[196:199], v128 offset:55312
	s_mov_b32 m0, s60
	s_nop 0
	buffer_load_dwordx4 v120, s[8:11], s76 offen lds
	s_nop 0
	s_mov_b32 m0, s70
	s_nop 0
	buffer_load_dwordx4 v121, s[8:11], s76 offen lds
	s_barrier
	s_nop 0
	s_setprio 1
	s_waitcnt lgkmcnt(5)
	v_mfma_scale_f32_16x16x128_f8f6f4 v[64:67], v[0:7], v[32:39], v[64:67], v149, v148 op_sel_hi:[0,0,0]
	v_mfma_scale_f32_16x16x128_f8f6f4 v[60:63], v[16:23], v[32:39], v[60:63], v149, v148 op_sel_hi:[0,0,0]
	s_waitcnt lgkmcnt(4)
	v_mfma_scale_f32_16x16x128_f8f6f4 v[44:47], v[0:7], v[168:175], v[200:203], v149, v148 op_sel_hi:[0,0,0]
	v_mfma_scale_f32_16x16x128_f8f6f4 v[40:43], v[16:23], v[168:175], v[204:207], v149, v148 op_sel_hi:[0,0,0]
	s_waitcnt lgkmcnt(1)
	v_mfma_scale_f32_16x16x128_f8f6f4 v[28:31], v[0:7], v[176:183], v[232:235], v149, v148 op_sel_hi:[0,0,0]
	v_mfma_scale_f32_16x16x128_f8f6f4 v[24:27], v[16:23], v[176:183], v[236:239], v149, v148 op_sel_hi:[0,0,0]
	s_waitcnt lgkmcnt(0)
	v_mfma_scale_f32_16x16x128_f8f6f4 v[12:15], v[0:7], v[192:199], v[240:243], v149, v148 op_sel_hi:[0,0,0]
	v_mfma_scale_f32_16x16x128_f8f6f4 v[244:247], v[16:23], v[192:199], v[244:247], v149, v148 op_sel_hi:[0,0,0]
	s_setprio 0
	s_barrier
	s_mov_b32 m0, s61
	s_nop 0
	buffer_load_dwordx4 v126, s[4:7], s77 offen lds
	s_nop 0
	s_mov_b32 m0, s71
	s_nop 0
	buffer_load_dwordx4 v126, s[4:7], s78 offen lds
	s_waitcnt vmcnt(10)
	s_barrier
	s_setprio 1
	v_mfma_scale_f32_16x16x128_f8f6f4 v[52:55], v[152:159], v[32:39], v[52:55], v149, v148 op_sel_hi:[0,0,0]
	v_mfma_scale_f32_16x16x128_f8f6f4 v[48:51], v[160:167], v[32:39], v[48:51], v149, v148 op_sel_hi:[0,0,0]
	v_mfma_scale_f32_16x16x128_f8f6f4 v[36:39], v[152:159], v[168:175], v[248:251], v149, v148 op_sel_hi:[0,0,0]
	v_mfma_scale_f32_16x16x128_f8f6f4 v[32:35], v[160:167], v[168:175], v[188:191], v149, v148 op_sel_hi:[0,0,0]
	v_mfma_scale_f32_16x16x128_f8f6f4 v[20:23], v[152:159], v[176:183], v[144:147], v149, v148 op_sel_hi:[0,0,0]
	v_mfma_scale_f32_16x16x128_f8f6f4 v[16:19], v[160:167], v[176:183], v[80:83], v149, v148 op_sel_hi:[0,0,0]
	v_mfma_scale_f32_16x16x128_f8f6f4 v[4:7], v[152:159], v[192:199], v[72:75], v149, v148 op_sel_hi:[0,0,0]
	v_mfma_scale_f32_16x16x128_f8f6f4 v[0:3], v[160:167], v[192:199], v[76:79], v149, v148 op_sel_hi:[0,0,0]
	s_setprio 0
	s_barrier
	s_mov_b32 s72, s75
	s_mov_b32 s73, s74
	s_cbranch_scc0 .LBB0_1483
	s_waitcnt vmcnt(0)
	s_cmpk_lt_u32 s15, 0x100
	s_cbranch_scc0 .LBB0_1486
	s_barrier

; #define G_WAIT_V(n) asm volatile("s_waitcnt vmcnt(" #n ")" ::: "memory")
; #define G_BAR() __builtin_amdgcn_s_barrier()
; #define G_SCHED() __builtin_amdgcn_sched_barrier(0)
; #define D_STAGE_A(slot, half, kt) D_STAGE(rsA, voffA, slot, half, kt)
; #define D_STAGE_B(slot, half, kt) D_STAGE(rsB, voffB, slot, half, kt)
; #define D_LDA(dst, slot) do { _Pragma("unroll") for (int m = 0; m < 4; ++m) _Pragma("unroll") for (int k = 0; k < 2; ++k) \
;     dst[m][k] = *(const LDS_AS bf16x8*)(lds + (slot) + aoff + m * 2048 + k * 1024); } while (0)
; #define D_LDB(dst, slot) do { _Pragma("unroll") for (int n = 0; n < 2; ++n) _Pragma("unroll") for (int k = 0; k < 2; ++k) \
;     dst[n][k] = *(const LDS_AS bf16x8*)(lds + (slot) + boff + n * 2048 + k * 1024); } while (0)
; #define D_WAIT_L(n) asm volatile("s_waitcnt lgkmcnt(" #n ")" ::: "memory")
; #define D_STAGE_A(slot, half, kt) D_STAGE(rsA, voffA, slot, half, kt)
; #define D_WAIT_L(n) asm volatile("s_waitcnt lgkmcnt(" #n ")" ::: "memory")
;     ...
;   for (int t = 0; t < (F8_PEEL ? nt - 2 : nt); t += 2) {
;     const int t1 = t + 1;
;     const int t2 = (F8_PEEL || t + 2 < nt) ? t + 2 : t;
;     const int t3 = (F8_PEEL || t + 2 < nt) ? t + 3 : t + 1;
;     D_LDB(B0, G_SB(0, 0)); G_SCHED(); D_LDA(At, G_SA(0, 0)); D_STAGE_A(G_SA(1, 1), 1, t1);
;     D_WAIT_L(8); G_BAR(); D_WAIT_L(0); G_SCHED(); D_MMA(0, 0, At, B0); G_BAR(); G_SCHED();
;     D_LDB(B1, G_SB(0, 1)); D_STAGE_B(G_SB(0, 0), 0, t2);
;     G_BAR(); D_WAIT_L(0); G_SCHED(); D_MMA(0, 1, At, B1); G_BAR(); G_SCHED();
;     D_LDA(At, G_SA(0, 1)); D_STAGE_A(G_SA(0, 0), 0, t2);
;     G_BAR(); D_WAIT_L(0); G_SCHED(); D_MMA(1, 0, At, B0); G_BAR(); G_SCHED();
;     D_STAGE_B(G_SB(0, 1), 1, t2);
;     G_WAIT_V(6); G_BAR(); G_SCHED(); D_MMA(1, 1, At, B1); G_BAR(); G_SCHED();
;     D_LDB(B0, G_SB(1, 0)); G_SCHED(); D_LDA(At, G_SA(1, 0)); D_STAGE_A(G_SA(0, 1), 1, t2);
;     D_WAIT_L(8); G_BAR(); D_WAIT_L(0); G_SCHED(); D_MMA(0, 0, At, B0); G_BAR(); G_SCHED();
;     D_LDB(B1, G_SB(1, 1)); D_STAGE_B(G_SB(1, 0), 0, t3);
;     G_BAR(); D_WAIT_L(0); G_SCHED(); D_MMA(0, 1, At, B1); G_BAR(); G_SCHED();
;     D_LDA(At, G_SA(1, 1)); D_STAGE_A(G_SA(1, 0), 0, t3);
;     G_BAR(); D_WAIT_L(0); G_SCHED(); D_MMA(1, 0, At, B0); G_BAR(); G_SCHED();
;     D_STAGE_B(G_SB(1, 1), 1, t3);
;     G_WAIT_V(6); G_BAR(); G_SCHED(); D_MMA(1, 1, At, B1); G_BAR(); G_SCHED();
;   }
.LBB0_1510:
	s_add_i32 s77, 0, 0x10010
	s_waitcnt vmcnt(62)
	v_add_u32_e32 v73, s77, v68
	s_waitcnt vmcnt(49)
	v_add_u32_e32 v86, s77, v69
	ds_read_b128 v[74:77], v73
	ds_read_b128 v[82:85], v73 offset:2048
	ds_read_b128 v[78:81], v86
	s_waitcnt vmcnt(46)
	ds_read_b128 v[86:89], v86 offset:2048
	s_add_i32 s38, s75, 1
	s_add_i32 s74, s75, 3
	s_add_i32 s73, s75, 2
	s_add_i32 s82, 0, 0x14010
	s_cmp_lt_u32 s75, 14
	s_cselect_b32 s76, s73, s75
	s_cselect_b32 s38, s74, s38
	s_lshl_b32 s81, s76, 7
	s_lshl_b32 s76, s38, 7
	s_add_i32 s83, s81, 0x20000
	s_add_i32 s84, s81, 0x2000
	s_add_i32 s85, s81, 0x22000
	s_add_i32 s86, 0, 0x18010
	s_add_i32 s80, 0, 0x1c010
	s_add_i32 s79, s76, 0x20000
	s_add_i32 s77, s76, 0x2000
	s_add_i32 s78, s76, 0x22000
	s_add_i32 s74, s72, 0x100
	s_cmp_gt_u32 s75, 13
	s_waitcnt vmcnt(42)
	ds_read_b128 v[90:93], v71 offset:16
	s_waitcnt vmcnt(34)
	ds_read_b128 v[98:101], v71 offset:2064
	ds_read_b128 v[94:97], v72 offset:16
	s_waitcnt vmcnt(30)
	ds_read_b128 v[102:105], v72 offset:2064
	s_waitcnt vmcnt(26)
	ds_read_b128 v[106:109], v71 offset:4112
	s_waitcnt vmcnt(18)
	ds_read_b128 v[114:117], v71 offset:6160
	ds_read_b128 v[110:113], v72 offset:4112
	s_waitcnt vmcnt(2)
	ds_read_b128 v[118:121], v72 offset:6160
	s_waitcnt lgkmcnt(12)
	s_mov_b32 m0, s26
	s_nop 0
	buffer_load_dwordx4 v66, s[8:11], s72 offen lds
	s_nop 0
	s_mov_b32 m0, s62
	s_nop 0
	buffer_load_dwordx4 v67, s[8:11], s72 offen lds
	s_waitcnt lgkmcnt(8)
	s_waitcnt vmcnt(10)
	s_barrier
	s_nop 0
	s_setprio 1
	s_waitcnt lgkmcnt(5)
	v_mfma_scale_f32_16x16x128_f8f6f4 v[56:59], v[74:81], v[90:97], v[56:59], v149, v148 op_sel_hi:[0,0,0]
	v_mfma_scale_f32_16x16x128_f8f6f4 v[60:63], v[82:89], v[90:97], v[60:63], v149, v148 op_sel_hi:[0,0,0]
	s_waitcnt lgkmcnt(4)
	v_mfma_scale_f32_16x16x128_f8f6f4 v[44:47], v[74:81], v[98:105], v[44:47], v149, v148 op_sel_hi:[0,0,0]
	v_mfma_scale_f32_16x16x128_f8f6f4 v[40:43], v[82:89], v[98:105], v[40:43], v149, v148 op_sel_hi:[0,0,0]
	s_waitcnt vmcnt(0) lgkmcnt(1)
	v_mfma_scale_f32_16x16x128_f8f6f4 v[122:125], v[74:81], v[106:113], v[28:31], v149, v148 op_sel_hi:[0,0,0]
	v_mfma_scale_f32_16x16x128_f8f6f4 v[126:129], v[82:89], v[106:113], v[24:27], v149, v148 op_sel_hi:[0,0,0]
	s_waitcnt lgkmcnt(0)
	v_mfma_scale_f32_16x16x128_f8f6f4 v[130:133], v[74:81], v[114:121], v[12:15], v149, v148 op_sel_hi:[0,0,0]
	v_mfma_scale_f32_16x16x128_f8f6f4 v[134:137], v[82:89], v[114:121], v[8:11], v149, v148 op_sel_hi:[0,0,0]
	s_setprio 0
	s_barrier
	s_nop 3
	v_add_u32_e32 v12, s82, v68
	v_add_u32_e32 v28, s82, v69
	ds_read_b128 v[8:11], v12
	ds_read_b128 v[24:27], v12 offset:2048
	ds_read_b128 v[12:15], v28
	ds_read_b128 v[28:31], v28 offset:2048
	s_mov_b32 m0, s27
	s_nop 0
	buffer_load_dwordx4 v70, s[4:7], s81 offen lds
	s_nop 0
	s_mov_b32 m0, s63
	s_nop 0
	buffer_load_dwordx4 v70, s[4:7], s83 offen lds
	s_waitcnt vmcnt(10)
	s_barrier
	s_nop 0
	s_setprio 1
	s_waitcnt lgkmcnt(1)
	v_mfma_scale_f32_16x16x128_f8f6f4 v[52:55], v[8:15], v[90:97], v[52:55], v149, v148 op_sel_hi:[0,0,0]
	s_waitcnt lgkmcnt(0)
	v_mfma_scale_f32_16x16x128_f8f6f4 v[48:51], v[24:31], v[90:97], v[48:51], v149, v148 op_sel_hi:[0,0,0]
	v_mfma_scale_f32_16x16x128_f8f6f4 v[138:141], v[8:15], v[98:105], v[36:39], v149, v148 op_sel_hi:[0,0,0]
	v_mfma_scale_f32_16x16x128_f8f6f4 v[152:155], v[24:31], v[98:105], v[32:35], v149, v148 op_sel_hi:[0,0,0]
	v_mfma_scale_f32_16x16x128_f8f6f4 v[156:159], v[8:15], v[106:113], v[20:23], v149, v148 op_sel_hi:[0,0,0]
	v_mfma_scale_f32_16x16x128_f8f6f4 v[106:109], v[24:31], v[106:113], v[16:19], v149, v148 op_sel_hi:[0,0,0]
	v_mfma_scale_f32_16x16x128_f8f6f4 v[110:113], v[8:15], v[114:121], v[4:7], v149, v148 op_sel_hi:[0,0,0]
	v_mfma_scale_f32_16x16x128_f8f6f4 v[114:117], v[24:31], v[114:121], v[0:3], v149, v148 op_sel_hi:[0,0,0]
	s_setprio 0
	s_barrier
; #define G_WAIT_V(n) asm volatile("s_waitcnt vmcnt(" #n ")" ::: "memory")
; #define G_BAR() __builtin_amdgcn_s_barrier()
; #define G_SCHED() __builtin_amdgcn_sched_barrier(0)
; #define D_STAGE_A(slot, half, kt) D_STAGE(rsA, voffA, slot, half, kt)
; #define D_STAGE_B(slot, half, kt) D_STAGE(rsB, voffB, slot, half, kt)
; #define D_LDA(dst, slot) do { _Pragma("unroll") for (int m = 0; m < 4; ++m) _Pragma("unroll") for (int k = 0; k < 2; ++k) \
;     dst[m][k] = *(const LDS_AS bf16x8*)(lds + (slot) + aoff + m * 2048 + k * 1024); } while (0)
; #define D_LDB(dst, slot) do { _Pragma("unroll") for (int n = 0; n < 2; ++n) _Pragma("unroll") for (int k = 0; k < 2; ++k) \
;     dst[n][k] = *(const LDS_AS bf16x8*)(lds + (slot) + boff + n * 2048 + k * 1024); } while (0)
; #define D_WAIT_L(n) asm volatile("s_waitcnt lgkmcnt(" #n ")" ::: "memory")
; #define D_STAGE_A(slot, half, kt) D_STAGE(rsA, voffA, slot, half, kt)
; #define D_WAIT_L(n) asm volatile("s_waitcnt lgkmcnt(" #n ")" ::: "memory")
;     ...
;   for (int t = 0; t < (F8_PEEL ? nt - 2 : nt); t += 2) {
;     const int t1 = t + 1;
;     const int t2 = (F8_PEEL || t + 2 < nt) ? t + 2 : t;
;     const int t3 = (F8_PEEL || t + 2 < nt) ? t + 3 : t + 1;
;     D_LDB(B0, G_SB(0, 0)); G_SCHED(); D_LDA(At, G_SA(0, 0)); D_STAGE_A(G_SA(1, 1), 1, t1);
;     D_WAIT_L(8); G_BAR(); D_WAIT_L(0); G_SCHED(); D_MMA(0, 0, At, B0); G_BAR(); G_SCHED();
;     D_LDB(B1, G_SB(0, 1)); D_STAGE_B(G_SB(0, 0), 0, t2);
;     G_BAR(); D_WAIT_L(0); G_SCHED(); D_MMA(0, 1, At, B1); G_BAR(); G_SCHED();
;     D_LDA(At, G_SA(0, 1)); D_STAGE_A(G_SA(0, 0), 0, t2);
;     G_BAR(); D_WAIT_L(0); G_SCHED(); D_MMA(1, 0, At, B0); G_BAR(); G_SCHED();
;     D_STAGE_B(G_SB(0, 1), 1, t2);
;     G_WAIT_V(6); G_BAR(); G_SCHED(); D_MMA(1, 1, At, B1); G_BAR(); G_SCHED();
;     D_LDB(B0, G_SB(1, 0)); G_SCHED(); D_LDA(At, G_SA(1, 0)); D_STAGE_A(G_SA(0, 1), 1, t2);
;     D_WAIT_L(8); G_BAR(); D_WAIT_L(0); G_SCHED(); D_MMA(0, 0, At, B0); G_BAR(); G_SCHED();
;     D_LDB(B1, G_SB(1, 1)); D_STAGE_B(G_SB(1, 0), 0, t3);
;     G_BAR(); D_WAIT_L(0); G_SCHED(); D_MMA(0, 1, At, B1); G_BAR(); G_SCHED();
;     D_LDA(At, G_SA(1, 1)); D_STAGE_A(G_SA(1, 0), 0, t3);
;     G_BAR(); D_WAIT_L(0); G_SCHED(); D_MMA(1, 0, At, B0); G_BAR(); G_SCHED();
;     D_STAGE_B(G_SB(1, 1), 1, t3);
;     G_WAIT_V(6); G_BAR(); G_SCHED(); D_MMA(1, 1, At, B1); G_BAR(); G_SCHED();
;   }
	s_mov_b32 m0, s17
	s_nop 0
	buffer_load_dwordx4 v64, s[8:11], s81 offen lds
	s_nop 0
	s_mov_b32 m0, s66
	s_nop 0
	buffer_load_dwordx4 v65, s[8:11], s81 offen lds
	s_barrier
	s_waitcnt lgkmcnt(0)
	s_barrier
	s_mov_b32 m0, s28
	s_nop 0
	buffer_load_dwordx4 v70, s[4:7], s84 offen lds
	s_nop 0
	s_mov_b32 m0, s67
	s_nop 0
	buffer_load_dwordx4 v70, s[4:7], s85 offen lds
	s_waitcnt vmcnt(10)
	s_barrier
	s_barrier
	v_add_u32_e32 v4, s86, v68
	v_add_u32_e32 v8, s86, v69
	ds_read_b128 v[0:3], v4
	ds_read_b128 v[16:19], v4 offset:2048
	ds_read_b128 v[4:7], v8
	ds_read_b128 v[20:23], v8 offset:2048
	ds_read_b128 v[32:35], v71 offset:32784
	ds_read_b128 v[74:77], v71 offset:34832
	ds_read_b128 v[36:39], v72 offset:32784
	ds_read_b128 v[78:81], v72 offset:34832
	ds_read_b128 v[82:85], v71 offset:36880
	ds_read_b128 v[90:93], v71 offset:38928
	ds_read_b128 v[86:89], v72 offset:36880
	ds_read_b128 v[94:97], v72 offset:38928
	s_mov_b32 m0, s29
	s_nop 0
	buffer_load_dwordx4 v66, s[8:11], s81 offen lds
	s_nop 0
	s_mov_b32 m0, s68
	s_nop 0
	buffer_load_dwordx4 v67, s[8:11], s81 offen lds
	s_waitcnt lgkmcnt(8)
	s_waitcnt vmcnt(10)
	s_barrier
	s_nop 0
	s_setprio 1
	s_waitcnt lgkmcnt(5)
	v_mfma_scale_f32_16x16x128_f8f6f4 v[56:59], v[0:7], v[32:39], v[56:59], v149, v148 op_sel_hi:[0,0,0]
	v_mfma_scale_f32_16x16x128_f8f6f4 v[60:63], v[16:23], v[32:39], v[60:63], v149, v148 op_sel_hi:[0,0,0]
	s_waitcnt lgkmcnt(4)
	v_mfma_scale_f32_16x16x128_f8f6f4 v[44:47], v[0:7], v[74:81], v[44:47], v149, v148 op_sel_hi:[0,0,0]
	v_mfma_scale_f32_16x16x128_f8f6f4 v[40:43], v[16:23], v[74:81], v[40:43], v149, v148 op_sel_hi:[0,0,0]
	s_waitcnt lgkmcnt(1)
	v_mfma_scale_f32_16x16x128_f8f6f4 v[28:31], v[0:7], v[82:89], v[122:125], v149, v148 op_sel_hi:[0,0,0]
	v_mfma_scale_f32_16x16x128_f8f6f4 v[24:27], v[16:23], v[82:89], v[126:129], v149, v148 op_sel_hi:[0,0,0]
	s_waitcnt lgkmcnt(0)
	v_mfma_scale_f32_16x16x128_f8f6f4 v[12:15], v[0:7], v[90:97], v[130:133], v149, v148 op_sel_hi:[0,0,0]
	v_mfma_scale_f32_16x16x128_f8f6f4 v[8:11], v[16:23], v[90:97], v[134:137], v149, v148 op_sel_hi:[0,0,0]
	s_setprio 0
	s_barrier
	v_add_u32_e32 v4, s80, v68
	v_add_u32_e32 v16, s80, v69
	ds_read_b128 v[0:3], v4
	ds_read_b128 v[98:101], v4 offset:2048
	ds_read_b128 v[4:7], v16
	ds_read_b128 v[102:105], v16 offset:2048
	s_mov_b32 m0, s39
	s_nop 0
	buffer_load_dwordx4 v70, s[4:7], s76 offen lds
	s_nop 0
	s_mov_b32 m0, s69
	s_nop 0
	buffer_load_dwordx4 v70, s[4:7], s79 offen lds
	s_waitcnt vmcnt(10)
	s_barrier
	s_nop 0
	s_setprio 1
	s_waitcnt lgkmcnt(1)
	v_mfma_scale_f32_16x16x128_f8f6f4 v[52:55], v[0:7], v[32:39], v[52:55], v149, v148 op_sel_hi:[0,0,0]
	s_waitcnt lgkmcnt(0)
	v_mfma_scale_f32_16x16x128_f8f6f4 v[48:51], v[98:105], v[32:39], v[48:51], v149, v148 op_sel_hi:[0,0,0]
	v_mfma_scale_f32_16x16x128_f8f6f4 v[36:39], v[0:7], v[74:81], v[138:141], v149, v148 op_sel_hi:[0,0,0]
	v_mfma_scale_f32_16x16x128_f8f6f4 v[32:35], v[98:105], v[74:81], v[152:155], v149, v148 op_sel_hi:[0,0,0]
	v_mfma_scale_f32_16x16x128_f8f6f4 v[20:23], v[0:7], v[82:89], v[156:159], v149, v148 op_sel_hi:[0,0,0]
	v_mfma_scale_f32_16x16x128_f8f6f4 v[16:19], v[98:105], v[82:89], v[106:109], v149, v148 op_sel_hi:[0,0,0]
	v_mfma_scale_f32_16x16x128_f8f6f4 v[4:7], v[0:7], v[90:97], v[110:113], v149, v148 op_sel_hi:[0,0,0]
	v_mfma_scale_f32_16x16x128_f8f6f4 v[0:3], v[98:105], v[90:97], v[114:117], v149, v148 op_sel_hi:[0,0,0]
	s_setprio 0
	s_barrier
	s_mov_b32 m0, s60
	s_nop 0
	buffer_load_dwordx4 v64, s[8:11], s76 offen lds
	s_nop 0
	s_mov_b32 m0, s70
	s_nop 0
	buffer_load_dwordx4 v65, s[8:11], s76 offen lds
	s_barrier
	s_waitcnt lgkmcnt(0)
	s_barrier
	s_mov_b32 m0, s61
	s_nop 0
	buffer_load_dwordx4 v70, s[4:7], s77 offen lds
	s_nop 0
	s_mov_b32 m0, s71
	s_nop 0
	buffer_load_dwordx4 v70, s[4:7], s78 offen lds
	s_waitcnt vmcnt(10)
	s_barrier
	s_barrier
	s_mov_b32 s72, s74
	s_mov_b32 s75, s73
	s_cbranch_scc0 .LBB0_1510
	s_waitcnt vmcnt(0)
	s_cmpk_lt_u32 s15, 0x100
	s_cbranch_scc0 .LBB0_1513
	s_barrier

; #define G_WAIT_V(n) asm volatile("s_waitcnt vmcnt(" #n ")" ::: "memory")
; #define G_BAR() __builtin_amdgcn_s_barrier()
; #define G_SCHED() __builtin_amdgcn_sched_barrier(0)
; #define D_STAGE_A(slot, half, kt) D_STAGE(rsA, voffA, slot, half, kt)
; #define D_STAGE_B(slot, half, kt) D_STAGE(rsB, voffB, slot, half, kt)
; #define D_LDA(dst, slot) do { _Pragma("unroll") for (int m = 0; m < 4; ++m) _Pragma("unroll") for (int k = 0; k < 2; ++k) \
;     dst[m][k] = *(const LDS_AS bf16x8*)(lds + (slot) + aoff + m * 2048 + k * 1024); } while (0)
; #define D_LDB(dst, slot) do { _Pragma("unroll") for (int n = 0; n < 2; ++n) _Pragma("unroll") for (int k = 0; k < 2; ++k) \
;     dst[n][k] = *(const LDS_AS bf16x8*)(lds + (slot) + boff + n * 2048 + k * 1024); } while (0)
; #define D_WAIT_L(n) asm volatile("s_waitcnt lgkmcnt(" #n ")" ::: "memory")
; #define D_STAGE_A(slot, half, kt) D_STAGE(rsA, voffA, slot, half, kt)
; #define D_WAIT_L(n) asm volatile("s_waitcnt lgkmcnt(" #n ")" ::: "memory")
;     ...
;   for (int t = 0; t < (F8_PEEL ? nt - 2 : nt); t += 2) {
;     const int t1 = t + 1;
;     const int t2 = (F8_PEEL || t + 2 < nt) ? t + 2 : t;
;     const int t3 = (F8_PEEL || t + 2 < nt) ? t + 3 : t + 1;
;     D_LDB(B0, G_SB(0, 0)); G_SCHED(); D_LDA(At, G_SA(0, 0)); D_STAGE_A(G_SA(1, 1), 1, t1);
;     D_WAIT_L(8); G_BAR(); D_WAIT_L(0); G_SCHED(); D_MMA(0, 0, At, B0); G_BAR(); G_SCHED();
;     D_LDB(B1, G_SB(0, 1)); D_STAGE_B(G_SB(0, 0), 0, t2);
;     G_BAR(); D_WAIT_L(0); G_SCHED(); D_MMA(0, 1, At, B1); G_BAR(); G_SCHED();
;     D_LDA(At, G_SA(0, 1)); D_STAGE_A(G_SA(0, 0), 0, t2);
;     G_BAR(); D_WAIT_L(0); G_SCHED(); D_MMA(1, 0, At, B0); G_BAR(); G_SCHED();
;     D_STAGE_B(G_SB(0, 1), 1, t2);
;     G_WAIT_V(6); G_BAR(); G_SCHED(); D_MMA(1, 1, At, B1); G_BAR(); G_SCHED();
;     D_LDB(B0, G_SB(1, 0)); G_SCHED(); D_LDA(At, G_SA(1, 0)); D_STAGE_A(G_SA(0, 1), 1, t2);
;     D_WAIT_L(8); G_BAR(); D_WAIT_L(0); G_SCHED(); D_MMA(0, 0, At, B0); G_BAR(); G_SCHED();
;     D_LDB(B1, G_SB(1, 1)); D_STAGE_B(G_SB(1, 0), 0, t3);
;     G_BAR(); D_WAIT_L(0); G_SCHED(); D_MMA(0, 1, At, B1); G_BAR(); G_SCHED();
;     D_LDA(At, G_SA(1, 1)); D_STAGE_A(G_SA(1, 0), 0, t3);
;     G_BAR(); D_WAIT_L(0); G_SCHED(); D_MMA(1, 0, At, B0); G_BAR(); G_SCHED();
;     D_STAGE_B(G_SB(1, 1), 1, t3);
;     G_WAIT_V(6); G_BAR(); G_SCHED(); D_MMA(1, 1, At, B1); G_BAR(); G_SCHED();
;   }
.LBB0_1606:
	s_add_i32 s74, 0, 0x10010
	v_add_u32_e32 v68, s74, v133
	v_add_u32_e32 v69, s74, v134
	ds_read_b128 v[146:149], v68
	ds_read_b128 v[154:157], v68 offset:2048
	ds_read_b128 v[150:153], v69
	ds_read_b128 v[158:161], v69 offset:2048
	s_add_i32 s38, s71, 1
	s_add_i32 s72, s71, 3
	s_add_i32 s70, s71, 2
	s_add_i32 s82, 0, 0x14010
	s_cmp_lt_u32 s71, 14
	s_cselect_b32 s73, s70, s71
	s_cselect_b32 s38, s72, s38
	s_lshl_b32 s78, s73, 7
	s_lshl_b32 s73, s38, 7
	s_add_i32 s83, s78, 0x20000
	s_add_i32 s81, s78, 0x40000
	s_add_i32 s80, s78, 0x60000
	s_add_i32 s79, 0, 0x18010
	s_add_i32 s77, 0, 0x1c010
	s_add_i32 s76, s73, 0x20000
	s_add_i32 s75, s73, 0x40000
	s_add_i32 s74, s73, 0x60000
	s_add_i32 s72, s69, 0x100
	s_cmp_gt_u32 s71, 13
	ds_read_b128 v[168:171], v135 offset:16
	ds_read_b128 v[176:179], v135 offset:2064
	ds_read_b128 v[172:175], v136 offset:16
	ds_read_b128 v[180:183], v136 offset:2064
	ds_read_b128 v[192:195], v135 offset:4112
	ds_read_b128 v[200:203], v135 offset:6160
	ds_read_b128 v[196:199], v136 offset:4112
	ds_read_b128 v[204:207], v136 offset:6160
	s_mov_b32 m0, s67
	s_nop 0
	buffer_load_dwordx4 v129, s[8:11], s69 offen lds
	s_nop 0
	s_mov_b32 m0, s68
	s_nop 0
	buffer_load_dwordx4 v132, s[8:11], s69 offen lds
	s_waitcnt lgkmcnt(8)
	s_waitcnt vmcnt(10)
	s_barrier
	s_nop 0
	s_setprio 1
	s_waitcnt lgkmcnt(0)
	v_mfma_scale_f32_16x16x128_f8f6f4 v[216:219], v[146:153], v[200:207], v[216:219], v165, v164 op_sel_hi:[0,0,0]
	v_mfma_scale_f32_16x16x128_f8f6f4 v[48:51], v[154:161], v[200:207], v[48:51], v165, v164 op_sel_hi:[0,0,0]
	v_mfma_scale_f32_16x16x128_f8f6f4 v[138:141], v[146:153], v[168:175], v[124:127], v165, v164 op_sel_hi:[0,0,0]
	v_mfma_scale_f32_16x16x128_f8f6f4 v[142:145], v[154:161], v[168:175], v[120:123], v165, v164 op_sel_hi:[0,0,0]
	v_mfma_scale_f32_16x16x128_f8f6f4 v[184:187], v[146:153], v[176:183], v[108:111], v165, v164 op_sel_hi:[0,0,0]
	v_mfma_scale_f32_16x16x128_f8f6f4 v[188:191], v[154:161], v[176:183], v[100:103], v165, v164 op_sel_hi:[0,0,0]
	v_mfma_scale_f32_16x16x128_f8f6f4 v[208:211], v[146:153], v[192:199], v[84:87], v165, v164 op_sel_hi:[0,0,0]
	v_mfma_scale_f32_16x16x128_f8f6f4 v[212:215], v[154:161], v[192:199], v[80:83], v165, v164 op_sel_hi:[0,0,0]
	s_setprio 0
	s_barrier
	v_add_u32_e32 v68, s82, v133
	v_add_u32_e32 v69, s82, v134
	s_nop 2
	ds_read_b128 v[80:83], v68
	ds_read_b128 v[120:123], v68 offset:2048
	ds_read_b128 v[84:87], v69
	ds_read_b128 v[124:127], v69 offset:2048
	s_mov_b32 m0, s39
	s_nop 0
	buffer_load_dwordx4 v130, s[4:7], s78 offen lds
	s_nop 0
	s_mov_b32 m0, s50
	s_nop 0
	buffer_load_dwordx4 v130, s[4:7], s83 offen lds
	s_waitcnt vmcnt(10)
	s_barrier
	s_nop 0
	s_setprio 1
	s_waitcnt lgkmcnt(1)
	v_mfma_scale_f32_16x16x128_f8f6f4 v[116:119], v[80:87], v[168:175], v[116:119], v165, v164 op_sel_hi:[0,0,0]
	s_waitcnt lgkmcnt(0)
	v_mfma_scale_f32_16x16x128_f8f6f4 v[112:115], v[120:127], v[168:175], v[112:115], v165, v164 op_sel_hi:[0,0,0]
	v_mfma_scale_f32_16x16x128_f8f6f4 v[76:79], v[80:87], v[200:207], v[76:79], v165, v164 op_sel_hi:[0,0,0]
	v_mfma_scale_f32_16x16x128_f8f6f4 v[166:169], v[80:87], v[176:183], v[104:107], v165, v164 op_sel_hi:[0,0,0]
	v_mfma_scale_f32_16x16x128_f8f6f4 v[170:173], v[120:127], v[176:183], v[96:99], v165, v164 op_sel_hi:[0,0,0]
	v_mfma_scale_f32_16x16x128_f8f6f4 v[174:177], v[80:87], v[192:199], v[92:95], v165, v164 op_sel_hi:[0,0,0]
	v_mfma_scale_f32_16x16x128_f8f6f4 v[178:181], v[120:127], v[192:199], v[88:91], v165, v164 op_sel_hi:[0,0,0]
	v_mfma_scale_f32_16x16x128_f8f6f4 v[192:195], v[120:127], v[200:207], v[16:19], v165, v164 op_sel_hi:[0,0,0]
	s_setprio 0
	s_barrier
	ds_read_b128 v[68:71], v135 offset:16400
	s_nop 2
	ds_read_b128 v[88:91], v135 offset:18448
	ds_read_b128 v[72:75], v136 offset:16400
	ds_read_b128 v[92:95], v136 offset:18448
	ds_read_b128 v[96:99], v135 offset:20496
	ds_read_b128 v[104:107], v135 offset:22544
	ds_read_b128 v[100:103], v136 offset:20496
	ds_read_b128 v[108:111], v136 offset:22544
	s_mov_b32 m0, s51
	s_nop 0
	buffer_load_dwordx4 v128, s[8:11], s78 offen lds
	s_nop 0
	s_mov_b32 m0, s54
	s_nop 0
	buffer_load_dwordx4 v131, s[8:11], s78 offen lds
	s_barrier
	s_nop 0
	s_setprio 1
	s_waitcnt lgkmcnt(5)
	v_mfma_scale_f32_16x16x128_f8f6f4 v[56:59], v[146:153], v[68:75], v[56:59], v165, v164 op_sel_hi:[0,0,0]
	v_mfma_scale_f32_16x16x128_f8f6f4 v[52:55], v[154:161], v[68:75], v[52:55], v165, v164 op_sel_hi:[0,0,0]
	s_waitcnt lgkmcnt(1)
	v_mfma_scale_f32_16x16x128_f8f6f4 v[224:227], v[154:161], v[96:103], v[224:227], v165, v164 op_sel_hi:[0,0,0]
	v_mfma_scale_f32_16x16x128_f8f6f4 v[200:203], v[146:153], v[88:95], v[36:39], v165, v164 op_sel_hi:[0,0,0]
	v_mfma_scale_f32_16x16x128_f8f6f4 v[204:207], v[154:161], v[88:95], v[32:35], v165, v164 op_sel_hi:[0,0,0]
	v_mfma_scale_f32_16x16x128_f8f6f4 v[220:223], v[146:153], v[96:103], v[20:23], v165, v164 op_sel_hi:[0,0,0]
	s_waitcnt lgkmcnt(0)
	v_mfma_scale_f32_16x16x128_f8f6f4 v[228:231], v[146:153], v[104:111], v[4:7], v165, v164 op_sel_hi:[0,0,0]
	v_mfma_scale_f32_16x16x128_f8f6f4 v[232:235], v[154:161], v[104:111], v[0:3], v165, v164 op_sel_hi:[0,0,0]
	s_setprio 0
	s_barrier
	s_mov_b32 m0, s55
	s_nop 0
	buffer_load_dwordx4 v130, s[4:7], s81 offen lds
	s_nop 0
	s_mov_b32 m0, s58
	s_nop 0
	buffer_load_dwordx4 v130, s[4:7], s80 offen lds
	s_waitcnt vmcnt(10)
	s_barrier
; #define G_WAIT_V(n) asm volatile("s_waitcnt vmcnt(" #n ")" ::: "memory")
; #define G_BAR() __builtin_amdgcn_s_barrier()
; #define G_SCHED() __builtin_amdgcn_sched_barrier(0)
; #define D_STAGE_A(slot, half, kt) D_STAGE(rsA, voffA, slot, half, kt)
; #define D_STAGE_B(slot, half, kt) D_STAGE(rsB, voffB, slot, half, kt)
; #define D_LDA(dst, slot) do { _Pragma("unroll") for (int m = 0; m < 4; ++m) _Pragma("unroll") for (int k = 0; k < 2; ++k) \
;     dst[m][k] = *(const LDS_AS bf16x8*)(lds + (slot) + aoff + m * 2048 + k * 1024); } while (0)
; #define D_LDB(dst, slot) do { _Pragma("unroll") for (int n = 0; n < 2; ++n) _Pragma("unroll") for (int k = 0; k < 2; ++k) \
;     dst[n][k] = *(const LDS_AS bf16x8*)(lds + (slot) + boff + n * 2048 + k * 1024); } while (0)
; #define D_WAIT_L(n) asm volatile("s_waitcnt lgkmcnt(" #n ")" ::: "memory")
; #define D_STAGE_A(slot, half, kt) D_STAGE(rsA, voffA, slot, half, kt)
; #define D_WAIT_L(n) asm volatile("s_waitcnt lgkmcnt(" #n ")" ::: "memory")
;     ...
;   for (int t = 0; t < (F8_PEEL ? nt - 2 : nt); t += 2) {
;     const int t1 = t + 1;
;     const int t2 = (F8_PEEL || t + 2 < nt) ? t + 2 : t;
;     const int t3 = (F8_PEEL || t + 2 < nt) ? t + 3 : t + 1;
;     D_LDB(B0, G_SB(0, 0)); G_SCHED(); D_LDA(At, G_SA(0, 0)); D_STAGE_A(G_SA(1, 1), 1, t1);
;     D_WAIT_L(8); G_BAR(); D_WAIT_L(0); G_SCHED(); D_MMA(0, 0, At, B0); G_BAR(); G_SCHED();
;     D_LDB(B1, G_SB(0, 1)); D_STAGE_B(G_SB(0, 0), 0, t2);
;     G_BAR(); D_WAIT_L(0); G_SCHED(); D_MMA(0, 1, At, B1); G_BAR(); G_SCHED();
;     D_LDA(At, G_SA(0, 1)); D_STAGE_A(G_SA(0, 0), 0, t2);
;     G_BAR(); D_WAIT_L(0); G_SCHED(); D_MMA(1, 0, At, B0); G_BAR(); G_SCHED();
;     D_STAGE_B(G_SB(0, 1), 1, t2);
;     G_WAIT_V(6); G_BAR(); G_SCHED(); D_MMA(1, 1, At, B1); G_BAR(); G_SCHED();
;     D_LDB(B0, G_SB(1, 0)); G_SCHED(); D_LDA(At, G_SA(1, 0)); D_STAGE_A(G_SA(0, 1), 1, t2);
;     D_WAIT_L(8); G_BAR(); D_WAIT_L(0); G_SCHED(); D_MMA(0, 0, At, B0); G_BAR(); G_SCHED();
;     D_LDB(B1, G_SB(1, 1)); D_STAGE_B(G_SB(1, 0), 0, t3);
;     G_BAR(); D_WAIT_L(0); G_SCHED(); D_MMA(0, 1, At, B1); G_BAR(); G_SCHED();
;     D_LDA(At, G_SA(1, 1)); D_STAGE_A(G_SA(1, 0), 0, t3);
;     G_BAR(); D_WAIT_L(0); G_SCHED(); D_MMA(1, 0, At, B0); G_BAR(); G_SCHED();
;     D_STAGE_B(G_SB(1, 1), 1, t3);
;     G_WAIT_V(6); G_BAR(); G_SCHED(); D_MMA(1, 1, At, B1); G_BAR(); G_SCHED();
;   }
	s_setprio 1
	v_mfma_scale_f32_16x16x128_f8f6f4 v[64:67], v[80:87], v[68:75], v[64:67], v165, v164 op_sel_hi:[0,0,0]
	v_mfma_scale_f32_16x16x128_f8f6f4 v[60:63], v[120:127], v[68:75], v[60:63], v165, v164 op_sel_hi:[0,0,0]
	v_mfma_scale_f32_16x16x128_f8f6f4 v[236:239], v[80:87], v[88:95], v[44:47], v165, v164 op_sel_hi:[0,0,0]
	v_mfma_scale_f32_16x16x128_f8f6f4 v[240:243], v[120:127], v[88:95], v[40:43], v165, v164 op_sel_hi:[0,0,0]
	v_mfma_scale_f32_16x16x128_f8f6f4 v[244:247], v[80:87], v[96:103], v[28:31], v165, v164 op_sel_hi:[0,0,0]
	v_mfma_scale_f32_16x16x128_f8f6f4 v[248:251], v[120:127], v[96:103], v[24:27], v165, v164 op_sel_hi:[0,0,0]
	v_mfma_scale_f32_16x16x128_f8f6f4 v[68:71], v[80:87], v[104:111], v[12:15], v165, v164 op_sel_hi:[0,0,0]
	v_mfma_scale_f32_16x16x128_f8f6f4 v[72:75], v[120:127], v[104:111], v[8:11], v165, v164 op_sel_hi:[0,0,0]
	s_setprio 0
	s_barrier
	v_add_u32_e32 v4, s79, v133
	s_nop 2
	v_add_u32_e32 v12, s79, v134
	ds_read_b128 v[0:3], v4
	ds_read_b128 v[8:11], v4 offset:2048
	ds_read_b128 v[4:7], v12
	ds_read_b128 v[12:15], v12 offset:2048
	ds_read_b128 v[16:19], v135 offset:32784
	ds_read_b128 v[24:27], v135 offset:34832
	ds_read_b128 v[20:23], v136 offset:32784
	ds_read_b128 v[28:31], v136 offset:34832
	ds_read_b128 v[32:35], v135 offset:36880
	ds_read_b128 v[40:43], v135 offset:38928
	ds_read_b128 v[36:39], v136 offset:36880
	ds_read_b128 v[44:47], v136 offset:38928
	s_mov_b32 m0, s59
	s_nop 0
	buffer_load_dwordx4 v129, s[8:11], s78 offen lds
	s_nop 0
	s_mov_b32 m0, s60
	s_nop 0
	buffer_load_dwordx4 v132, s[8:11], s78 offen lds
	s_waitcnt lgkmcnt(8)
	s_waitcnt vmcnt(10)
	s_barrier
	s_nop 0
	s_setprio 1
	s_waitcnt lgkmcnt(5)
	v_mfma_scale_f32_16x16x128_f8f6f4 v[124:127], v[0:7], v[16:23], v[138:141], v165, v164 op_sel_hi:[0,0,0]
	v_mfma_scale_f32_16x16x128_f8f6f4 v[120:123], v[8:15], v[16:23], v[142:145], v165, v164 op_sel_hi:[0,0,0]
	s_waitcnt lgkmcnt(4)
	v_mfma_scale_f32_16x16x128_f8f6f4 v[108:111], v[0:7], v[24:31], v[184:187], v165, v164 op_sel_hi:[0,0,0]
	v_mfma_scale_f32_16x16x128_f8f6f4 v[100:103], v[8:15], v[24:31], v[188:191], v165, v164 op_sel_hi:[0,0,0]
	s_waitcnt lgkmcnt(1)
	v_mfma_scale_f32_16x16x128_f8f6f4 v[84:87], v[0:7], v[32:39], v[208:211], v165, v164 op_sel_hi:[0,0,0]
	v_mfma_scale_f32_16x16x128_f8f6f4 v[80:83], v[8:15], v[32:39], v[212:215], v165, v164 op_sel_hi:[0,0,0]
	s_waitcnt lgkmcnt(0)
	v_mfma_scale_f32_16x16x128_f8f6f4 v[216:219], v[0:7], v[40:47], v[216:219], v165, v164 op_sel_hi:[0,0,0]
	v_mfma_scale_f32_16x16x128_f8f6f4 v[48:51], v[8:15], v[40:47], v[48:51], v165, v164 op_sel_hi:[0,0,0]
	s_setprio 0
	s_barrier
	v_add_u32_e32 v88, s77, v133
	v_add_u32_e32 v89, s77, v134
	ds_read_b128 v[146:149], v88
	ds_read_b128 v[154:157], v88 offset:2048
	ds_read_b128 v[150:153], v89
	ds_read_b128 v[158:161], v89 offset:2048
	s_mov_b32 m0, s61
	s_nop 0
	buffer_load_dwordx4 v130, s[4:7], s73 offen lds
	s_nop 0
	s_mov_b32 m0, s62
	s_nop 0
	buffer_load_dwordx4 v130, s[4:7], s76 offen lds
	s_waitcnt vmcnt(10)
	s_barrier
	s_nop 0
	s_setprio 1
	s_waitcnt lgkmcnt(1)
	v_mfma_scale_f32_16x16x128_f8f6f4 v[116:119], v[146:153], v[16:23], v[116:119], v165, v164 op_sel_hi:[0,0,0]
	s_waitcnt lgkmcnt(0)
	v_mfma_scale_f32_16x16x128_f8f6f4 v[112:115], v[154:161], v[16:23], v[112:115], v165, v164 op_sel_hi:[0,0,0]
	v_mfma_scale_f32_16x16x128_f8f6f4 v[104:107], v[146:153], v[24:31], v[166:169], v165, v164 op_sel_hi:[0,0,0]
	v_mfma_scale_f32_16x16x128_f8f6f4 v[96:99], v[154:161], v[24:31], v[170:173], v165, v164 op_sel_hi:[0,0,0]
	v_mfma_scale_f32_16x16x128_f8f6f4 v[92:95], v[146:153], v[32:39], v[174:177], v165, v164 op_sel_hi:[0,0,0]
	v_mfma_scale_f32_16x16x128_f8f6f4 v[88:91], v[154:161], v[32:39], v[178:181], v165, v164 op_sel_hi:[0,0,0]
	v_mfma_scale_f32_16x16x128_f8f6f4 v[76:79], v[146:153], v[40:47], v[76:79], v165, v164 op_sel_hi:[0,0,0]
	v_mfma_scale_f32_16x16x128_f8f6f4 v[16:19], v[154:161], v[40:47], v[192:195], v165, v164 op_sel_hi:[0,0,0]
	s_setprio 0
	s_barrier
	ds_read_b128 v[24:27], v135 offset:49168
	ds_read_b128 v[168:171], v135 offset:51216
	ds_read_b128 v[28:31], v136 offset:49168
	ds_read_b128 v[172:175], v136 offset:51216
	ds_read_b128 v[176:179], v135 offset:53264
	ds_read_b128 v[192:195], v135 offset:55312
	ds_read_b128 v[180:183], v136 offset:53264
	ds_read_b128 v[196:199], v136 offset:55312
	s_mov_b32 m0, s63
	s_nop 0
	buffer_load_dwordx4 v128, s[8:11], s73 offen lds
	s_nop 0
	s_mov_b32 m0, s64
	s_nop 0
	buffer_load_dwordx4 v131, s[8:11], s73 offen lds
	s_barrier
	s_nop 0
	s_setprio 1
	s_waitcnt lgkmcnt(5)
	v_mfma_scale_f32_16x16x128_f8f6f4 v[56:59], v[0:7], v[24:31], v[56:59], v165, v164 op_sel_hi:[0,0,0]
	v_mfma_scale_f32_16x16x128_f8f6f4 v[52:55], v[8:15], v[24:31], v[52:55], v165, v164 op_sel_hi:[0,0,0]
	s_waitcnt lgkmcnt(4)
	v_mfma_scale_f32_16x16x128_f8f6f4 v[36:39], v[0:7], v[168:175], v[200:203], v165, v164 op_sel_hi:[0,0,0]
	v_mfma_scale_f32_16x16x128_f8f6f4 v[32:35], v[8:15], v[168:175], v[204:207], v165, v164 op_sel_hi:[0,0,0]
	s_waitcnt lgkmcnt(1)
	v_mfma_scale_f32_16x16x128_f8f6f4 v[20:23], v[0:7], v[176:183], v[220:223], v165, v164 op_sel_hi:[0,0,0]
	v_mfma_scale_f32_16x16x128_f8f6f4 v[224:227], v[8:15], v[176:183], v[224:227], v165, v164 op_sel_hi:[0,0,0]
	s_waitcnt lgkmcnt(0)
	v_mfma_scale_f32_16x16x128_f8f6f4 v[4:7], v[0:7], v[192:199], v[228:231], v165, v164 op_sel_hi:[0,0,0]
	v_mfma_scale_f32_16x16x128_f8f6f4 v[0:3], v[8:15], v[192:199], v[232:235], v165, v164 op_sel_hi:[0,0,0]
	s_setprio 0
	s_barrier
	s_mov_b32 m0, s65
	s_nop 0
	buffer_load_dwordx4 v130, s[4:7], s75 offen lds
	s_nop 0
	s_mov_b32 m0, s66
	s_nop 0
	buffer_load_dwordx4 v130, s[4:7], s74 offen lds
	s_waitcnt vmcnt(10)
	s_barrier
	s_setprio 1
	v_mfma_scale_f32_16x16x128_f8f6f4 v[64:67], v[146:153], v[24:31], v[64:67], v165, v164 op_sel_hi:[0,0,0]
	v_mfma_scale_f32_16x16x128_f8f6f4 v[60:63], v[154:161], v[24:31], v[60:63], v165, v164 op_sel_hi:[0,0,0]
	v_mfma_scale_f32_16x16x128_f8f6f4 v[44:47], v[146:153], v[168:175], v[236:239], v165, v164 op_sel_hi:[0,0,0]
	v_mfma_scale_f32_16x16x128_f8f6f4 v[40:43], v[154:161], v[168:175], v[240:243], v165, v164 op_sel_hi:[0,0,0]
	v_mfma_scale_f32_16x16x128_f8f6f4 v[28:31], v[146:153], v[176:183], v[244:247], v165, v164 op_sel_hi:[0,0,0]
	v_mfma_scale_f32_16x16x128_f8f6f4 v[24:27], v[154:161], v[176:183], v[248:251], v165, v164 op_sel_hi:[0,0,0]
	v_mfma_scale_f32_16x16x128_f8f6f4 v[12:15], v[146:153], v[192:199], v[68:71], v165, v164 op_sel_hi:[0,0,0]
	v_mfma_scale_f32_16x16x128_f8f6f4 v[8:11], v[154:161], v[192:199], v[72:75], v165, v164 op_sel_hi:[0,0,0]
	s_setprio 0
	s_barrier
	s_mov_b32 s69, s72
	s_mov_b32 s71, s70
	s_cbranch_scc0 .LBB0_1606
	s_waitcnt vmcnt(0)
	s_cmpk_lt_u32 s13, 0x100
	s_cbranch_scc0 .LBB0_1609
	s_barrier

; #define G_WAIT_V(n) asm volatile("s_waitcnt vmcnt(" #n ")" ::: "memory")
; #define G_BAR() __builtin_amdgcn_s_barrier()
; #define G_SCHED() __builtin_amdgcn_sched_barrier(0)
; #define D_STAGE_A(slot, half, kt) D_STAGE(rsA, voffA, slot, half, kt)
; #define D_STAGE_B(slot, half, kt) D_STAGE(rsB, voffB, slot, half, kt)
; #define D_LDA(dst, slot) do { _Pragma("unroll") for (int m = 0; m < 4; ++m) _Pragma("unroll") for (int k = 0; k < 2; ++k) \
;     dst[m][k] = *(const LDS_AS bf16x8*)(lds + (slot) + aoff + m * 2048 + k * 1024); } while (0)
; #define D_LDB(dst, slot) do { _Pragma("unroll") for (int n = 0; n < 2; ++n) _Pragma("unroll") for (int k = 0; k < 2; ++k) \
;     dst[n][k] = *(const LDS_AS bf16x8*)(lds + (slot) + boff + n * 2048 + k * 1024); } while (0)
; #define D_WAIT_L(n) asm volatile("s_waitcnt lgkmcnt(" #n ")" ::: "memory")
; #define D_STAGE_A(slot, half, kt) D_STAGE(rsA, voffA, slot, half, kt)
; #define D_WAIT_L(n) asm volatile("s_waitcnt lgkmcnt(" #n ")" ::: "memory")
;     ...
;   for (int t = 0; t < (F8_PEEL ? nt - 2 : nt); t += 2) {
;     const int t1 = t + 1;
;     const int t2 = (F8_PEEL || t + 2 < nt) ? t + 2 : t;
;     const int t3 = (F8_PEEL || t + 2 < nt) ? t + 3 : t + 1;
;     D_LDB(B0, G_SB(0, 0)); G_SCHED(); D_LDA(At, G_SA(0, 0)); D_STAGE_A(G_SA(1, 1), 1, t1);
;     D_WAIT_L(8); G_BAR(); D_WAIT_L(0); G_SCHED(); D_MMA(0, 0, At, B0); G_BAR(); G_SCHED();
;     D_LDB(B1, G_SB(0, 1)); D_STAGE_B(G_SB(0, 0), 0, t2);
;     G_BAR(); D_WAIT_L(0); G_SCHED(); D_MMA(0, 1, At, B1); G_BAR(); G_SCHED();
;     D_LDA(At, G_SA(0, 1)); D_STAGE_A(G_SA(0, 0), 0, t2);
;     G_BAR(); D_WAIT_L(0); G_SCHED(); D_MMA(1, 0, At, B0); G_BAR(); G_SCHED();
;     D_STAGE_B(G_SB(0, 1), 1, t2);
;     G_WAIT_V(6); G_BAR(); G_SCHED(); D_MMA(1, 1, At, B1); G_BAR(); G_SCHED();
;     D_LDB(B0, G_SB(1, 0)); G_SCHED(); D_LDA(At, G_SA(1, 0)); D_STAGE_A(G_SA(0, 1), 1, t2);
;     D_WAIT_L(8); G_BAR(); D_WAIT_L(0); G_SCHED(); D_MMA(0, 0, At, B0); G_BAR(); G_SCHED();
;     D_LDB(B1, G_SB(1, 1)); D_STAGE_B(G_SB(1, 0), 0, t3);
;     G_BAR(); D_WAIT_L(0); G_SCHED(); D_MMA(0, 1, At, B1); G_BAR(); G_SCHED();
;     D_LDA(At, G_SA(1, 1)); D_STAGE_A(G_SA(1, 0), 0, t3);
;     G_BAR(); D_WAIT_L(0); G_SCHED(); D_MMA(1, 0, At, B0); G_BAR(); G_SCHED();
;     D_STAGE_B(G_SB(1, 1), 1, t3);
;     G_WAIT_V(6); G_BAR(); G_SCHED(); D_MMA(1, 1, At, B1); G_BAR(); G_SCHED();
;   }
.LBB0_1634:
	s_add_i32 s73, 0, 0x10010
	v_add_u32_e32 v73, s73, v69
	v_add_u32_e32 v86, s73, v70
	ds_read_b128 v[74:77], v73
	ds_read_b128 v[82:85], v73 offset:2048
	ds_read_b128 v[78:81], v86
	ds_read_b128 v[86:89], v86 offset:2048
	s_add_i32 s38, s71, 1
	s_add_i32 s70, s71, 3
	s_add_i32 s68, s71, 2
	s_add_i32 s78, 0, 0x14010
	s_cmp_lt_u32 s71, 14
	s_cselect_b32 s72, s68, s71
	s_cselect_b32 s38, s70, s38
	s_lshl_b32 s77, s72, 7
	s_lshl_b32 s72, s38, 7
	s_add_i32 s79, s77, 0x20000
	s_add_i32 s80, s77, 0x40000
	s_add_i32 s81, s77, 0x60000
	s_add_i32 s82, 0, 0x18010
	s_add_i32 s76, 0, 0x1c010
	s_add_i32 s75, s72, 0x20000
	s_add_i32 s74, s72, 0x40000
	s_add_i32 s73, s72, 0x60000
	s_add_i32 s70, s69, 0x100
	s_cmp_gt_u32 s71, 13
	ds_read_b128 v[90:93], v71 offset:16
	ds_read_b128 v[98:101], v71 offset:2064
	ds_read_b128 v[94:97], v72 offset:16
	ds_read_b128 v[102:105], v72 offset:2064
	ds_read_b128 v[106:109], v71 offset:4112
	ds_read_b128 v[114:117], v71 offset:6160
	ds_read_b128 v[110:113], v72 offset:4112
	ds_read_b128 v[118:121], v72 offset:6160
	s_mov_b32 m0, s66
	s_nop 0
	buffer_load_dwordx4 v65, s[8:11], s69 offen lds
	s_nop 0
	s_mov_b32 m0, s67
	s_nop 0
	buffer_load_dwordx4 v68, s[8:11], s69 offen lds
	s_waitcnt lgkmcnt(8)
	s_waitcnt vmcnt(10)
	s_barrier
	s_nop 0
	s_setprio 1
	s_waitcnt lgkmcnt(4)
	v_mfma_scale_f32_16x16x128_f8f6f4 v[40:43], v[74:81], v[98:105], v[40:43], v165, v164 op_sel_hi:[0,0,0]
	v_mfma_scale_f32_16x16x128_f8f6f4 v[32:35], v[82:89], v[98:105], v[32:35], v165, v164 op_sel_hi:[0,0,0]
	s_waitcnt lgkmcnt(1)
	v_mfma_scale_f32_16x16x128_f8f6f4 v[24:27], v[74:81], v[106:113], v[24:27], v165, v164 op_sel_hi:[0,0,0]
	v_mfma_scale_f32_16x16x128_f8f6f4 v[16:19], v[82:89], v[106:113], v[16:19], v165, v164 op_sel_hi:[0,0,0]
	s_waitcnt lgkmcnt(0)
	v_mfma_scale_f32_16x16x128_f8f6f4 v[8:11], v[74:81], v[114:121], v[8:11], v165, v164 op_sel_hi:[0,0,0]
	v_mfma_scale_f32_16x16x128_f8f6f4 v[122:125], v[74:81], v[90:97], v[48:51], v165, v164 op_sel_hi:[0,0,0]
	v_mfma_scale_f32_16x16x128_f8f6f4 v[126:129], v[82:89], v[90:97], v[52:55], v165, v164 op_sel_hi:[0,0,0]
	v_mfma_scale_f32_16x16x128_f8f6f4 v[130:133], v[82:89], v[114:121], v[0:3], v165, v164 op_sel_hi:[0,0,0]
	s_setprio 0
	s_barrier
	s_nop 4
	v_add_u32_e32 v0, s78, v69
	v_add_u32_e32 v1, s78, v70
	ds_read_b128 v[48:51], v0
	ds_read_b128 v[74:77], v0 offset:2048
	ds_read_b128 v[52:55], v1
	ds_read_b128 v[78:81], v1 offset:2048
	s_mov_b32 m0, s39
	s_nop 0
	buffer_load_dwordx4 v66, s[4:7], s77 offen lds
	s_nop 0
	s_mov_b32 m0, s49
	s_nop 0
	buffer_load_dwordx4 v66, s[4:7], s79 offen lds
	s_waitcnt vmcnt(10)
	s_barrier
	s_nop 0
	s_setprio 1
	s_waitcnt lgkmcnt(1)
	v_mfma_scale_f32_16x16x128_f8f6f4 v[44:47], v[48:55], v[98:105], v[44:47], v165, v164 op_sel_hi:[0,0,0]
	s_waitcnt lgkmcnt(0)
	v_mfma_scale_f32_16x16x128_f8f6f4 v[36:39], v[74:81], v[98:105], v[36:39], v165, v164 op_sel_hi:[0,0,0]
	v_mfma_scale_f32_16x16x128_f8f6f4 v[28:31], v[48:55], v[106:113], v[28:31], v165, v164 op_sel_hi:[0,0,0]
	v_mfma_scale_f32_16x16x128_f8f6f4 v[20:23], v[74:81], v[106:113], v[20:23], v165, v164 op_sel_hi:[0,0,0]
	v_mfma_scale_f32_16x16x128_f8f6f4 v[12:15], v[48:55], v[114:121], v[12:15], v165, v164 op_sel_hi:[0,0,0]
	v_mfma_scale_f32_16x16x128_f8f6f4 v[134:137], v[48:55], v[90:97], v[60:63], v165, v164 op_sel_hi:[0,0,0]
	v_mfma_scale_f32_16x16x128_f8f6f4 v[138:141], v[74:81], v[90:97], v[56:59], v165, v164 op_sel_hi:[0,0,0]
	v_mfma_scale_f32_16x16x128_f8f6f4 v[142:145], v[74:81], v[114:121], v[4:7], v165, v164 op_sel_hi:[0,0,0]
	s_setprio 0
	s_barrier
	s_mov_b32 m0, s50
	s_nop 0
	buffer_load_dwordx4 v64, s[8:11], s77 offen lds
	s_nop 0
	s_mov_b32 m0, s51
	s_nop 0
	buffer_load_dwordx4 v67, s[8:11], s77 offen lds
	s_barrier
	s_waitcnt lgkmcnt(0)
	s_barrier
; #define G_WAIT_V(n) asm volatile("s_waitcnt vmcnt(" #n ")" ::: "memory")
; #define G_BAR() __builtin_amdgcn_s_barrier()
; #define G_SCHED() __builtin_amdgcn_sched_barrier(0)
; #define D_STAGE_A(slot, half, kt) D_STAGE(rsA, voffA, slot, half, kt)
; #define D_STAGE_B(slot, half, kt) D_STAGE(rsB, voffB, slot, half, kt)
; #define D_LDA(dst, slot) do { _Pragma("unroll") for (int m = 0; m < 4; ++m) _Pragma("unroll") for (int k = 0; k < 2; ++k) \
;     dst[m][k] = *(const LDS_AS bf16x8*)(lds + (slot) + aoff + m * 2048 + k * 1024); } while (0)
; #define D_LDB(dst, slot) do { _Pragma("unroll") for (int n = 0; n < 2; ++n) _Pragma("unroll") for (int k = 0; k < 2; ++k) \
;     dst[n][k] = *(const LDS_AS bf16x8*)(lds + (slot) + boff + n * 2048 + k * 1024); } while (0)
; #define D_WAIT_L(n) asm volatile("s_waitcnt lgkmcnt(" #n ")" ::: "memory")
; #define D_STAGE_A(slot, half, kt) D_STAGE(rsA, voffA, slot, half, kt)
; #define D_WAIT_L(n) asm volatile("s_waitcnt lgkmcnt(" #n ")" ::: "memory")
;     ...
;   for (int t = 0; t < (F8_PEEL ? nt - 2 : nt); t += 2) {
;     const int t1 = t + 1;
;     const int t2 = (F8_PEEL || t + 2 < nt) ? t + 2 : t;
;     const int t3 = (F8_PEEL || t + 2 < nt) ? t + 3 : t + 1;
;     D_LDB(B0, G_SB(0, 0)); G_SCHED(); D_LDA(At, G_SA(0, 0)); D_STAGE_A(G_SA(1, 1), 1, t1);
;     D_WAIT_L(8); G_BAR(); D_WAIT_L(0); G_SCHED(); D_MMA(0, 0, At, B0); G_BAR(); G_SCHED();
;     D_LDB(B1, G_SB(0, 1)); D_STAGE_B(G_SB(0, 0), 0, t2);
;     G_BAR(); D_WAIT_L(0); G_SCHED(); D_MMA(0, 1, At, B1); G_BAR(); G_SCHED();
;     D_LDA(At, G_SA(0, 1)); D_STAGE_A(G_SA(0, 0), 0, t2);
;     G_BAR(); D_WAIT_L(0); G_SCHED(); D_MMA(1, 0, At, B0); G_BAR(); G_SCHED();
;     D_STAGE_B(G_SB(0, 1), 1, t2);
;     G_WAIT_V(6); G_BAR(); G_SCHED(); D_MMA(1, 1, At, B1); G_BAR(); G_SCHED();
;     D_LDB(B0, G_SB(1, 0)); G_SCHED(); D_LDA(At, G_SA(1, 0)); D_STAGE_A(G_SA(0, 1), 1, t2);
;     D_WAIT_L(8); G_BAR(); D_WAIT_L(0); G_SCHED(); D_MMA(0, 0, At, B0); G_BAR(); G_SCHED();
;     D_LDB(B1, G_SB(1, 1)); D_STAGE_B(G_SB(1, 0), 0, t3);
;     G_BAR(); D_WAIT_L(0); G_SCHED(); D_MMA(0, 1, At, B1); G_BAR(); G_SCHED();
;     D_LDA(At, G_SA(1, 1)); D_STAGE_A(G_SA(1, 0), 0, t3);
;     G_BAR(); D_WAIT_L(0); G_SCHED(); D_MMA(1, 0, At, B0); G_BAR(); G_SCHED();
;     D_STAGE_B(G_SB(1, 1), 1, t3);
;     G_WAIT_V(6); G_BAR(); G_SCHED(); D_MMA(1, 1, At, B1); G_BAR(); G_SCHED();
;   }
	s_mov_b32 m0, s54
	s_nop 0
	buffer_load_dwordx4 v66, s[4:7], s80 offen lds
	s_nop 0
	s_mov_b32 m0, s55
	s_nop 0
	buffer_load_dwordx4 v66, s[4:7], s81 offen lds
	s_waitcnt vmcnt(10)
	s_barrier
	s_barrier
	v_add_u32_e32 v4, s82, v69
	v_add_u32_e32 v48, s82, v70
	ds_read_b128 v[0:3], v4
	ds_read_b128 v[56:59], v4 offset:2048
	ds_read_b128 v[4:7], v48
	ds_read_b128 v[60:63], v48 offset:2048
	ds_read_b128 v[74:77], v71 offset:32784
	ds_read_b128 v[82:85], v71 offset:34832
	ds_read_b128 v[78:81], v72 offset:32784
	ds_read_b128 v[86:89], v72 offset:34832
	ds_read_b128 v[90:93], v71 offset:36880
	ds_read_b128 v[98:101], v71 offset:38928
	ds_read_b128 v[94:97], v72 offset:36880
	ds_read_b128 v[102:105], v72 offset:38928
	s_mov_b32 m0, s58
	s_nop 0
	buffer_load_dwordx4 v65, s[8:11], s77 offen lds
	s_nop 0
	s_mov_b32 m0, s59
	s_nop 0
	buffer_load_dwordx4 v68, s[8:11], s77 offen lds
	s_waitcnt lgkmcnt(8)
	s_waitcnt vmcnt(10)
	s_barrier
	s_nop 0
	s_setprio 1
	s_waitcnt lgkmcnt(5)
	v_mfma_scale_f32_16x16x128_f8f6f4 v[48:51], v[0:7], v[74:81], v[122:125], v165, v164 op_sel_hi:[0,0,0]
	v_mfma_scale_f32_16x16x128_f8f6f4 v[52:55], v[56:63], v[74:81], v[126:129], v165, v164 op_sel_hi:[0,0,0]
	s_waitcnt lgkmcnt(4)
	v_mfma_scale_f32_16x16x128_f8f6f4 v[40:43], v[0:7], v[82:89], v[40:43], v165, v164 op_sel_hi:[0,0,0]
	v_mfma_scale_f32_16x16x128_f8f6f4 v[32:35], v[56:63], v[82:89], v[32:35], v165, v164 op_sel_hi:[0,0,0]
	s_waitcnt lgkmcnt(1)
	v_mfma_scale_f32_16x16x128_f8f6f4 v[24:27], v[0:7], v[90:97], v[24:27], v165, v164 op_sel_hi:[0,0,0]
	v_mfma_scale_f32_16x16x128_f8f6f4 v[16:19], v[56:63], v[90:97], v[16:19], v165, v164 op_sel_hi:[0,0,0]
	s_waitcnt lgkmcnt(0)
	v_mfma_scale_f32_16x16x128_f8f6f4 v[8:11], v[0:7], v[98:105], v[8:11], v165, v164 op_sel_hi:[0,0,0]
	v_mfma_scale_f32_16x16x128_f8f6f4 v[0:3], v[56:63], v[98:105], v[130:133], v165, v164 op_sel_hi:[0,0,0]
	s_setprio 0
	s_barrier
	v_add_u32_e32 v4, s76, v69
	v_add_u32_e32 v5, s76, v70
	ds_read_b128 v[106:109], v4
	ds_read_b128 v[114:117], v4 offset:2048
	ds_read_b128 v[110:113], v5
	ds_read_b128 v[118:121], v5 offset:2048
	s_mov_b32 m0, s60
	s_nop 0
	buffer_load_dwordx4 v66, s[4:7], s72 offen lds
	s_nop 0
	s_mov_b32 m0, s61
	s_nop 0
	buffer_load_dwordx4 v66, s[4:7], s75 offen lds
	s_waitcnt vmcnt(10)
	s_barrier
	s_nop 0
	s_setprio 1
	s_waitcnt lgkmcnt(1)
	v_mfma_scale_f32_16x16x128_f8f6f4 v[60:63], v[106:113], v[74:81], v[134:137], v165, v164 op_sel_hi:[0,0,0]
	s_waitcnt lgkmcnt(0)
	v_mfma_scale_f32_16x16x128_f8f6f4 v[56:59], v[114:121], v[74:81], v[138:141], v165, v164 op_sel_hi:[0,0,0]
	v_mfma_scale_f32_16x16x128_f8f6f4 v[44:47], v[106:113], v[82:89], v[44:47], v165, v164 op_sel_hi:[0,0,0]
	v_mfma_scale_f32_16x16x128_f8f6f4 v[36:39], v[114:121], v[82:89], v[36:39], v165, v164 op_sel_hi:[0,0,0]
	v_mfma_scale_f32_16x16x128_f8f6f4 v[28:31], v[106:113], v[90:97], v[28:31], v165, v164 op_sel_hi:[0,0,0]
	v_mfma_scale_f32_16x16x128_f8f6f4 v[20:23], v[114:121], v[90:97], v[20:23], v165, v164 op_sel_hi:[0,0,0]
	v_mfma_scale_f32_16x16x128_f8f6f4 v[12:15], v[106:113], v[98:105], v[12:15], v165, v164 op_sel_hi:[0,0,0]
	v_mfma_scale_f32_16x16x128_f8f6f4 v[4:7], v[114:121], v[98:105], v[142:145], v165, v164 op_sel_hi:[0,0,0]
	s_setprio 0
	s_barrier
	s_mov_b32 m0, s62
	s_nop 0
	buffer_load_dwordx4 v64, s[8:11], s72 offen lds
	s_nop 0
	s_mov_b32 m0, s63
	s_nop 0
	buffer_load_dwordx4 v67, s[8:11], s72 offen lds
	s_barrier
	s_waitcnt lgkmcnt(0)
	s_barrier
	s_mov_b32 m0, s64
	s_nop 0
	buffer_load_dwordx4 v66, s[4:7], s74 offen lds
	s_nop 0
	s_mov_b32 m0, s65
	s_nop 0
	buffer_load_dwordx4 v66, s[4:7], s73 offen lds
	s_waitcnt vmcnt(10)
	s_barrier
	s_barrier
	s_mov_b32 s69, s70
	s_mov_b32 s71, s68
	s_cbranch_scc0 .LBB0_1634
	s_waitcnt vmcnt(0)
	s_cmpk_lt_u32 s13, 0x100
	s_cbranch_scc0 .LBB0_1637
	s_barrier

; #define G_WAIT_V(n) asm volatile("s_waitcnt vmcnt(" #n ")" ::: "memory")
; #define G_BAR() __builtin_amdgcn_s_barrier()
; #define G_SCHED() __builtin_amdgcn_sched_barrier(0)
; #define D_STAGE_A(slot, half, kt) D_STAGE(rsA, voffA, slot, half, kt)
; #define D_STAGE_B(slot, half, kt) D_STAGE(rsB, voffB, slot, half, kt)
; #define D_LDA(dst, slot) do { _Pragma("unroll") for (int m = 0; m < 4; ++m) _Pragma("unroll") for (int k = 0; k < 2; ++k) \
;     dst[m][k] = *(const LDS_AS bf16x8*)(lds + (slot) + aoff + m * 2048 + k * 1024); } while (0)
; #define D_LDB(dst, slot) do { _Pragma("unroll") for (int n = 0; n < 2; ++n) _Pragma("unroll") for (int k = 0; k < 2; ++k) \
;     dst[n][k] = *(const LDS_AS bf16x8*)(lds + (slot) + boff + n * 2048 + k * 1024); } while (0)
; #define D_WAIT_L(n) asm volatile("s_waitcnt lgkmcnt(" #n ")" ::: "memory")
; #define D_STAGE_A(slot, half, kt) D_STAGE(rsA, voffA, slot, half, kt)
; #define D_WAIT_L(n) asm volatile("s_waitcnt lgkmcnt(" #n ")" ::: "memory")
;     ...
;   for (int t = 0; t < (F8_PEEL ? nt - 2 : nt); t += 2) {
;     const int t1 = t + 1;
;     const int t2 = (F8_PEEL || t + 2 < nt) ? t + 2 : t;
;     const int t3 = (F8_PEEL || t + 2 < nt) ? t + 3 : t + 1;
;     D_LDB(B0, G_SB(0, 0)); G_SCHED(); D_LDA(At, G_SA(0, 0)); D_STAGE_A(G_SA(1, 1), 1, t1);
;     D_WAIT_L(8); G_BAR(); D_WAIT_L(0); G_SCHED(); D_MMA(0, 0, At, B0); G_BAR(); G_SCHED();
;     D_LDB(B1, G_SB(0, 1)); D_STAGE_B(G_SB(0, 0), 0, t2);
;     G_BAR(); D_WAIT_L(0); G_SCHED(); D_MMA(0, 1, At, B1); G_BAR(); G_SCHED();
;     D_LDA(At, G_SA(0, 1)); D_STAGE_A(G_SA(0, 0), 0, t2);
;     G_BAR(); D_WAIT_L(0); G_SCHED(); D_MMA(1, 0, At, B0); G_BAR(); G_SCHED();
;     D_STAGE_B(G_SB(0, 1), 1, t2);
;     G_WAIT_V(6); G_BAR(); G_SCHED(); D_MMA(1, 1, At, B1); G_BAR(); G_SCHED();
;     D_LDB(B0, G_SB(1, 0)); G_SCHED(); D_LDA(At, G_SA(1, 0)); D_STAGE_A(G_SA(0, 1), 1, t2);
;     D_WAIT_L(8); G_BAR(); D_WAIT_L(0); G_SCHED(); D_MMA(0, 0, At, B0); G_BAR(); G_SCHED();
;     D_LDB(B1, G_SB(1, 1)); D_STAGE_B(G_SB(1, 0), 0, t3);
;     G_BAR(); D_WAIT_L(0); G_SCHED(); D_MMA(0, 1, At, B1); G_BAR(); G_SCHED();
;     D_LDA(At, G_SA(1, 1)); D_STAGE_A(G_SA(1, 0), 0, t3);
;     G_BAR(); D_WAIT_L(0); G_SCHED(); D_MMA(1, 0, At, B0); G_BAR(); G_SCHED();
;     D_STAGE_B(G_SB(1, 1), 1, t3);
;     G_WAIT_V(6); G_BAR(); G_SCHED(); D_MMA(1, 1, At, B1); G_BAR(); G_SCHED();
;   }
.LBB0_1674:
	s_add_i32 s68, 0, 0x10010
	s_nop 0
	v_add_u32_e32 v68, s68, v132
	v_add_u32_e32 v69, s68, v133
	ds_read_b128 v[146:149], v68
	ds_read_b128 v[154:157], v68 offset:2048
	ds_read_b128 v[150:153], v69
	ds_read_b128 v[158:161], v69 offset:2048
	s_add_i32 s38, s64, 1
	s_add_i32 s66, s64, 3
	s_add_i32 s65, s64, 2
	s_add_i32 s76, 0, 0x14010
	s_cmp_lt_u32 s64, 14
	s_cselect_b32 s67, s65, s64
	s_cselect_b32 s38, s66, s38
	s_lshl_b32 s72, s67, 7
	s_lshl_b32 s67, s38, 7
	s_add_i32 s77, s72, 0x20000
	s_add_i32 s74, s72, 0x40000
	s_add_i32 s75, s72, 0x60000
	s_add_i32 s73, 0, 0x18010
	s_add_i32 s71, 0, 0x1c010
	s_add_i32 s70, s67, 0x20000
	s_add_i32 s68, s67, 0x40000
	s_add_i32 s69, s67, 0x60000
	s_add_i32 s66, s63, 0x100
	s_cmp_gt_u32 s64, 13
	ds_read_b128 v[168:171], v135 offset:16
	ds_read_b128 v[176:179], v135 offset:2064
	ds_read_b128 v[172:175], v136 offset:16
	ds_read_b128 v[180:183], v136 offset:2064
	ds_read_b128 v[192:195], v135 offset:4112
	ds_read_b128 v[200:203], v135 offset:6160
	ds_read_b128 v[196:199], v136 offset:4112
	ds_read_b128 v[204:207], v136 offset:6160
	s_waitcnt lgkmcnt(12)
	s_mov_b32 m0, s24
	s_nop 0
	buffer_load_dwordx4 v166, s[8:11], s63 offen lds
	s_nop 0
	s_mov_b32 m0, s51
	s_nop 0
	buffer_load_dwordx4 v167, s[8:11], s63 offen lds
	s_waitcnt lgkmcnt(8)
	s_waitcnt vmcnt(10)
	s_barrier
	s_nop 0
	s_setprio 1
	s_waitcnt lgkmcnt(0)
	v_mfma_scale_f32_16x16x128_f8f6f4 v[220:223], v[146:153], v[200:207], v[220:223], v165, v164 op_sel_hi:[0,0,0]
	v_mfma_scale_f32_16x16x128_f8f6f4 v[48:51], v[154:161], v[200:207], v[48:51], v165, v164 op_sel_hi:[0,0,0]
	v_mfma_scale_f32_16x16x128_f8f6f4 v[138:141], v[146:153], v[168:175], v[124:127], v165, v164 op_sel_hi:[0,0,0]
	v_mfma_scale_f32_16x16x128_f8f6f4 v[184:187], v[154:161], v[168:175], v[120:123], v165, v164 op_sel_hi:[0,0,0]
	v_mfma_scale_f32_16x16x128_f8f6f4 v[188:191], v[146:153], v[176:183], v[108:111], v165, v164 op_sel_hi:[0,0,0]
	v_mfma_scale_f32_16x16x128_f8f6f4 v[208:211], v[154:161], v[176:183], v[100:103], v165, v164 op_sel_hi:[0,0,0]
	v_mfma_scale_f32_16x16x128_f8f6f4 v[212:215], v[146:153], v[192:199], v[84:87], v165, v164 op_sel_hi:[0,0,0]
	v_mfma_scale_f32_16x16x128_f8f6f4 v[216:219], v[154:161], v[192:199], v[80:83], v165, v164 op_sel_hi:[0,0,0]
	s_setprio 0
	s_barrier
	v_add_u32_e32 v68, s76, v132
	v_add_u32_e32 v69, s76, v133
	s_nop 2
	ds_read_b128 v[80:83], v68
	ds_read_b128 v[120:123], v68 offset:2048
	ds_read_b128 v[84:87], v69
	ds_read_b128 v[124:127], v69 offset:2048
	s_mov_b32 m0, s25
	s_nop 0
	buffer_load_dwordx4 v134, s[4:7], s72 offen lds
	s_nop 0
	s_mov_b32 m0, s54
	s_nop 0
	buffer_load_dwordx4 v134, s[4:7], s77 offen lds
	s_waitcnt vmcnt(10)
	s_barrier
	s_nop 0
	s_setprio 1
	s_waitcnt lgkmcnt(1)
	v_mfma_scale_f32_16x16x128_f8f6f4 v[116:119], v[80:87], v[168:175], v[116:119], v165, v164 op_sel_hi:[0,0,0]
	s_waitcnt lgkmcnt(0)
	v_mfma_scale_f32_16x16x128_f8f6f4 v[112:115], v[120:127], v[168:175], v[112:115], v165, v164 op_sel_hi:[0,0,0]
	v_mfma_scale_f32_16x16x128_f8f6f4 v[76:79], v[80:87], v[200:207], v[76:79], v165, v164 op_sel_hi:[0,0,0]
	v_mfma_scale_f32_16x16x128_f8f6f4 v[168:171], v[80:87], v[176:183], v[104:107], v165, v164 op_sel_hi:[0,0,0]
	v_mfma_scale_f32_16x16x128_f8f6f4 v[172:175], v[120:127], v[176:183], v[96:99], v165, v164 op_sel_hi:[0,0,0]
	v_mfma_scale_f32_16x16x128_f8f6f4 v[176:179], v[80:87], v[192:199], v[92:95], v165, v164 op_sel_hi:[0,0,0]
	v_mfma_scale_f32_16x16x128_f8f6f4 v[180:183], v[120:127], v[192:199], v[88:91], v165, v164 op_sel_hi:[0,0,0]
	v_mfma_scale_f32_16x16x128_f8f6f4 v[192:195], v[120:127], v[200:207], v[72:75], v165, v164 op_sel_hi:[0,0,0]
	s_setprio 0
	s_barrier
	ds_read_b128 v[68:71], v135 offset:16400
	s_nop 2
	ds_read_b128 v[88:91], v135 offset:18448
	ds_read_b128 v[72:75], v136 offset:16400
	ds_read_b128 v[92:95], v136 offset:18448
	ds_read_b128 v[96:99], v135 offset:20496
	ds_read_b128 v[104:107], v135 offset:22544
	ds_read_b128 v[100:103], v136 offset:20496
	ds_read_b128 v[108:111], v136 offset:22544
	s_mov_b32 m0, s15
	s_nop 0
	buffer_load_dwordx4 v162, s[8:11], s72 offen lds
	s_nop 0
	s_mov_b32 m0, s55
	s_nop 0
	buffer_load_dwordx4 v163, s[8:11], s72 offen lds
	s_barrier
	s_nop 0
	s_setprio 1
	s_waitcnt lgkmcnt(5)
	v_mfma_scale_f32_16x16x128_f8f6f4 v[56:59], v[146:153], v[68:75], v[56:59], v165, v164 op_sel_hi:[0,0,0]
	v_mfma_scale_f32_16x16x128_f8f6f4 v[52:55], v[154:161], v[68:75], v[52:55], v165, v164 op_sel_hi:[0,0,0]
	s_waitcnt lgkmcnt(4)
	v_mfma_scale_f32_16x16x128_f8f6f4 v[200:203], v[146:153], v[88:95], v[36:39], v165, v164 op_sel_hi:[0,0,0]
	v_mfma_scale_f32_16x16x128_f8f6f4 v[204:207], v[154:161], v[88:95], v[32:35], v165, v164 op_sel_hi:[0,0,0]
	s_waitcnt lgkmcnt(1)
	v_mfma_scale_f32_16x16x128_f8f6f4 v[224:227], v[146:153], v[96:103], v[20:23], v165, v164 op_sel_hi:[0,0,0]
	v_mfma_scale_f32_16x16x128_f8f6f4 v[228:231], v[154:161], v[96:103], v[16:19], v165, v164 op_sel_hi:[0,0,0]
	s_waitcnt lgkmcnt(0)
	v_mfma_scale_f32_16x16x128_f8f6f4 v[232:235], v[146:153], v[104:111], v[4:7], v165, v164 op_sel_hi:[0,0,0]
	v_mfma_scale_f32_16x16x128_f8f6f4 v[236:239], v[154:161], v[104:111], v[0:3], v165, v164 op_sel_hi:[0,0,0]
	s_setprio 0
	s_barrier
	s_mov_b32 m0, s26
	s_nop 0
	buffer_load_dwordx4 v134, s[4:7], s74 offen lds
	s_nop 0
	s_mov_b32 m0, s58
	s_nop 0
	buffer_load_dwordx4 v134, s[4:7], s75 offen lds
	s_waitcnt vmcnt(10)
	s_barrier
; #define G_WAIT_V(n) asm volatile("s_waitcnt vmcnt(" #n ")" ::: "memory")
; #define G_BAR() __builtin_amdgcn_s_barrier()
; #define G_SCHED() __builtin_amdgcn_sched_barrier(0)
; #define D_STAGE_A(slot, half, kt) D_STAGE(rsA, voffA, slot, half, kt)
; #define D_STAGE_B(slot, half, kt) D_STAGE(rsB, voffB, slot, half, kt)
; #define D_LDA(dst, slot) do { _Pragma("unroll") for (int m = 0; m < 4; ++m) _Pragma("unroll") for (int k = 0; k < 2; ++k) \
;     dst[m][k] = *(const LDS_AS bf16x8*)(lds + (slot) + aoff + m * 2048 + k * 1024); } while (0)
; #define D_LDB(dst, slot) do { _Pragma("unroll") for (int n = 0; n < 2; ++n) _Pragma("unroll") for (int k = 0; k < 2; ++k) \
;     dst[n][k] = *(const LDS_AS bf16x8*)(lds + (slot) + boff + n * 2048 + k * 1024); } while (0)
; #define D_WAIT_L(n) asm volatile("s_waitcnt lgkmcnt(" #n ")" ::: "memory")
; #define D_STAGE_A(slot, half, kt) D_STAGE(rsA, voffA, slot, half, kt)
; #define D_WAIT_L(n) asm volatile("s_waitcnt lgkmcnt(" #n ")" ::: "memory")
;     ...
;   for (int t = 0; t < (F8_PEEL ? nt - 2 : nt); t += 2) {
;     const int t1 = t + 1;
;     const int t2 = (F8_PEEL || t + 2 < nt) ? t + 2 : t;
;     const int t3 = (F8_PEEL || t + 2 < nt) ? t + 3 : t + 1;
;     D_LDB(B0, G_SB(0, 0)); G_SCHED(); D_LDA(At, G_SA(0, 0)); D_STAGE_A(G_SA(1, 1), 1, t1);
;     D_WAIT_L(8); G_BAR(); D_WAIT_L(0); G_SCHED(); D_MMA(0, 0, At, B0); G_BAR(); G_SCHED();
;     D_LDB(B1, G_SB(0, 1)); D_STAGE_B(G_SB(0, 0), 0, t2);
;     G_BAR(); D_WAIT_L(0); G_SCHED(); D_MMA(0, 1, At, B1); G_BAR(); G_SCHED();
;     D_LDA(At, G_SA(0, 1)); D_STAGE_A(G_SA(0, 0), 0, t2);
;     G_BAR(); D_WAIT_L(0); G_SCHED(); D_MMA(1, 0, At, B0); G_BAR(); G_SCHED();
;     D_STAGE_B(G_SB(0, 1), 1, t2);
;     G_WAIT_V(6); G_BAR(); G_SCHED(); D_MMA(1, 1, At, B1); G_BAR(); G_SCHED();
;     D_LDB(B0, G_SB(1, 0)); G_SCHED(); D_LDA(At, G_SA(1, 0)); D_STAGE_A(G_SA(0, 1), 1, t2);
;     D_WAIT_L(8); G_BAR(); D_WAIT_L(0); G_SCHED(); D_MMA(0, 0, At, B0); G_BAR(); G_SCHED();
;     D_LDB(B1, G_SB(1, 1)); D_STAGE_B(G_SB(1, 0), 0, t3);
;     G_BAR(); D_WAIT_L(0); G_SCHED(); D_MMA(0, 1, At, B1); G_BAR(); G_SCHED();
;     D_LDA(At, G_SA(1, 1)); D_STAGE_A(G_SA(1, 0), 0, t3);
;     G_BAR(); D_WAIT_L(0); G_SCHED(); D_MMA(1, 0, At, B0); G_BAR(); G_SCHED();
;     D_STAGE_B(G_SB(1, 1), 1, t3);
;     G_WAIT_V(6); G_BAR(); G_SCHED(); D_MMA(1, 1, At, B1); G_BAR(); G_SCHED();
;   }
	s_setprio 1
	v_mfma_scale_f32_16x16x128_f8f6f4 v[64:67], v[80:87], v[68:75], v[64:67], v165, v164 op_sel_hi:[0,0,0]
	v_mfma_scale_f32_16x16x128_f8f6f4 v[60:63], v[120:127], v[68:75], v[60:63], v165, v164 op_sel_hi:[0,0,0]
	v_mfma_scale_f32_16x16x128_f8f6f4 v[240:243], v[80:87], v[88:95], v[44:47], v165, v164 op_sel_hi:[0,0,0]
	v_mfma_scale_f32_16x16x128_f8f6f4 v[244:247], v[120:127], v[88:95], v[40:43], v165, v164 op_sel_hi:[0,0,0]
	v_mfma_scale_f32_16x16x128_f8f6f4 v[248:251], v[80:87], v[96:103], v[28:31], v165, v164 op_sel_hi:[0,0,0]
	v_mfma_scale_f32_16x16x128_f8f6f4 v[142:145], v[120:127], v[96:103], v[24:27], v165, v164 op_sel_hi:[0,0,0]
	v_mfma_scale_f32_16x16x128_f8f6f4 v[128:131], v[80:87], v[104:111], v[12:15], v165, v164 op_sel_hi:[0,0,0]
	v_mfma_scale_f32_16x16x128_f8f6f4 v[68:71], v[120:127], v[104:111], v[8:11], v165, v164 op_sel_hi:[0,0,0]
	s_setprio 0
	s_barrier
	v_add_u32_e32 v4, s73, v132
	s_nop 2
	v_add_u32_e32 v12, s73, v133
	ds_read_b128 v[0:3], v4
	ds_read_b128 v[8:11], v4 offset:2048
	ds_read_b128 v[4:7], v12
	ds_read_b128 v[12:15], v12 offset:2048
	ds_read_b128 v[16:19], v135 offset:32784
	ds_read_b128 v[24:27], v135 offset:34832
	ds_read_b128 v[20:23], v136 offset:32784
	ds_read_b128 v[28:31], v136 offset:34832
	ds_read_b128 v[32:35], v135 offset:36880
	ds_read_b128 v[40:43], v135 offset:38928
	ds_read_b128 v[36:39], v136 offset:36880
	ds_read_b128 v[44:47], v136 offset:38928
	s_mov_b32 m0, s27
	s_nop 0
	buffer_load_dwordx4 v166, s[8:11], s72 offen lds
	s_nop 0
	s_mov_b32 m0, s59
	s_nop 0
	buffer_load_dwordx4 v167, s[8:11], s72 offen lds
	s_waitcnt lgkmcnt(8)
	s_waitcnt vmcnt(10)
	s_barrier
	s_nop 0
	s_setprio 1
	s_waitcnt lgkmcnt(5)
	v_mfma_scale_f32_16x16x128_f8f6f4 v[124:127], v[0:7], v[16:23], v[138:141], v165, v164 op_sel_hi:[0,0,0]
	v_mfma_scale_f32_16x16x128_f8f6f4 v[120:123], v[8:15], v[16:23], v[184:187], v165, v164 op_sel_hi:[0,0,0]
	s_waitcnt lgkmcnt(4)
	v_mfma_scale_f32_16x16x128_f8f6f4 v[108:111], v[0:7], v[24:31], v[188:191], v165, v164 op_sel_hi:[0,0,0]
	v_mfma_scale_f32_16x16x128_f8f6f4 v[100:103], v[8:15], v[24:31], v[208:211], v165, v164 op_sel_hi:[0,0,0]
	s_waitcnt lgkmcnt(1)
	v_mfma_scale_f32_16x16x128_f8f6f4 v[84:87], v[0:7], v[32:39], v[212:215], v165, v164 op_sel_hi:[0,0,0]
	v_mfma_scale_f32_16x16x128_f8f6f4 v[80:83], v[8:15], v[32:39], v[216:219], v165, v164 op_sel_hi:[0,0,0]
	s_waitcnt lgkmcnt(0)
	v_mfma_scale_f32_16x16x128_f8f6f4 v[220:223], v[0:7], v[40:47], v[220:223], v165, v164 op_sel_hi:[0,0,0]
	v_mfma_scale_f32_16x16x128_f8f6f4 v[48:51], v[8:15], v[40:47], v[48:51], v165, v164 op_sel_hi:[0,0,0]
	s_setprio 0
	s_barrier
	v_add_u32_e32 v72, s71, v132
	v_add_u32_e32 v73, s71, v133
	ds_read_b128 v[146:149], v72
	ds_read_b128 v[154:157], v72 offset:2048
	ds_read_b128 v[150:153], v73
	ds_read_b128 v[158:161], v73 offset:2048
	s_mov_b32 m0, s39
	s_nop 0
	buffer_load_dwordx4 v134, s[4:7], s67 offen lds
	s_nop 0
	s_mov_b32 m0, s60
	s_nop 0
	buffer_load_dwordx4 v134, s[4:7], s70 offen lds
	s_waitcnt vmcnt(10)
	s_barrier
	s_nop 0
	s_setprio 1
	s_waitcnt lgkmcnt(1)
	v_mfma_scale_f32_16x16x128_f8f6f4 v[116:119], v[146:153], v[16:23], v[116:119], v165, v164 op_sel_hi:[0,0,0]
	s_waitcnt lgkmcnt(0)
	v_mfma_scale_f32_16x16x128_f8f6f4 v[112:115], v[154:161], v[16:23], v[112:115], v165, v164 op_sel_hi:[0,0,0]
	v_mfma_scale_f32_16x16x128_f8f6f4 v[104:107], v[146:153], v[24:31], v[168:171], v165, v164 op_sel_hi:[0,0,0]
	v_mfma_scale_f32_16x16x128_f8f6f4 v[96:99], v[154:161], v[24:31], v[172:175], v165, v164 op_sel_hi:[0,0,0]
	v_mfma_scale_f32_16x16x128_f8f6f4 v[92:95], v[146:153], v[32:39], v[176:179], v165, v164 op_sel_hi:[0,0,0]
	v_mfma_scale_f32_16x16x128_f8f6f4 v[88:91], v[154:161], v[32:39], v[180:183], v165, v164 op_sel_hi:[0,0,0]
	v_mfma_scale_f32_16x16x128_f8f6f4 v[76:79], v[146:153], v[40:47], v[76:79], v165, v164 op_sel_hi:[0,0,0]
	v_mfma_scale_f32_16x16x128_f8f6f4 v[72:75], v[154:161], v[40:47], v[192:195], v165, v164 op_sel_hi:[0,0,0]
	s_setprio 0
	s_barrier
	ds_read_b128 v[24:27], v135 offset:49168
	ds_read_b128 v[168:171], v135 offset:51216
	ds_read_b128 v[28:31], v136 offset:49168
	ds_read_b128 v[172:175], v136 offset:51216
	ds_read_b128 v[176:179], v135 offset:53264
	ds_read_b128 v[192:195], v135 offset:55312
	ds_read_b128 v[180:183], v136 offset:53264
	ds_read_b128 v[196:199], v136 offset:55312
	s_mov_b32 m0, s49
	s_nop 0
	buffer_load_dwordx4 v162, s[8:11], s67 offen lds
	s_nop 0
	s_mov_b32 m0, s61
	s_nop 0
	buffer_load_dwordx4 v163, s[8:11], s67 offen lds
	s_barrier
	s_nop 0
	s_setprio 1
	s_waitcnt lgkmcnt(5)
	v_mfma_scale_f32_16x16x128_f8f6f4 v[56:59], v[0:7], v[24:31], v[56:59], v165, v164 op_sel_hi:[0,0,0]
	v_mfma_scale_f32_16x16x128_f8f6f4 v[52:55], v[8:15], v[24:31], v[52:55], v165, v164 op_sel_hi:[0,0,0]
	s_waitcnt lgkmcnt(4)
	v_mfma_scale_f32_16x16x128_f8f6f4 v[36:39], v[0:7], v[168:175], v[200:203], v165, v164 op_sel_hi:[0,0,0]
	v_mfma_scale_f32_16x16x128_f8f6f4 v[32:35], v[8:15], v[168:175], v[204:207], v165, v164 op_sel_hi:[0,0,0]
	s_waitcnt lgkmcnt(1)
	v_mfma_scale_f32_16x16x128_f8f6f4 v[20:23], v[0:7], v[176:183], v[224:227], v165, v164 op_sel_hi:[0,0,0]
	v_mfma_scale_f32_16x16x128_f8f6f4 v[16:19], v[8:15], v[176:183], v[228:231], v165, v164 op_sel_hi:[0,0,0]
	s_waitcnt lgkmcnt(0)
	v_mfma_scale_f32_16x16x128_f8f6f4 v[4:7], v[0:7], v[192:199], v[232:235], v165, v164 op_sel_hi:[0,0,0]
	v_mfma_scale_f32_16x16x128_f8f6f4 v[0:3], v[8:15], v[192:199], v[236:239], v165, v164 op_sel_hi:[0,0,0]
	s_setprio 0
	s_barrier
	s_mov_b32 m0, s50
	s_nop 0
	buffer_load_dwordx4 v134, s[4:7], s68 offen lds
	s_nop 0
	s_mov_b32 m0, s62
	s_nop 0
	buffer_load_dwordx4 v134, s[4:7], s69 offen lds
	s_waitcnt vmcnt(10)
	s_barrier
	s_setprio 1
	v_mfma_scale_f32_16x16x128_f8f6f4 v[64:67], v[146:153], v[24:31], v[64:67], v165, v164 op_sel_hi:[0,0,0]
	v_mfma_scale_f32_16x16x128_f8f6f4 v[60:63], v[154:161], v[24:31], v[60:63], v165, v164 op_sel_hi:[0,0,0]
	v_mfma_scale_f32_16x16x128_f8f6f4 v[44:47], v[146:153], v[168:175], v[240:243], v165, v164 op_sel_hi:[0,0,0]
	v_mfma_scale_f32_16x16x128_f8f6f4 v[40:43], v[154:161], v[168:175], v[244:247], v165, v164 op_sel_hi:[0,0,0]
	v_mfma_scale_f32_16x16x128_f8f6f4 v[28:31], v[146:153], v[176:183], v[248:251], v165, v164 op_sel_hi:[0,0,0]
	v_mfma_scale_f32_16x16x128_f8f6f4 v[24:27], v[154:161], v[176:183], v[142:145], v165, v164 op_sel_hi:[0,0,0]
	v_mfma_scale_f32_16x16x128_f8f6f4 v[12:15], v[146:153], v[192:199], v[128:131], v165, v164 op_sel_hi:[0,0,0]
	v_mfma_scale_f32_16x16x128_f8f6f4 v[8:11], v[154:161], v[192:199], v[68:71], v165, v164 op_sel_hi:[0,0,0]
	s_setprio 0
	s_barrier
	s_mov_b32 s63, s66
	s_mov_b32 s64, s65
	s_cbranch_scc0 .LBB0_1674
	s_waitcnt vmcnt(0)
	s_cmpk_lt_u32 s13, 0x100
	s_cbranch_scc0 .LBB0_1677
	s_barrier

; #define G_WAIT_V(n) asm volatile("s_waitcnt vmcnt(" #n ")" ::: "memory")
; #define G_BAR() __builtin_amdgcn_s_barrier()
; #define G_SCHED() __builtin_amdgcn_sched_barrier(0)
; #define D_STAGE_A(slot, half, kt) D_STAGE(rsA, voffA, slot, half, kt)
; #define D_STAGE_B(slot, half, kt) D_STAGE(rsB, voffB, slot, half, kt)
; #define D_LDA(dst, slot) do { _Pragma("unroll") for (int m = 0; m < 4; ++m) _Pragma("unroll") for (int k = 0; k < 2; ++k) \
;     dst[m][k] = *(const LDS_AS bf16x8*)(lds + (slot) + aoff + m * 2048 + k * 1024); } while (0)
; #define D_LDB(dst, slot) do { _Pragma("unroll") for (int n = 0; n < 2; ++n) _Pragma("unroll") for (int k = 0; k < 2; ++k) \
;     dst[n][k] = *(const LDS_AS bf16x8*)(lds + (slot) + boff + n * 2048 + k * 1024); } while (0)
; #define D_WAIT_L(n) asm volatile("s_waitcnt lgkmcnt(" #n ")" ::: "memory")
; #define D_STAGE_A(slot, half, kt) D_STAGE(rsA, voffA, slot, half, kt)
; #define D_WAIT_L(n) asm volatile("s_waitcnt lgkmcnt(" #n ")" ::: "memory")
;     ...
;   for (int t = 0; t < (F8_PEEL ? nt - 2 : nt); t += 2) {
;     const int t1 = t + 1;
;     const int t2 = (F8_PEEL || t + 2 < nt) ? t + 2 : t;
;     const int t3 = (F8_PEEL || t + 2 < nt) ? t + 3 : t + 1;
;     D_LDB(B0, G_SB(0, 0)); G_SCHED(); D_LDA(At, G_SA(0, 0)); D_STAGE_A(G_SA(1, 1), 1, t1);
;     D_WAIT_L(8); G_BAR(); D_WAIT_L(0); G_SCHED(); D_MMA(0, 0, At, B0); G_BAR(); G_SCHED();
;     D_LDB(B1, G_SB(0, 1)); D_STAGE_B(G_SB(0, 0), 0, t2);
;     G_BAR(); D_WAIT_L(0); G_SCHED(); D_MMA(0, 1, At, B1); G_BAR(); G_SCHED();
;     D_LDA(At, G_SA(0, 1)); D_STAGE_A(G_SA(0, 0), 0, t2);
;     G_BAR(); D_WAIT_L(0); G_SCHED(); D_MMA(1, 0, At, B0); G_BAR(); G_SCHED();
;     D_STAGE_B(G_SB(0, 1), 1, t2);
;     G_WAIT_V(6); G_BAR(); G_SCHED(); D_MMA(1, 1, At, B1); G_BAR(); G_SCHED();
;     D_LDB(B0, G_SB(1, 0)); G_SCHED(); D_LDA(At, G_SA(1, 0)); D_STAGE_A(G_SA(0, 1), 1, t2);
;     D_WAIT_L(8); G_BAR(); D_WAIT_L(0); G_SCHED(); D_MMA(0, 0, At, B0); G_BAR(); G_SCHED();
;     D_LDB(B1, G_SB(1, 1)); D_STAGE_B(G_SB(1, 0), 0, t3);
;     G_BAR(); D_WAIT_L(0); G_SCHED(); D_MMA(0, 1, At, B1); G_BAR(); G_SCHED();
;     D_LDA(At, G_SA(1, 1)); D_STAGE_A(G_SA(1, 0), 0, t3);
;     G_BAR(); D_WAIT_L(0); G_SCHED(); D_MMA(1, 0, At, B0); G_BAR(); G_SCHED();
;     D_STAGE_B(G_SB(1, 1), 1, t3);
;     G_WAIT_V(6); G_BAR(); G_SCHED(); D_MMA(1, 1, At, B1); G_BAR(); G_SCHED();
;   }
.LBB0_1701:
	s_add_i32 s68, 0, 0x10010
	s_waitcnt vmcnt(62)
	v_add_u32_e32 v73, s68, v68
	s_waitcnt vmcnt(49)
	v_add_u32_e32 v86, s68, v69
	ds_read_b128 v[74:77], v73
	ds_read_b128 v[82:85], v73 offset:2048
	ds_read_b128 v[78:81], v86
	s_waitcnt vmcnt(46)
	ds_read_b128 v[86:89], v86 offset:2048
	s_add_i32 s38, s66, 1
	s_add_i32 s65, s66, 3
	s_add_i32 s64, s66, 2
	s_add_i32 s73, 0, 0x14010
	s_cmp_lt_u32 s66, 14
	s_cselect_b32 s67, s64, s66
	s_cselect_b32 s38, s65, s38
	s_lshl_b32 s72, s67, 7
	s_lshl_b32 s67, s38, 7
	s_add_i32 s74, s72, 0x20000
	s_add_i32 s75, s72, 0x40000
	s_add_i32 s76, s72, 0x60000
	s_add_i32 s77, 0, 0x18010
	s_add_i32 s71, 0, 0x1c010
	s_add_i32 s70, s67, 0x20000
	s_add_i32 s68, s67, 0x40000
	s_add_i32 s69, s67, 0x60000
	s_add_i32 s65, s63, 0x100
	s_cmp_gt_u32 s66, 13
	s_waitcnt vmcnt(42)
	ds_read_b128 v[90:93], v71 offset:16
	s_waitcnt vmcnt(34)
	ds_read_b128 v[98:101], v71 offset:2064
	ds_read_b128 v[94:97], v72 offset:16
	s_waitcnt vmcnt(30)
	ds_read_b128 v[102:105], v72 offset:2064
	s_waitcnt vmcnt(26)
	ds_read_b128 v[106:109], v71 offset:4112
	s_waitcnt vmcnt(18)
	ds_read_b128 v[114:117], v71 offset:6160
	ds_read_b128 v[110:113], v72 offset:4112
	s_waitcnt vmcnt(2)
	ds_read_b128 v[118:121], v72 offset:6160
	s_waitcnt lgkmcnt(12)
	s_mov_b32 m0, s24
	s_nop 0
	buffer_load_dwordx4 v66, s[8:11], s63 offen lds
	s_nop 0
	s_mov_b32 m0, s51
	s_nop 0
	buffer_load_dwordx4 v67, s[8:11], s63 offen lds
	s_waitcnt lgkmcnt(8)
	s_waitcnt vmcnt(10)
	s_barrier
	s_nop 0
	s_setprio 1
	s_waitcnt lgkmcnt(4)
	v_mfma_scale_f32_16x16x128_f8f6f4 v[40:43], v[74:81], v[98:105], v[40:43], v165, v164 op_sel_hi:[0,0,0]
	v_mfma_scale_f32_16x16x128_f8f6f4 v[32:35], v[82:89], v[98:105], v[32:35], v165, v164 op_sel_hi:[0,0,0]
	s_waitcnt lgkmcnt(1)
	v_mfma_scale_f32_16x16x128_f8f6f4 v[24:27], v[74:81], v[106:113], v[24:27], v165, v164 op_sel_hi:[0,0,0]
	v_mfma_scale_f32_16x16x128_f8f6f4 v[16:19], v[82:89], v[106:113], v[16:19], v165, v164 op_sel_hi:[0,0,0]
	s_waitcnt lgkmcnt(0)
	v_mfma_scale_f32_16x16x128_f8f6f4 v[8:11], v[74:81], v[114:121], v[8:11], v165, v164 op_sel_hi:[0,0,0]
	s_waitcnt vmcnt(0)
	v_mfma_scale_f32_16x16x128_f8f6f4 v[122:125], v[74:81], v[90:97], v[48:51], v165, v164 op_sel_hi:[0,0,0]
	v_mfma_scale_f32_16x16x128_f8f6f4 v[126:129], v[82:89], v[90:97], v[52:55], v165, v164 op_sel_hi:[0,0,0]
	v_mfma_scale_f32_16x16x128_f8f6f4 v[130:133], v[82:89], v[114:121], v[0:3], v165, v164 op_sel_hi:[0,0,0]
	s_setprio 0
	s_barrier
	s_nop 4
	v_add_u32_e32 v0, s73, v68
	v_add_u32_e32 v1, s73, v69
	ds_read_b128 v[48:51], v0
	ds_read_b128 v[74:77], v0 offset:2048
	ds_read_b128 v[52:55], v1
	ds_read_b128 v[78:81], v1 offset:2048
	s_mov_b32 m0, s25
	s_nop 0
	buffer_load_dwordx4 v70, s[4:7], s72 offen lds
	s_nop 0
	s_mov_b32 m0, s54
	s_nop 0
	buffer_load_dwordx4 v70, s[4:7], s74 offen lds
	s_waitcnt vmcnt(10)
	s_barrier
	s_nop 0
	s_setprio 1
	s_waitcnt lgkmcnt(1)
	v_mfma_scale_f32_16x16x128_f8f6f4 v[44:47], v[48:55], v[98:105], v[44:47], v165, v164 op_sel_hi:[0,0,0]
	s_waitcnt lgkmcnt(0)
	v_mfma_scale_f32_16x16x128_f8f6f4 v[36:39], v[74:81], v[98:105], v[36:39], v165, v164 op_sel_hi:[0,0,0]
	v_mfma_scale_f32_16x16x128_f8f6f4 v[28:31], v[48:55], v[106:113], v[28:31], v165, v164 op_sel_hi:[0,0,0]
	v_mfma_scale_f32_16x16x128_f8f6f4 v[20:23], v[74:81], v[106:113], v[20:23], v165, v164 op_sel_hi:[0,0,0]
	v_mfma_scale_f32_16x16x128_f8f6f4 v[12:15], v[48:55], v[114:121], v[12:15], v165, v164 op_sel_hi:[0,0,0]
	v_mfma_scale_f32_16x16x128_f8f6f4 v[134:137], v[48:55], v[90:97], v[60:63], v165, v164 op_sel_hi:[0,0,0]
	v_mfma_scale_f32_16x16x128_f8f6f4 v[138:141], v[74:81], v[90:97], v[56:59], v165, v164 op_sel_hi:[0,0,0]
	v_mfma_scale_f32_16x16x128_f8f6f4 v[146:149], v[74:81], v[114:121], v[4:7], v165, v164 op_sel_hi:[0,0,0]
	s_setprio 0
	s_barrier
	s_mov_b32 m0, s15
	s_nop 0
	buffer_load_dwordx4 v64, s[8:11], s72 offen lds
	s_nop 0
	s_mov_b32 m0, s55
	s_nop 0
	buffer_load_dwordx4 v65, s[8:11], s72 offen lds
	s_barrier
; #define G_WAIT_V(n) asm volatile("s_waitcnt vmcnt(" #n ")" ::: "memory")
; #define G_BAR() __builtin_amdgcn_s_barrier()
; #define G_SCHED() __builtin_amdgcn_sched_barrier(0)
; #define D_STAGE_A(slot, half, kt) D_STAGE(rsA, voffA, slot, half, kt)
; #define D_STAGE_B(slot, half, kt) D_STAGE(rsB, voffB, slot, half, kt)
; #define D_LDA(dst, slot) do { _Pragma("unroll") for (int m = 0; m < 4; ++m) _Pragma("unroll") for (int k = 0; k < 2; ++k) \
;     dst[m][k] = *(const LDS_AS bf16x8*)(lds + (slot) + aoff + m * 2048 + k * 1024); } while (0)
; #define D_LDB(dst, slot) do { _Pragma("unroll") for (int n = 0; n < 2; ++n) _Pragma("unroll") for (int k = 0; k < 2; ++k) \
;     dst[n][k] = *(const LDS_AS bf16x8*)(lds + (slot) + boff + n * 2048 + k * 1024); } while (0)
; #define D_WAIT_L(n) asm volatile("s_waitcnt lgkmcnt(" #n ")" ::: "memory")
; #define D_STAGE_A(slot, half, kt) D_STAGE(rsA, voffA, slot, half, kt)
; #define D_WAIT_L(n) asm volatile("s_waitcnt lgkmcnt(" #n ")" ::: "memory")
;     ...
;   for (int t = 0; t < (F8_PEEL ? nt - 2 : nt); t += 2) {
;     const int t1 = t + 1;
;     const int t2 = (F8_PEEL || t + 2 < nt) ? t + 2 : t;
;     const int t3 = (F8_PEEL || t + 2 < nt) ? t + 3 : t + 1;
;     D_LDB(B0, G_SB(0, 0)); G_SCHED(); D_LDA(At, G_SA(0, 0)); D_STAGE_A(G_SA(1, 1), 1, t1);
;     D_WAIT_L(8); G_BAR(); D_WAIT_L(0); G_SCHED(); D_MMA(0, 0, At, B0); G_BAR(); G_SCHED();
;     D_LDB(B1, G_SB(0, 1)); D_STAGE_B(G_SB(0, 0), 0, t2);
;     G_BAR(); D_WAIT_L(0); G_SCHED(); D_MMA(0, 1, At, B1); G_BAR(); G_SCHED();
;     D_LDA(At, G_SA(0, 1)); D_STAGE_A(G_SA(0, 0), 0, t2);
;     G_BAR(); D_WAIT_L(0); G_SCHED(); D_MMA(1, 0, At, B0); G_BAR(); G_SCHED();
;     D_STAGE_B(G_SB(0, 1), 1, t2);
;     G_WAIT_V(6); G_BAR(); G_SCHED(); D_MMA(1, 1, At, B1); G_BAR(); G_SCHED();
;     D_LDB(B0, G_SB(1, 0)); G_SCHED(); D_LDA(At, G_SA(1, 0)); D_STAGE_A(G_SA(0, 1), 1, t2);
;     D_WAIT_L(8); G_BAR(); D_WAIT_L(0); G_SCHED(); D_MMA(0, 0, At, B0); G_BAR(); G_SCHED();
;     D_LDB(B1, G_SB(1, 1)); D_STAGE_B(G_SB(1, 0), 0, t3);
;     G_BAR(); D_WAIT_L(0); G_SCHED(); D_MMA(0, 1, At, B1); G_BAR(); G_SCHED();
;     D_LDA(At, G_SA(1, 1)); D_STAGE_A(G_SA(1, 0), 0, t3);
;     G_BAR(); D_WAIT_L(0); G_SCHED(); D_MMA(1, 0, At, B0); G_BAR(); G_SCHED();
;     D_STAGE_B(G_SB(1, 1), 1, t3);
;     G_WAIT_V(6); G_BAR(); G_SCHED(); D_MMA(1, 1, At, B1); G_BAR(); G_SCHED();
;   }
	s_waitcnt lgkmcnt(0)
	s_barrier
	s_mov_b32 m0, s26
	s_nop 0
	buffer_load_dwordx4 v70, s[4:7], s75 offen lds
	s_nop 0
	s_mov_b32 m0, s58
	s_nop 0
	buffer_load_dwordx4 v70, s[4:7], s76 offen lds
	s_waitcnt vmcnt(10)
	s_barrier
	s_barrier
	v_add_u32_e32 v4, s77, v68
	v_add_u32_e32 v48, s77, v69
	ds_read_b128 v[0:3], v4
	ds_read_b128 v[56:59], v4 offset:2048
	ds_read_b128 v[4:7], v48
	ds_read_b128 v[60:63], v48 offset:2048
	ds_read_b128 v[74:77], v71 offset:32784
	ds_read_b128 v[82:85], v71 offset:34832
	ds_read_b128 v[78:81], v72 offset:32784
	ds_read_b128 v[86:89], v72 offset:34832
	ds_read_b128 v[90:93], v71 offset:36880
	ds_read_b128 v[98:101], v71 offset:38928
	ds_read_b128 v[94:97], v72 offset:36880
	ds_read_b128 v[102:105], v72 offset:38928
	s_mov_b32 m0, s27
	s_nop 0
	buffer_load_dwordx4 v66, s[8:11], s72 offen lds
	s_nop 0
	s_mov_b32 m0, s59
	s_nop 0
	buffer_load_dwordx4 v67, s[8:11], s72 offen lds
	s_waitcnt lgkmcnt(8)
	s_waitcnt vmcnt(10)
	s_barrier
	s_nop 0
	s_setprio 1
	s_waitcnt lgkmcnt(5)
	v_mfma_scale_f32_16x16x128_f8f6f4 v[48:51], v[0:7], v[74:81], v[122:125], v165, v164 op_sel_hi:[0,0,0]
	v_mfma_scale_f32_16x16x128_f8f6f4 v[52:55], v[56:63], v[74:81], v[126:129], v165, v164 op_sel_hi:[0,0,0]
	s_waitcnt lgkmcnt(4)
	v_mfma_scale_f32_16x16x128_f8f6f4 v[40:43], v[0:7], v[82:89], v[40:43], v165, v164 op_sel_hi:[0,0,0]
	v_mfma_scale_f32_16x16x128_f8f6f4 v[32:35], v[56:63], v[82:89], v[32:35], v165, v164 op_sel_hi:[0,0,0]
	s_waitcnt lgkmcnt(1)
	v_mfma_scale_f32_16x16x128_f8f6f4 v[24:27], v[0:7], v[90:97], v[24:27], v165, v164 op_sel_hi:[0,0,0]
	v_mfma_scale_f32_16x16x128_f8f6f4 v[16:19], v[56:63], v[90:97], v[16:19], v165, v164 op_sel_hi:[0,0,0]
	s_waitcnt lgkmcnt(0)
	v_mfma_scale_f32_16x16x128_f8f6f4 v[8:11], v[0:7], v[98:105], v[8:11], v165, v164 op_sel_hi:[0,0,0]
	v_mfma_scale_f32_16x16x128_f8f6f4 v[0:3], v[56:63], v[98:105], v[130:133], v165, v164 op_sel_hi:[0,0,0]
	s_setprio 0
	s_barrier
	v_add_u32_e32 v4, s71, v68
	v_add_u32_e32 v5, s71, v69
	ds_read_b128 v[106:109], v4
	ds_read_b128 v[114:117], v4 offset:2048
	ds_read_b128 v[110:113], v5
	ds_read_b128 v[118:121], v5 offset:2048
	s_mov_b32 m0, s39
	s_nop 0
	buffer_load_dwordx4 v70, s[4:7], s67 offen lds
	s_nop 0
	s_mov_b32 m0, s60
	s_nop 0
	buffer_load_dwordx4 v70, s[4:7], s70 offen lds
	s_waitcnt vmcnt(10)
	s_barrier
	s_nop 0
	s_setprio 1
	s_waitcnt lgkmcnt(1)
	v_mfma_scale_f32_16x16x128_f8f6f4 v[60:63], v[106:113], v[74:81], v[134:137], v165, v164 op_sel_hi:[0,0,0]
	s_waitcnt lgkmcnt(0)
	v_mfma_scale_f32_16x16x128_f8f6f4 v[56:59], v[114:121], v[74:81], v[138:141], v165, v164 op_sel_hi:[0,0,0]
	v_mfma_scale_f32_16x16x128_f8f6f4 v[44:47], v[106:113], v[82:89], v[44:47], v165, v164 op_sel_hi:[0,0,0]
	v_mfma_scale_f32_16x16x128_f8f6f4 v[36:39], v[114:121], v[82:89], v[36:39], v165, v164 op_sel_hi:[0,0,0]
	v_mfma_scale_f32_16x16x128_f8f6f4 v[28:31], v[106:113], v[90:97], v[28:31], v165, v164 op_sel_hi:[0,0,0]
	v_mfma_scale_f32_16x16x128_f8f6f4 v[20:23], v[114:121], v[90:97], v[20:23], v165, v164 op_sel_hi:[0,0,0]
	v_mfma_scale_f32_16x16x128_f8f6f4 v[12:15], v[106:113], v[98:105], v[12:15], v165, v164 op_sel_hi:[0,0,0]
	v_mfma_scale_f32_16x16x128_f8f6f4 v[4:7], v[114:121], v[98:105], v[146:149], v165, v164 op_sel_hi:[0,0,0]
	s_setprio 0
	s_barrier
	s_mov_b32 m0, s49
	s_nop 0
	buffer_load_dwordx4 v64, s[8:11], s67 offen lds
	s_nop 0
	s_mov_b32 m0, s61
	s_nop 0
	buffer_load_dwordx4 v65, s[8:11], s67 offen lds
	s_barrier
	s_waitcnt lgkmcnt(0)
	s_barrier
	s_mov_b32 m0, s50
	s_nop 0
	buffer_load_dwordx4 v70, s[4:7], s68 offen lds
	s_nop 0
	s_mov_b32 m0, s62
	s_nop 0
	buffer_load_dwordx4 v70, s[4:7], s69 offen lds
	s_waitcnt vmcnt(10)
	s_barrier
	s_barrier
	s_mov_b32 s63, s65
	s_mov_b32 s66, s64
	s_cbranch_scc0 .LBB0_1701
	s_waitcnt vmcnt(0)
	s_cmpk_lt_u32 s13, 0x100
	s_cbranch_scc0 .LBB0_1704
	s_barrier
